# non-temporal epilogue stores in the four MoE GEMM phases (outputs are only read after the next grid barrier)
# baseline (speedup 1.0000x reference)
.LBB0_887:
	s_lshl_b32 s12, s69, 7
	s_or_b32 s12, s12, s58
	v_lshl_or_b32 v0, v0, 3, s12
	v_or_b32_e32 v18, s57, v1
	v_lshl_add_u32 v1, v0, 2, 0
	v_add_u32_e32 v2, 0x21000, v1
	v_add_u32_e32 v1, 0x22000, v1
	ds_read_b128 v[4:7], v2
	ds_read_b128 v[8:11], v1
	ds_read_b128 v[12:15], v2 offset:16
	ds_read_b128 v[20:23], v1 offset:16
	v_ashrrev_i32_e32 v1, 31, v0
	v_cmp_gt_i32_e32 vcc, s67, v18
	s_waitcnt lgkmcnt(0)
	v_pk_fma_f32 v[2:3], v[8:9], 4.0, 4.0 op_sel_hi:[1,0,0]
	v_pk_fma_f32 v[8:9], v[10:11], 4.0, 4.0 op_sel_hi:[1,0,0]
	v_pk_mul_f32 v[16:17], v[14:15], s[20:21] op_sel_hi:[1,0]
	v_pk_fma_f32 v[10:11], v[20:21], 4.0, 4.0 op_sel_hi:[1,0,0]
	v_pk_fma_f32 v[14:15], v[22:23], 4.0, 4.0 op_sel_hi:[1,0,0]
	v_pk_mul_f32 v[4:5], v[4:5], s[20:21] op_sel_hi:[1,0]
	v_pk_mul_f32 v[6:7], v[6:7], s[20:21] op_sel_hi:[1,0]
	v_pk_mul_f32 v[2:3], v[2:3], s[22:23] op_sel_hi:[1,0]
	v_pk_mul_f32 v[8:9], v[8:9], s[22:23] op_sel_hi:[1,0]
	v_pk_mul_f32 v[12:13], v[12:13], s[20:21] op_sel_hi:[1,0]
	v_pk_mul_f32 v[10:11], v[10:11], s[22:23] op_sel_hi:[1,0]
	v_pk_mul_f32 v[14:15], v[14:15], s[22:23] op_sel_hi:[1,0]
	s_and_saveexec_b64 s[34:35], vcc
	s_cbranch_execz .LBB0_889
	v_pk_fma_f32 v[20:21], v[154:155], s[26:27], v[16:17] op_sel_hi:[1,0,1] neg_lo:[1,0,0] neg_hi:[1,0,0]
	v_pk_fma_f32 v[26:27], v[152:153], s[26:27], v[12:13] op_sel_hi:[1,0,1] neg_lo:[1,0,0] neg_hi:[1,0,0]
	v_max_f32_e32 v20, 0xc1898193, v20
	v_max_f32_e32 v21, 0xc1898193, v21
	v_exp_f32_e32 v22, v20
	v_exp_f32_e32 v23, v21
	v_max_f32_e32 v26, 0xc1898193, v26
	v_max_f32_e32 v27, 0xc1898193, v27
	v_exp_f32_e32 v28, v26
	v_pk_add_f32 v[22:23], v[22:23], 1.0 op_sel_hi:[1,0]
	v_exp_f32_e32 v29, v27
	v_rcp_f32_e32 v22, v22
	v_rcp_f32_e32 v23, v23
	v_pk_fma_f32 v[30:31], v[144:145], s[26:27], v[4:5] op_sel_hi:[1,0,1] neg_lo:[1,0,0] neg_hi:[1,0,0]
	v_pk_fma_f32 v[24:25], v[158:159], s[24:25], v[14:15] op_sel_hi:[1,0,1] neg_lo:[1,0,0] neg_hi:[1,0,0]
	v_max_f32_e32 v30, 0xc1898193, v30
	v_pk_mul_f32 v[20:21], v[20:21], v[22:23]
	v_pk_add_f32 v[22:23], v[28:29], 1.0 op_sel_hi:[1,0]
	v_max_f32_e32 v31, 0xc1898193, v31
	v_rcp_f32_e32 v22, v22
	v_rcp_f32_e32 v23, v23
	v_exp_f32_e32 v144, v30
	v_exp_f32_e32 v145, v31
	v_med3_f32 v24, v24, s65, v178
	v_pk_mul_f32 v[22:23], v[26:27], v[22:23]
	v_pk_fma_f32 v[26:27], v[146:147], s[26:27], v[6:7] op_sel_hi:[1,0,1] neg_lo:[1,0,0] neg_hi:[1,0,0]
	v_pk_add_f32 v[144:145], v[144:145], 1.0 op_sel_hi:[1,0]
	v_max_f32_e32 v26, 0xc1898193, v26
	v_max_f32_e32 v27, 0xc1898193, v27
	v_exp_f32_e32 v28, v26
	v_exp_f32_e32 v29, v27
	v_rcp_f32_e32 v144, v144
	v_rcp_f32_e32 v145, v145
	v_med3_f32 v25, v25, s65, v178
	v_pk_mul_f32 v[20:21], v[24:25], v[20:21]
	v_pk_fma_f32 v[24:25], v[156:157], s[24:25], v[10:11] op_sel_hi:[1,0,1] neg_lo:[1,0,0] neg_hi:[1,0,0]
	v_pk_add_f32 v[28:29], v[28:29], 1.0 op_sel_hi:[1,0]
	v_med3_f32 v24, v24, s65, v178
	v_med3_f32 v25, v25, s65, v178
	v_pk_fma_f32 v[146:147], v[148:149], s[24:25], v[2:3] op_sel_hi:[1,0,1] neg_lo:[1,0,0] neg_hi:[1,0,0]
	v_pk_mul_f32 v[22:23], v[24:25], v[22:23]
	v_rcp_f32_e32 v28, v28
	v_rcp_f32_e32 v29, v29
	v_med3_f32 v146, v146, s65, v178
	v_med3_f32 v147, v147, s65, v178
	v_pk_mul_f32 v[30:31], v[30:31], v[144:145]
	v_mov_b32_e32 v145, v161
	v_pk_mul_f32 v[30:31], v[146:147], v[30:31]
	v_mov_b32_e32 v144, v161
	v_cvt_pk_fp8_f32 v145, v22, v23
	v_cvt_pk_fp8_f32 v144, v30, v31
	v_pk_fma_f32 v[24:25], v[150:151], s[24:25], v[8:9] op_sel_hi:[1,0,1] neg_lo:[1,0,0] neg_hi:[1,0,0]
	v_pk_mul_f32 v[22:23], v[26:27], v[28:29]
	v_med3_f32 v24, v24, s65, v178
	v_med3_f32 v25, v25, s65, v178
	v_pk_mul_f32 v[22:23], v[24:25], v[22:23]
	v_cvt_pk_fp8_f32 v145, v20, v21 op_sel:[0,0,1]
	v_add_u32_e32 v20, s66, v18
	v_cvt_pk_fp8_f32 v144, v22, v23 op_sel:[0,0,1]
	v_ashrrev_i32_e32 v21, 31, v20
	v_lshlrev_b64 v[20:21], 10, v[20:21]
	v_lshl_add_u64 v[20:21], s[14:15], 0, v[20:21]
	v_lshl_add_u64 v[20:21], v[20:21], 0, v[0:1]
	global_store_dwordx2 v[20:21], v[144:145], off nt
.LBB0_889:
	s_or_b64 exec, exec, s[34:35]
	v_or_b32_e32 v19, 16, v18
	v_cmp_gt_i32_e32 vcc, s67, v19
	s_and_saveexec_b64 s[34:35], vcc
	s_cbranch_execz .LBB0_891
	v_pk_fma_f32 v[20:21], v[138:139], s[26:27], v[16:17] op_sel_hi:[1,0,1] neg_lo:[1,0,0] neg_hi:[1,0,0]
	v_pk_fma_f32 v[26:27], v[136:137], s[26:27], v[12:13] op_sel_hi:[1,0,1] neg_lo:[1,0,0] neg_hi:[1,0,0]
	v_max_f32_e32 v20, 0xc1898193, v20
	v_max_f32_e32 v21, 0xc1898193, v21
	v_exp_f32_e32 v22, v20
	v_exp_f32_e32 v23, v21
	v_max_f32_e32 v26, 0xc1898193, v26
	v_max_f32_e32 v27, 0xc1898193, v27
	v_exp_f32_e32 v28, v26
	v_pk_add_f32 v[22:23], v[22:23], 1.0 op_sel_hi:[1,0]
	v_exp_f32_e32 v29, v27
	v_rcp_f32_e32 v22, v22
	v_rcp_f32_e32 v23, v23
	v_pk_fma_f32 v[30:31], v[128:129], s[26:27], v[4:5] op_sel_hi:[1,0,1] neg_lo:[1,0,0] neg_hi:[1,0,0]
	v_pk_fma_f32 v[24:25], v[142:143], s[24:25], v[14:15] op_sel_hi:[1,0,1] neg_lo:[1,0,0] neg_hi:[1,0,0]
	v_max_f32_e32 v30, 0xc1898193, v30
	v_pk_mul_f32 v[20:21], v[20:21], v[22:23]
	v_pk_add_f32 v[22:23], v[28:29], 1.0 op_sel_hi:[1,0]
	v_max_f32_e32 v31, 0xc1898193, v31
	v_rcp_f32_e32 v22, v22
	v_rcp_f32_e32 v23, v23
	v_exp_f32_e32 v128, v30
	v_exp_f32_e32 v129, v31
	v_med3_f32 v24, v24, s65, v178
	v_pk_mul_f32 v[22:23], v[26:27], v[22:23]
	v_pk_fma_f32 v[26:27], v[130:131], s[26:27], v[6:7] op_sel_hi:[1,0,1] neg_lo:[1,0,0] neg_hi:[1,0,0]
	v_pk_add_f32 v[128:129], v[128:129], 1.0 op_sel_hi:[1,0]
	v_max_f32_e32 v26, 0xc1898193, v26
	v_max_f32_e32 v27, 0xc1898193, v27
	v_exp_f32_e32 v28, v26
	v_exp_f32_e32 v29, v27
	v_rcp_f32_e32 v128, v128
	v_rcp_f32_e32 v129, v129
	v_med3_f32 v25, v25, s65, v178
	v_pk_mul_f32 v[20:21], v[24:25], v[20:21]
	v_pk_fma_f32 v[24:25], v[140:141], s[24:25], v[10:11] op_sel_hi:[1,0,1] neg_lo:[1,0,0] neg_hi:[1,0,0]
	v_pk_add_f32 v[28:29], v[28:29], 1.0 op_sel_hi:[1,0]
	v_med3_f32 v24, v24, s65, v178
	v_med3_f32 v25, v25, s65, v178
	v_pk_fma_f32 v[130:131], v[132:133], s[24:25], v[2:3] op_sel_hi:[1,0,1] neg_lo:[1,0,0] neg_hi:[1,0,0]
	v_pk_mul_f32 v[22:23], v[24:25], v[22:23]
	v_rcp_f32_e32 v28, v28
	v_rcp_f32_e32 v29, v29
	v_med3_f32 v130, v130, s65, v178
	v_med3_f32 v131, v131, s65, v178
	v_pk_mul_f32 v[30:31], v[30:31], v[128:129]
	v_mov_b32_e32 v129, v161
	v_pk_mul_f32 v[30:31], v[130:131], v[30:31]
	v_mov_b32_e32 v128, v161
	v_cvt_pk_fp8_f32 v129, v22, v23
	v_cvt_pk_fp8_f32 v128, v30, v31
	v_pk_fma_f32 v[24:25], v[134:135], s[24:25], v[8:9] op_sel_hi:[1,0,1] neg_lo:[1,0,0] neg_hi:[1,0,0]
	v_pk_mul_f32 v[22:23], v[26:27], v[28:29]
	v_med3_f32 v24, v24, s65, v178
	v_med3_f32 v25, v25, s65, v178
	v_pk_mul_f32 v[22:23], v[24:25], v[22:23]
	v_cvt_pk_fp8_f32 v129, v20, v21 op_sel:[0,0,1]
	v_add_u32_e32 v20, s66, v19
	v_cvt_pk_fp8_f32 v128, v22, v23 op_sel:[0,0,1]
	v_ashrrev_i32_e32 v21, 31, v20
	v_lshlrev_b64 v[20:21], 10, v[20:21]
	v_lshl_add_u64 v[20:21], s[14:15], 0, v[20:21]
	v_lshl_add_u64 v[20:21], v[20:21], 0, v[0:1]
	global_store_dwordx2 v[20:21], v[128:129], off nt
.LBB0_891:
	s_or_b64 exec, exec, s[34:35]
	v_or_b32_e32 v19, 32, v18
	v_cmp_gt_i32_e32 vcc, s67, v19
	s_and_saveexec_b64 s[34:35], vcc
	s_cbranch_execz .LBB0_893
	v_pk_fma_f32 v[20:21], v[122:123], s[26:27], v[16:17] op_sel_hi:[1,0,1] neg_lo:[1,0,0] neg_hi:[1,0,0]
	v_pk_fma_f32 v[26:27], v[120:121], s[26:27], v[12:13] op_sel_hi:[1,0,1] neg_lo:[1,0,0] neg_hi:[1,0,0]
	v_max_f32_e32 v20, 0xc1898193, v20
	v_max_f32_e32 v21, 0xc1898193, v21
	v_exp_f32_e32 v22, v20
	v_exp_f32_e32 v23, v21
	v_max_f32_e32 v26, 0xc1898193, v26
	v_max_f32_e32 v27, 0xc1898193, v27
	v_exp_f32_e32 v28, v26
	v_pk_add_f32 v[22:23], v[22:23], 1.0 op_sel_hi:[1,0]
	v_exp_f32_e32 v29, v27
	v_rcp_f32_e32 v22, v22
	v_rcp_f32_e32 v23, v23
	v_pk_fma_f32 v[30:31], v[112:113], s[26:27], v[4:5] op_sel_hi:[1,0,1] neg_lo:[1,0,0] neg_hi:[1,0,0]
	v_pk_fma_f32 v[24:25], v[126:127], s[24:25], v[14:15] op_sel_hi:[1,0,1] neg_lo:[1,0,0] neg_hi:[1,0,0]
	v_max_f32_e32 v30, 0xc1898193, v30
	v_pk_mul_f32 v[20:21], v[20:21], v[22:23]
	v_pk_add_f32 v[22:23], v[28:29], 1.0 op_sel_hi:[1,0]
	v_max_f32_e32 v31, 0xc1898193, v31
	v_rcp_f32_e32 v22, v22
	v_rcp_f32_e32 v23, v23
	v_exp_f32_e32 v112, v30
	v_exp_f32_e32 v113, v31
	v_med3_f32 v24, v24, s65, v178
	v_pk_mul_f32 v[22:23], v[26:27], v[22:23]
	v_pk_fma_f32 v[26:27], v[114:115], s[26:27], v[6:7] op_sel_hi:[1,0,1] neg_lo:[1,0,0] neg_hi:[1,0,0]
	v_pk_add_f32 v[112:113], v[112:113], 1.0 op_sel_hi:[1,0]
	v_max_f32_e32 v26, 0xc1898193, v26
	v_max_f32_e32 v27, 0xc1898193, v27
	v_exp_f32_e32 v28, v26
	v_exp_f32_e32 v29, v27
	v_rcp_f32_e32 v112, v112
	v_rcp_f32_e32 v113, v113
	v_med3_f32 v25, v25, s65, v178
	v_pk_mul_f32 v[20:21], v[24:25], v[20:21]
	v_pk_fma_f32 v[24:25], v[124:125], s[24:25], v[10:11] op_sel_hi:[1,0,1] neg_lo:[1,0,0] neg_hi:[1,0,0]
	v_pk_add_f32 v[28:29], v[28:29], 1.0 op_sel_hi:[1,0]
	v_med3_f32 v24, v24, s65, v178
	v_med3_f32 v25, v25, s65, v178
	v_pk_fma_f32 v[114:115], v[116:117], s[24:25], v[2:3] op_sel_hi:[1,0,1] neg_lo:[1,0,0] neg_hi:[1,0,0]
	v_pk_mul_f32 v[22:23], v[24:25], v[22:23]
	v_rcp_f32_e32 v28, v28
	v_rcp_f32_e32 v29, v29
	v_med3_f32 v114, v114, s65, v178
	v_med3_f32 v115, v115, s65, v178
	v_pk_mul_f32 v[30:31], v[30:31], v[112:113]
	v_mov_b32_e32 v113, v161
	v_pk_mul_f32 v[30:31], v[114:115], v[30:31]
	v_mov_b32_e32 v112, v161
	v_cvt_pk_fp8_f32 v113, v22, v23
	v_cvt_pk_fp8_f32 v112, v30, v31
	v_pk_fma_f32 v[24:25], v[118:119], s[24:25], v[8:9] op_sel_hi:[1,0,1] neg_lo:[1,0,0] neg_hi:[1,0,0]
	v_pk_mul_f32 v[22:23], v[26:27], v[28:29]
	v_med3_f32 v24, v24, s65, v178
	v_med3_f32 v25, v25, s65, v178
	v_pk_mul_f32 v[22:23], v[24:25], v[22:23]
	v_cvt_pk_fp8_f32 v113, v20, v21 op_sel:[0,0,1]
	v_add_u32_e32 v20, s66, v19
	v_cvt_pk_fp8_f32 v112, v22, v23 op_sel:[0,0,1]
	v_ashrrev_i32_e32 v21, 31, v20
	v_lshlrev_b64 v[20:21], 10, v[20:21]
	v_lshl_add_u64 v[20:21], s[14:15], 0, v[20:21]
	v_lshl_add_u64 v[20:21], v[20:21], 0, v[0:1]
	global_store_dwordx2 v[20:21], v[112:113], off nt
.LBB0_893:
	s_or_b64 exec, exec, s[34:35]
	v_or_b32_e32 v19, 48, v18
	v_cmp_gt_i32_e32 vcc, s67, v19
	s_and_saveexec_b64 s[34:35], vcc
	s_cbranch_execz .LBB0_895
	v_pk_fma_f32 v[20:21], v[106:107], s[26:27], v[16:17] op_sel_hi:[1,0,1] neg_lo:[1,0,0] neg_hi:[1,0,0]
	v_pk_fma_f32 v[26:27], v[104:105], s[26:27], v[12:13] op_sel_hi:[1,0,1] neg_lo:[1,0,0] neg_hi:[1,0,0]
	v_max_f32_e32 v20, 0xc1898193, v20
	v_max_f32_e32 v21, 0xc1898193, v21
	v_exp_f32_e32 v22, v20
	v_exp_f32_e32 v23, v21
	v_max_f32_e32 v26, 0xc1898193, v26
	v_max_f32_e32 v27, 0xc1898193, v27
	v_exp_f32_e32 v28, v26
	v_pk_add_f32 v[22:23], v[22:23], 1.0 op_sel_hi:[1,0]
	v_exp_f32_e32 v29, v27
	v_rcp_f32_e32 v22, v22
	v_rcp_f32_e32 v23, v23
	v_pk_fma_f32 v[30:31], v[88:89], s[26:27], v[4:5] op_sel_hi:[1,0,1] neg_lo:[1,0,0] neg_hi:[1,0,0]
	v_pk_fma_f32 v[24:25], v[110:111], s[24:25], v[14:15] op_sel_hi:[1,0,1] neg_lo:[1,0,0] neg_hi:[1,0,0]
	v_max_f32_e32 v30, 0xc1898193, v30
	v_pk_mul_f32 v[20:21], v[20:21], v[22:23]
	v_pk_add_f32 v[22:23], v[28:29], 1.0 op_sel_hi:[1,0]
	v_max_f32_e32 v31, 0xc1898193, v31
	v_rcp_f32_e32 v22, v22
	v_rcp_f32_e32 v23, v23
	v_exp_f32_e32 v88, v30
	v_exp_f32_e32 v89, v31
	v_med3_f32 v24, v24, s65, v178
	v_pk_mul_f32 v[22:23], v[26:27], v[22:23]
	v_pk_fma_f32 v[26:27], v[90:91], s[26:27], v[6:7] op_sel_hi:[1,0,1] neg_lo:[1,0,0] neg_hi:[1,0,0]
	v_pk_add_f32 v[88:89], v[88:89], 1.0 op_sel_hi:[1,0]
	v_max_f32_e32 v26, 0xc1898193, v26
	v_max_f32_e32 v27, 0xc1898193, v27
	v_exp_f32_e32 v28, v26
	v_exp_f32_e32 v29, v27
	v_rcp_f32_e32 v88, v88
	v_rcp_f32_e32 v89, v89
	v_med3_f32 v25, v25, s65, v178
	v_pk_mul_f32 v[20:21], v[24:25], v[20:21]
	v_pk_fma_f32 v[24:25], v[108:109], s[24:25], v[10:11] op_sel_hi:[1,0,1] neg_lo:[1,0,0] neg_hi:[1,0,0]
	v_pk_add_f32 v[28:29], v[28:29], 1.0 op_sel_hi:[1,0]
	v_med3_f32 v24, v24, s65, v178
	v_med3_f32 v25, v25, s65, v178
	v_pk_fma_f32 v[90:91], v[96:97], s[24:25], v[2:3] op_sel_hi:[1,0,1] neg_lo:[1,0,0] neg_hi:[1,0,0]
	v_pk_mul_f32 v[22:23], v[24:25], v[22:23]
	v_rcp_f32_e32 v28, v28
	v_rcp_f32_e32 v29, v29
	v_med3_f32 v90, v90, s65, v178
	v_med3_f32 v91, v91, s65, v178
	v_pk_mul_f32 v[30:31], v[30:31], v[88:89]
	v_mov_b32_e32 v89, v161
	v_pk_mul_f32 v[30:31], v[90:91], v[30:31]
	v_mov_b32_e32 v88, v161
	v_cvt_pk_fp8_f32 v89, v22, v23
	v_cvt_pk_fp8_f32 v88, v30, v31
	v_pk_fma_f32 v[24:25], v[98:99], s[24:25], v[8:9] op_sel_hi:[1,0,1] neg_lo:[1,0,0] neg_hi:[1,0,0]
	v_pk_mul_f32 v[22:23], v[26:27], v[28:29]
	v_med3_f32 v24, v24, s65, v178
	v_med3_f32 v25, v25, s65, v178
	v_pk_mul_f32 v[22:23], v[24:25], v[22:23]
	v_cvt_pk_fp8_f32 v89, v20, v21 op_sel:[0,0,1]
	v_add_u32_e32 v20, s66, v19
	v_cvt_pk_fp8_f32 v88, v22, v23 op_sel:[0,0,1]
	v_ashrrev_i32_e32 v21, 31, v20
	v_lshlrev_b64 v[20:21], 10, v[20:21]
	v_lshl_add_u64 v[20:21], s[14:15], 0, v[20:21]
	v_lshl_add_u64 v[20:21], v[20:21], 0, v[0:1]
	global_store_dwordx2 v[20:21], v[88:89], off nt
.LBB0_895:
	s_or_b64 exec, exec, s[34:35]
	v_add_u32_e32 v19, 0x80, v18
	v_cmp_gt_i32_e32 vcc, s67, v19
	s_and_saveexec_b64 s[34:35], vcc
	s_cbranch_execz .LBB0_897
	v_pk_fma_f32 v[20:21], v[94:95], s[26:27], v[16:17] op_sel_hi:[1,0,1] neg_lo:[1,0,0] neg_hi:[1,0,0]
	v_pk_fma_f32 v[26:27], v[92:93], s[26:27], v[12:13] op_sel_hi:[1,0,1] neg_lo:[1,0,0] neg_hi:[1,0,0]
	v_max_f32_e32 v20, 0xc1898193, v20
	v_max_f32_e32 v21, 0xc1898193, v21
	v_exp_f32_e32 v22, v20
	v_exp_f32_e32 v23, v21
	v_max_f32_e32 v26, 0xc1898193, v26
	v_max_f32_e32 v27, 0xc1898193, v27
	v_exp_f32_e32 v28, v26
	v_pk_add_f32 v[22:23], v[22:23], 1.0 op_sel_hi:[1,0]
	v_exp_f32_e32 v29, v27
	v_rcp_f32_e32 v22, v22
	v_rcp_f32_e32 v23, v23
	v_pk_fma_f32 v[30:31], v[80:81], s[26:27], v[4:5] op_sel_hi:[1,0,1] neg_lo:[1,0,0] neg_hi:[1,0,0]
	v_pk_fma_f32 v[24:25], v[102:103], s[24:25], v[14:15] op_sel_hi:[1,0,1] neg_lo:[1,0,0] neg_hi:[1,0,0]
	v_max_f32_e32 v30, 0xc1898193, v30
	v_pk_mul_f32 v[20:21], v[20:21], v[22:23]
	v_pk_add_f32 v[22:23], v[28:29], 1.0 op_sel_hi:[1,0]
	v_max_f32_e32 v31, 0xc1898193, v31
	v_rcp_f32_e32 v22, v22
	v_rcp_f32_e32 v23, v23
	v_exp_f32_e32 v80, v30
	v_exp_f32_e32 v81, v31
	v_med3_f32 v24, v24, s65, v178
	v_pk_mul_f32 v[22:23], v[26:27], v[22:23]
	v_pk_fma_f32 v[26:27], v[82:83], s[26:27], v[6:7] op_sel_hi:[1,0,1] neg_lo:[1,0,0] neg_hi:[1,0,0]
	v_pk_add_f32 v[80:81], v[80:81], 1.0 op_sel_hi:[1,0]
	v_max_f32_e32 v26, 0xc1898193, v26
	v_max_f32_e32 v27, 0xc1898193, v27
	v_exp_f32_e32 v28, v26
	v_exp_f32_e32 v29, v27
	v_rcp_f32_e32 v80, v80
	v_rcp_f32_e32 v81, v81
	v_med3_f32 v25, v25, s65, v178
	v_pk_mul_f32 v[20:21], v[24:25], v[20:21]
	v_pk_fma_f32 v[24:25], v[100:101], s[24:25], v[10:11] op_sel_hi:[1,0,1] neg_lo:[1,0,0] neg_hi:[1,0,0]
	v_pk_add_f32 v[28:29], v[28:29], 1.0 op_sel_hi:[1,0]
	v_med3_f32 v24, v24, s65, v178
	v_med3_f32 v25, v25, s65, v178
	v_pk_fma_f32 v[82:83], v[84:85], s[24:25], v[2:3] op_sel_hi:[1,0,1] neg_lo:[1,0,0] neg_hi:[1,0,0]
	v_pk_mul_f32 v[22:23], v[24:25], v[22:23]
	v_rcp_f32_e32 v28, v28
	v_rcp_f32_e32 v29, v29
	v_med3_f32 v82, v82, s65, v178
	v_med3_f32 v83, v83, s65, v178
	v_pk_mul_f32 v[30:31], v[30:31], v[80:81]
	v_mov_b32_e32 v81, v161
	v_pk_mul_f32 v[30:31], v[82:83], v[30:31]
	v_mov_b32_e32 v80, v161
	v_cvt_pk_fp8_f32 v81, v22, v23
	v_cvt_pk_fp8_f32 v80, v30, v31
	v_pk_fma_f32 v[24:25], v[86:87], s[24:25], v[8:9] op_sel_hi:[1,0,1] neg_lo:[1,0,0] neg_hi:[1,0,0]
	v_pk_mul_f32 v[22:23], v[26:27], v[28:29]
	v_med3_f32 v24, v24, s65, v178
	v_med3_f32 v25, v25, s65, v178
	v_pk_mul_f32 v[22:23], v[24:25], v[22:23]
	v_cvt_pk_fp8_f32 v81, v20, v21 op_sel:[0,0,1]
	v_add_u32_e32 v20, s66, v19
	v_cvt_pk_fp8_f32 v80, v22, v23 op_sel:[0,0,1]
	v_ashrrev_i32_e32 v21, 31, v20
	v_lshlrev_b64 v[20:21], 10, v[20:21]
	v_lshl_add_u64 v[20:21], s[14:15], 0, v[20:21]
	v_lshl_add_u64 v[20:21], v[20:21], 0, v[0:1]
	global_store_dwordx2 v[20:21], v[80:81], off nt
.LBB0_897:
	s_or_b64 exec, exec, s[34:35]
	v_add_u32_e32 v19, 0x90, v18
	v_cmp_gt_i32_e32 vcc, s67, v19
	s_and_saveexec_b64 s[34:35], vcc
	s_cbranch_execz .LBB0_899
	v_pk_fma_f32 v[20:21], v[74:75], s[26:27], v[16:17] op_sel_hi:[1,0,1] neg_lo:[1,0,0] neg_hi:[1,0,0]
	v_pk_fma_f32 v[26:27], v[72:73], s[26:27], v[12:13] op_sel_hi:[1,0,1] neg_lo:[1,0,0] neg_hi:[1,0,0]
	v_max_f32_e32 v20, 0xc1898193, v20
	v_max_f32_e32 v21, 0xc1898193, v21
	v_exp_f32_e32 v22, v20
	v_exp_f32_e32 v23, v21
	v_max_f32_e32 v26, 0xc1898193, v26
	v_max_f32_e32 v27, 0xc1898193, v27
	v_exp_f32_e32 v28, v26
	v_pk_add_f32 v[22:23], v[22:23], 1.0 op_sel_hi:[1,0]
	v_exp_f32_e32 v29, v27
	v_rcp_f32_e32 v22, v22
	v_rcp_f32_e32 v23, v23
	v_pk_fma_f32 v[30:31], v[64:65], s[26:27], v[4:5] op_sel_hi:[1,0,1] neg_lo:[1,0,0] neg_hi:[1,0,0]
	v_pk_fma_f32 v[24:25], v[78:79], s[24:25], v[14:15] op_sel_hi:[1,0,1] neg_lo:[1,0,0] neg_hi:[1,0,0]
	v_max_f32_e32 v30, 0xc1898193, v30
	v_pk_mul_f32 v[20:21], v[20:21], v[22:23]
	v_pk_add_f32 v[22:23], v[28:29], 1.0 op_sel_hi:[1,0]
	v_max_f32_e32 v31, 0xc1898193, v31
	v_rcp_f32_e32 v22, v22
	v_rcp_f32_e32 v23, v23
	v_exp_f32_e32 v64, v30
	v_exp_f32_e32 v65, v31
	v_med3_f32 v24, v24, s65, v178
	v_pk_mul_f32 v[22:23], v[26:27], v[22:23]
	v_pk_fma_f32 v[26:27], v[66:67], s[26:27], v[6:7] op_sel_hi:[1,0,1] neg_lo:[1,0,0] neg_hi:[1,0,0]
	v_pk_add_f32 v[64:65], v[64:65], 1.0 op_sel_hi:[1,0]
	v_max_f32_e32 v26, 0xc1898193, v26
	v_max_f32_e32 v27, 0xc1898193, v27
	v_exp_f32_e32 v28, v26
	v_exp_f32_e32 v29, v27
	v_rcp_f32_e32 v64, v64
	v_rcp_f32_e32 v65, v65
	v_med3_f32 v25, v25, s65, v178
	v_pk_mul_f32 v[20:21], v[24:25], v[20:21]
	v_pk_fma_f32 v[24:25], v[76:77], s[24:25], v[10:11] op_sel_hi:[1,0,1] neg_lo:[1,0,0] neg_hi:[1,0,0]
	v_pk_add_f32 v[28:29], v[28:29], 1.0 op_sel_hi:[1,0]
	v_med3_f32 v24, v24, s65, v178
	v_med3_f32 v25, v25, s65, v178
	v_pk_fma_f32 v[66:67], v[68:69], s[24:25], v[2:3] op_sel_hi:[1,0,1] neg_lo:[1,0,0] neg_hi:[1,0,0]
	v_pk_mul_f32 v[22:23], v[24:25], v[22:23]
	v_rcp_f32_e32 v28, v28
	v_rcp_f32_e32 v29, v29
	v_med3_f32 v66, v66, s65, v178
	v_med3_f32 v67, v67, s65, v178
	v_pk_mul_f32 v[30:31], v[30:31], v[64:65]
	v_mov_b32_e32 v65, v161
	v_pk_mul_f32 v[30:31], v[66:67], v[30:31]
	v_mov_b32_e32 v64, v161
	v_cvt_pk_fp8_f32 v65, v22, v23
	v_cvt_pk_fp8_f32 v64, v30, v31
	v_pk_fma_f32 v[24:25], v[70:71], s[24:25], v[8:9] op_sel_hi:[1,0,1] neg_lo:[1,0,0] neg_hi:[1,0,0]
	v_pk_mul_f32 v[22:23], v[26:27], v[28:29]
	v_med3_f32 v24, v24, s65, v178
	v_med3_f32 v25, v25, s65, v178
	v_pk_mul_f32 v[22:23], v[24:25], v[22:23]
	v_cvt_pk_fp8_f32 v65, v20, v21 op_sel:[0,0,1]
	v_add_u32_e32 v20, s66, v19
	v_cvt_pk_fp8_f32 v64, v22, v23 op_sel:[0,0,1]
	v_ashrrev_i32_e32 v21, 31, v20
	v_lshlrev_b64 v[20:21], 10, v[20:21]
	v_lshl_add_u64 v[20:21], s[14:15], 0, v[20:21]
	v_lshl_add_u64 v[20:21], v[20:21], 0, v[0:1]
	global_store_dwordx2 v[20:21], v[64:65], off nt
.LBB0_899:
	s_or_b64 exec, exec, s[34:35]
	v_add_u32_e32 v19, 0xa0, v18
	v_cmp_gt_i32_e32 vcc, s67, v19
	s_and_saveexec_b64 s[34:35], vcc
	s_cbranch_execz .LBB0_901
	v_pk_fma_f32 v[20:21], v[58:59], s[26:27], v[16:17] op_sel_hi:[1,0,1] neg_lo:[1,0,0] neg_hi:[1,0,0]
	v_pk_fma_f32 v[26:27], v[56:57], s[26:27], v[12:13] op_sel_hi:[1,0,1] neg_lo:[1,0,0] neg_hi:[1,0,0]
	v_max_f32_e32 v20, 0xc1898193, v20
	v_max_f32_e32 v21, 0xc1898193, v21
	v_exp_f32_e32 v22, v20
	v_exp_f32_e32 v23, v21
	v_max_f32_e32 v26, 0xc1898193, v26
	v_max_f32_e32 v27, 0xc1898193, v27
	v_exp_f32_e32 v28, v26
	v_pk_add_f32 v[22:23], v[22:23], 1.0 op_sel_hi:[1,0]
	v_exp_f32_e32 v29, v27
	v_rcp_f32_e32 v22, v22
	v_rcp_f32_e32 v23, v23
	v_pk_fma_f32 v[30:31], v[48:49], s[26:27], v[4:5] op_sel_hi:[1,0,1] neg_lo:[1,0,0] neg_hi:[1,0,0]
	v_pk_fma_f32 v[24:25], v[62:63], s[24:25], v[14:15] op_sel_hi:[1,0,1] neg_lo:[1,0,0] neg_hi:[1,0,0]
	v_max_f32_e32 v30, 0xc1898193, v30
	v_pk_mul_f32 v[20:21], v[20:21], v[22:23]
	v_pk_add_f32 v[22:23], v[28:29], 1.0 op_sel_hi:[1,0]
	v_max_f32_e32 v31, 0xc1898193, v31
	v_rcp_f32_e32 v22, v22
	v_rcp_f32_e32 v23, v23
	v_exp_f32_e32 v48, v30
	v_exp_f32_e32 v49, v31
	v_med3_f32 v24, v24, s65, v178
	v_pk_mul_f32 v[22:23], v[26:27], v[22:23]
	v_pk_fma_f32 v[26:27], v[50:51], s[26:27], v[6:7] op_sel_hi:[1,0,1] neg_lo:[1,0,0] neg_hi:[1,0,0]
	v_pk_add_f32 v[48:49], v[48:49], 1.0 op_sel_hi:[1,0]
	v_max_f32_e32 v26, 0xc1898193, v26
	v_max_f32_e32 v27, 0xc1898193, v27
	v_exp_f32_e32 v28, v26
	v_exp_f32_e32 v29, v27
	v_rcp_f32_e32 v48, v48
	v_rcp_f32_e32 v49, v49
	v_med3_f32 v25, v25, s65, v178
	v_pk_mul_f32 v[20:21], v[24:25], v[20:21]
	v_pk_fma_f32 v[24:25], v[60:61], s[24:25], v[10:11] op_sel_hi:[1,0,1] neg_lo:[1,0,0] neg_hi:[1,0,0]
	v_pk_add_f32 v[28:29], v[28:29], 1.0 op_sel_hi:[1,0]
	v_med3_f32 v24, v24, s65, v178
	v_med3_f32 v25, v25, s65, v178
	v_pk_fma_f32 v[50:51], v[52:53], s[24:25], v[2:3] op_sel_hi:[1,0,1] neg_lo:[1,0,0] neg_hi:[1,0,0]
	v_pk_mul_f32 v[22:23], v[24:25], v[22:23]
	v_rcp_f32_e32 v28, v28
	v_rcp_f32_e32 v29, v29
	v_med3_f32 v50, v50, s65, v178
	v_med3_f32 v51, v51, s65, v178
	v_pk_mul_f32 v[30:31], v[30:31], v[48:49]
	v_mov_b32_e32 v49, v161
	v_pk_mul_f32 v[30:31], v[50:51], v[30:31]
	v_mov_b32_e32 v48, v161
	v_cvt_pk_fp8_f32 v49, v22, v23
	v_cvt_pk_fp8_f32 v48, v30, v31
	v_pk_fma_f32 v[24:25], v[54:55], s[24:25], v[8:9] op_sel_hi:[1,0,1] neg_lo:[1,0,0] neg_hi:[1,0,0]
	v_pk_mul_f32 v[22:23], v[26:27], v[28:29]
	v_med3_f32 v24, v24, s65, v178
	v_med3_f32 v25, v25, s65, v178
	v_pk_mul_f32 v[22:23], v[24:25], v[22:23]
	v_cvt_pk_fp8_f32 v49, v20, v21 op_sel:[0,0,1]
	v_add_u32_e32 v20, s66, v19
	v_cvt_pk_fp8_f32 v48, v22, v23 op_sel:[0,0,1]
	v_ashrrev_i32_e32 v21, 31, v20
	v_lshlrev_b64 v[20:21], 10, v[20:21]
	v_lshl_add_u64 v[20:21], s[14:15], 0, v[20:21]
	v_lshl_add_u64 v[20:21], v[20:21], 0, v[0:1]
	global_store_dwordx2 v[20:21], v[48:49], off nt
.LBB0_901:
	s_or_b64 exec, exec, s[34:35]
	v_add_u32_e32 v18, 0xb0, v18
	v_cmp_gt_i32_e32 vcc, s67, v18
	s_and_saveexec_b64 s[34:35], vcc
	s_cbranch_execz .LBB0_903
	v_pk_fma_f32 v[16:17], v[46:47], s[26:27], v[16:17] op_sel_hi:[1,0,1] neg_lo:[1,0,0] neg_hi:[1,0,0]
	v_pk_fma_f32 v[12:13], v[44:45], s[26:27], v[12:13] op_sel_hi:[1,0,1] neg_lo:[1,0,0] neg_hi:[1,0,0]
	v_max_f32_e32 v16, 0xc1898193, v16
	v_max_f32_e32 v17, 0xc1898193, v17
	v_exp_f32_e32 v20, v16
	v_exp_f32_e32 v21, v17
	v_max_f32_e32 v12, 0xc1898193, v12
	v_max_f32_e32 v13, 0xc1898193, v13
	v_exp_f32_e32 v22, v12
	v_pk_add_f32 v[20:21], v[20:21], 1.0 op_sel_hi:[1,0]
	v_exp_f32_e32 v23, v13
	v_rcp_f32_e32 v20, v20
	v_rcp_f32_e32 v21, v21
	v_pk_fma_f32 v[14:15], v[42:43], s[24:25], v[14:15] op_sel_hi:[1,0,1] neg_lo:[1,0,0] neg_hi:[1,0,0]
	v_pk_fma_f32 v[4:5], v[36:37], s[26:27], v[4:5] op_sel_hi:[1,0,1] neg_lo:[1,0,0] neg_hi:[1,0,0]
	v_med3_f32 v14, v14, s65, v178
	v_med3_f32 v15, v15, s65, v178
	v_pk_mul_f32 v[16:17], v[16:17], v[20:21]
	v_max_f32_e32 v4, 0xc1898193, v4
	v_pk_mul_f32 v[14:15], v[14:15], v[16:17]
	v_pk_add_f32 v[16:17], v[22:23], 1.0 op_sel_hi:[1,0]
	v_max_f32_e32 v5, 0xc1898193, v5
	v_rcp_f32_e32 v16, v16
	v_rcp_f32_e32 v17, v17
	v_pk_fma_f32 v[10:11], v[40:41], s[24:25], v[10:11] op_sel_hi:[1,0,1] neg_lo:[1,0,0] neg_hi:[1,0,0]
	v_pk_fma_f32 v[6:7], v[38:39], s[26:27], v[6:7] op_sel_hi:[1,0,1] neg_lo:[1,0,0] neg_hi:[1,0,0]
	v_med3_f32 v10, v10, s65, v178
	v_pk_mul_f32 v[12:13], v[12:13], v[16:17]
	v_exp_f32_e32 v16, v4
	v_exp_f32_e32 v17, v5
	v_med3_f32 v11, v11, s65, v178
	v_max_f32_e32 v6, 0xc1898193, v6
	v_max_f32_e32 v7, 0xc1898193, v7
	v_pk_mul_f32 v[10:11], v[10:11], v[12:13]
	v_exp_f32_e32 v12, v6
	v_exp_f32_e32 v13, v7
	v_pk_add_f32 v[16:17], v[16:17], 1.0 op_sel_hi:[1,0]
	v_pk_fma_f32 v[2:3], v[32:33], s[24:25], v[2:3] op_sel_hi:[1,0,1] neg_lo:[1,0,0] neg_hi:[1,0,0]
	v_rcp_f32_e32 v16, v16
	v_rcp_f32_e32 v17, v17
	v_pk_add_f32 v[12:13], v[12:13], 1.0 op_sel_hi:[1,0]
	v_med3_f32 v2, v2, s65, v178
	v_rcp_f32_e32 v12, v12
	v_rcp_f32_e32 v13, v13
	v_med3_f32 v3, v3, s65, v178
	v_pk_mul_f32 v[4:5], v[4:5], v[16:17]
	v_pk_fma_f32 v[8:9], v[34:35], s[24:25], v[8:9] op_sel_hi:[1,0,1] neg_lo:[1,0,0] neg_hi:[1,0,0]
	v_pk_mul_f32 v[2:3], v[2:3], v[4:5]
	v_mov_b32_e32 v4, v161
	v_cvt_pk_fp8_f32 v4, v2, v3
	v_mov_b32_e32 v5, v161
	v_cvt_pk_fp8_f32 v5, v10, v11
	v_med3_f32 v8, v8, s65, v178
	v_med3_f32 v9, v9, s65, v178
	v_pk_mul_f32 v[2:3], v[6:7], v[12:13]
	v_cvt_pk_fp8_f32 v5, v14, v15 op_sel:[0,0,1]
	v_pk_mul_f32 v[2:3], v[8:9], v[2:3]
	s_nop 0
	v_cvt_pk_fp8_f32 v4, v2, v3 op_sel:[0,0,1]
	v_add_u32_e32 v2, s66, v18
	v_ashrrev_i32_e32 v3, 31, v2
	v_lshlrev_b64 v[2:3], 10, v[2:3]
	v_lshl_add_u64 v[2:3], s[14:15], 0, v[2:3]
	v_lshl_add_u64 v[0:1], v[2:3], 0, v[0:1]
	global_store_dwordx2 v[0:1], v[4:5], off nt

.LBB0_964:
	v_mul_f32_e32 v128, 0x42000000, v108
	v_mul_f32_e32 v129, 0x42000000, v68
	v_med3_f32 v131, v128, s34, v144
	v_med3_f32 v129, v129, s34, v144
	v_mov_b32_e32 v128, v137
	v_cvt_pk_fp8_f32 v128, v131, v129
	v_mul_f32_e32 v130, 0x42000000, v64
	v_mul_f32_e32 v129, 0x42000000, v76
	v_med3_f32 v130, v130, s34, v144
	v_med3_f32 v129, v129, s34, v144
	v_cvt_pk_fp8_f32 v128, v130, v129 op_sel:[0,0,1]
	v_mul_f32_e32 v129, 0x42000000, v72
	v_mul_f32_e32 v130, 0x42000000, v84
	v_med3_f32 v145, v129, s34, v144
	v_med3_f32 v130, v130, s34, v144
	v_mov_b32_e32 v129, v137
	v_cvt_pk_fp8_f32 v129, v145, v130
	v_mul_f32_e32 v131, 0x42000000, v80
	v_mul_f32_e32 v130, 0x42000000, v92
	v_med3_f32 v131, v131, s34, v144
	v_med3_f32 v130, v130, s34, v144
	v_cvt_pk_fp8_f32 v129, v131, v130 op_sel:[0,0,1]
	v_mul_f32_e32 v130, 0x42000000, v88
	v_mul_f32_e32 v131, 0x42000000, v100
	v_med3_f32 v148, v130, s34, v144
	v_med3_f32 v131, v131, s34, v144
	v_mov_b32_e32 v130, v137
	v_cvt_pk_fp8_f32 v130, v148, v131
	s_lshr_b32 s12, s16, 8
	v_mul_f32_e32 v145, 0x42000000, v96
	v_mul_f32_e32 v131, 0x42000000, v104
	s_add_i32 s12, s12, 32
	v_med3_f32 v145, v145, s34, v144
	v_med3_f32 v131, v131, s34, v144
	s_mul_hi_u32 s13, s12, 0x300000
	s_mul_i32 s12, s12, 0x300000
	v_cvt_pk_fp8_f32 v130, v145, v131 op_sel:[0,0,1]
	v_mul_f32_e32 v131, 0x42000000, v112
	v_mul_f32_e32 v145, 0x42000000, v116
	s_add_u32 s12, s22, s12
	v_med3_f32 v149, v131, s34, v144
	v_med3_f32 v145, v145, s34, v144
	v_mov_b32_e32 v131, v137
	s_addc_u32 s13, s23, s13
	v_cvt_pk_fp8_f32 v131, v149, v145
	s_add_u32 s12, s12, s6
	s_addc_u32 s13, s13, 0
	v_mul_f32_e32 v148, 0x42000000, v120
	v_mul_f32_e32 v145, 0x42000000, v124
	v_lshl_add_u64 v[146:147], s[12:13], 0, v[132:133]
	v_med3_f32 v148, v148, s34, v144
	v_med3_f32 v145, v145, s34, v144
	v_cvt_pk_fp8_f32 v131, v148, v145 op_sel:[0,0,1]
	v_lshl_add_u64 v[146:147], v[146:147], 0, v[136:137]
	v_mul_f32_e32 v136, 0x42000000, v109
	v_mul_f32_e32 v145, 0x42000000, v69
	v_lshl_add_u64 v[158:159], v[146:147], 0, s[8:9]
	v_add_co_u32_e32 v160, vcc, s35, v146
	v_med3_f32 v136, v136, s34, v144
	v_med3_f32 v145, v145, s34, v144
	v_mov_b32_e32 v146, v137
	v_cvt_pk_fp8_f32 v146, v136, v145
	v_addc_co_u32_e32 v161, vcc, 0, v147, vcc
	v_mul_f32_e32 v147, 0x42000000, v65
	v_mul_f32_e32 v136, 0x42000000, v77
	v_med3_f32 v145, v147, s34, v144
	v_med3_f32 v136, v136, s34, v144
	v_cvt_pk_fp8_f32 v146, v145, v136 op_sel:[0,0,1]
	v_mul_f32_e32 v136, 0x42000000, v73
	v_mul_f32_e32 v145, 0x42000000, v85
	v_med3_f32 v136, v136, s34, v144
	v_med3_f32 v145, v145, s34, v144
	v_mov_b32_e32 v147, v137
	v_cvt_pk_fp8_f32 v147, v136, v145
	v_mul_f32_e32 v148, 0x42000000, v81
	v_mul_f32_e32 v136, 0x42000000, v93
	v_med3_f32 v145, v148, s34, v144
	v_med3_f32 v136, v136, s34, v144
	v_cvt_pk_fp8_f32 v147, v145, v136 op_sel:[0,0,1]
	v_mul_f32_e32 v136, 0x42000000, v89
	v_mul_f32_e32 v145, 0x42000000, v101
	v_med3_f32 v136, v136, s34, v144
	v_med3_f32 v145, v145, s34, v144
	v_mov_b32_e32 v148, v137
	v_cvt_pk_fp8_f32 v148, v136, v145
	v_mul_f32_e32 v149, 0x42000000, v97
	v_mul_f32_e32 v136, 0x42000000, v105
	v_med3_f32 v145, v149, s34, v144
	v_med3_f32 v136, v136, s34, v144
	v_cvt_pk_fp8_f32 v148, v145, v136 op_sel:[0,0,1]
	v_mul_f32_e32 v136, 0x42000000, v113
	v_mul_f32_e32 v145, 0x42000000, v117
	v_med3_f32 v136, v136, s34, v144
	v_med3_f32 v145, v145, s34, v144
	v_mov_b32_e32 v149, v137
	v_cvt_pk_fp8_f32 v149, v136, v145
	v_mul_f32_e32 v150, 0x42000000, v121
	v_mul_f32_e32 v136, 0x42000000, v125
	v_med3_f32 v145, v150, s34, v144
	v_med3_f32 v136, v136, s34, v144
	v_cvt_pk_fp8_f32 v149, v145, v136 op_sel:[0,0,1]
	v_mul_f32_e32 v136, 0x42000000, v110
	v_mul_f32_e32 v145, 0x42000000, v70
	v_med3_f32 v136, v136, s34, v144
	v_med3_f32 v145, v145, s34, v144
	v_mov_b32_e32 v150, v137
	v_cvt_pk_fp8_f32 v150, v136, v145
	v_mul_f32_e32 v151, 0x42000000, v66
	v_mul_f32_e32 v136, 0x42000000, v78
	v_med3_f32 v145, v151, s34, v144
	v_med3_f32 v136, v136, s34, v144
	v_cvt_pk_fp8_f32 v150, v145, v136 op_sel:[0,0,1]
	v_mul_f32_e32 v136, 0x42000000, v74
	v_mul_f32_e32 v145, 0x42000000, v86
	v_med3_f32 v136, v136, s34, v144
	v_med3_f32 v145, v145, s34, v144
	v_mov_b32_e32 v151, v137
	v_cvt_pk_fp8_f32 v151, v136, v145
	v_mul_f32_e32 v152, 0x42000000, v82
	v_mul_f32_e32 v136, 0x42000000, v94
	v_med3_f32 v145, v152, s34, v144
	v_med3_f32 v136, v136, s34, v144
	v_cvt_pk_fp8_f32 v151, v145, v136 op_sel:[0,0,1]
	v_mul_f32_e32 v136, 0x42000000, v90
	v_mul_f32_e32 v145, 0x42000000, v102
	v_med3_f32 v136, v136, s34, v144
	v_med3_f32 v145, v145, s34, v144
	v_mov_b32_e32 v152, v137
	v_cvt_pk_fp8_f32 v152, v136, v145
	v_mul_f32_e32 v153, 0x42000000, v98
	v_mul_f32_e32 v136, 0x42000000, v106
	v_med3_f32 v145, v153, s34, v144
	v_med3_f32 v136, v136, s34, v144
	v_cvt_pk_fp8_f32 v152, v145, v136 op_sel:[0,0,1]
	v_mul_f32_e32 v136, 0x42000000, v114
	v_mul_f32_e32 v145, 0x42000000, v118
	v_med3_f32 v136, v136, s34, v144
	v_med3_f32 v145, v145, s34, v144
	v_mov_b32_e32 v153, v137
	v_cvt_pk_fp8_f32 v153, v136, v145
	v_mul_f32_e32 v154, 0x42000000, v122
	v_mul_f32_e32 v136, 0x42000000, v126
	v_med3_f32 v145, v154, s34, v144
	v_med3_f32 v136, v136, s34, v144
	v_cvt_pk_fp8_f32 v153, v145, v136 op_sel:[0,0,1]
	v_mul_f32_e32 v136, 0x42000000, v111
	v_mul_f32_e32 v145, 0x42000000, v71
	v_med3_f32 v136, v136, s34, v144
	v_med3_f32 v145, v145, s34, v144
	v_mov_b32_e32 v154, v137
	v_cvt_pk_fp8_f32 v154, v136, v145
	v_mul_f32_e32 v155, 0x42000000, v67
	v_mul_f32_e32 v136, 0x42000000, v79
	v_med3_f32 v145, v155, s34, v144
	v_med3_f32 v136, v136, s34, v144
	v_cvt_pk_fp8_f32 v154, v145, v136 op_sel:[0,0,1]
	v_mul_f32_e32 v136, 0x42000000, v75
	v_mul_f32_e32 v145, 0x42000000, v87
	v_med3_f32 v136, v136, s34, v144
	v_med3_f32 v145, v145, s34, v144
	v_mov_b32_e32 v155, v137
	v_cvt_pk_fp8_f32 v155, v136, v145
	v_mul_f32_e32 v156, 0x42000000, v83
	v_mul_f32_e32 v136, 0x42000000, v95
	v_med3_f32 v145, v156, s34, v144
	v_med3_f32 v136, v136, s34, v144
	v_cvt_pk_fp8_f32 v155, v145, v136 op_sel:[0,0,1]
	v_mul_f32_e32 v136, 0x42000000, v91
	v_mul_f32_e32 v145, 0x42000000, v103
	v_med3_f32 v136, v136, s34, v144
	v_med3_f32 v145, v145, s34, v144
	v_mov_b32_e32 v156, v137
	v_cvt_pk_fp8_f32 v156, v136, v145
	v_mul_f32_e32 v157, 0x42000000, v99
	v_mul_f32_e32 v136, 0x42000000, v107
	v_med3_f32 v145, v157, s34, v144
	v_med3_f32 v136, v136, s34, v144
	v_cvt_pk_fp8_f32 v156, v145, v136 op_sel:[0,0,1]
	v_mul_f32_e32 v136, 0x42000000, v115
	v_mul_f32_e32 v145, 0x42000000, v119
	v_med3_f32 v136, v136, s34, v144
	v_med3_f32 v145, v145, s34, v144
	v_mov_b32_e32 v157, v137
	v_cvt_pk_fp8_f32 v157, v136, v145
	v_mul_f32_e32 v162, 0x42000000, v123
	v_mul_f32_e32 v136, 0x42000000, v127
	s_addk_i32 s24, 0x200
	s_addk_i32 s20, 0x800
	s_addk_i32 s21, 0x4000
	v_med3_f32 v145, v162, s34, v144
	v_med3_f32 v136, v136, s34, v144
	s_cmpk_gt_i32 s36, 0x1dff
	v_cvt_pk_fp8_f32 v157, v145, v136 op_sel:[0,0,1]
	v_lshl_add_u64 v[138:139], v[138:139], 0, s[10:11]
	s_cselect_b64 s[14:15], -1, 0
	global_store_dwordx4 v[160:161], v[128:131], off nt
	global_store_dwordx4 v[158:159], v[146:149], off offset:1024 nt
	global_store_dwordx4 v[158:159], v[150:153], off offset:2048 nt
	global_store_dwordx4 v[158:159], v[154:157], off offset:3072 nt

.LBB0_970:
	v_or_b32_e32 v128, s12, v134
	v_lshrrev_b32_e32 v128, 1, v128
	v_and_b32_e32 v128, 0x78, v128
	v_bitop3_b32 v129, s12, v143, v134 bitop3:0xc8
	v_or3_b32 v136, v142, v129, v128
	s_waitcnt vmcnt(7)
	v_mul_f32_e32 v128, 0x42000000, v24
	s_waitcnt vmcnt(14)
	v_mul_f32_e32 v129, 0x42000000, v0
	v_med3_f32 v131, v128, s34, v144
	v_med3_f32 v129, v129, s34, v144
	v_mov_b32_e32 v128, v137
	v_cvt_pk_fp8_f32 v128, v131, v129
	s_waitcnt vmcnt(13)
	v_mul_f32_e32 v130, 0x42000000, v4
	s_waitcnt vmcnt(12)
	v_mul_f32_e32 v129, 0x42000000, v8
	v_med3_f32 v130, v130, s34, v144
	v_med3_f32 v129, v129, s34, v144
	v_cvt_pk_fp8_f32 v128, v130, v129 op_sel:[0,0,1]
	s_waitcnt vmcnt(11)
	v_mul_f32_e32 v129, 0x42000000, v12
	s_waitcnt vmcnt(10)
	v_mul_f32_e32 v130, 0x42000000, v16
	v_med3_f32 v145, v129, s34, v144
	v_med3_f32 v130, v130, s34, v144
	v_mov_b32_e32 v129, v137
	v_cvt_pk_fp8_f32 v129, v145, v130
	s_waitcnt vmcnt(9)
	v_mul_f32_e32 v131, 0x42000000, v20
	s_waitcnt vmcnt(8)
	v_mul_f32_e32 v130, 0x42000000, v28
	v_med3_f32 v131, v131, s34, v144
	v_med3_f32 v130, v130, s34, v144
	v_cvt_pk_fp8_f32 v129, v131, v130 op_sel:[0,0,1]
	s_waitcnt vmcnt(7)
	v_mul_f32_e32 v130, 0x42000000, v32
	s_waitcnt vmcnt(6)
	v_mul_f32_e32 v131, 0x42000000, v36
	v_med3_f32 v146, v130, s34, v144
	v_med3_f32 v131, v131, s34, v144
	v_mov_b32_e32 v130, v137
	v_cvt_pk_fp8_f32 v130, v146, v131
	s_waitcnt vmcnt(5)
	v_mul_f32_e32 v145, 0x42000000, v40
	s_waitcnt vmcnt(4)
	v_mul_f32_e32 v131, 0x42000000, v44
	v_med3_f32 v145, v145, s34, v144
	v_med3_f32 v131, v131, s34, v144
	v_cvt_pk_fp8_f32 v130, v145, v131 op_sel:[0,0,1]
	s_waitcnt vmcnt(3)
	v_mul_f32_e32 v131, 0x42000000, v48
	s_waitcnt vmcnt(2)
	v_mul_f32_e32 v145, 0x42000000, v52
	v_med3_f32 v147, v131, s34, v144
	v_med3_f32 v145, v145, s34, v144
	v_mov_b32_e32 v131, v137
	v_cvt_pk_fp8_f32 v131, v147, v145
	s_waitcnt vmcnt(1)
	v_mul_f32_e32 v146, 0x42000000, v56
	s_waitcnt vmcnt(0)
	v_mul_f32_e32 v145, 0x42000000, v60
	v_med3_f32 v146, v146, s34, v144
	v_med3_f32 v145, v145, s34, v144
	v_lshlrev_b32_e32 v136, 10, v136
	v_cvt_pk_fp8_f32 v131, v146, v145 op_sel:[0,0,1]
	v_lshl_add_u64 v[146:147], v[136:137], 0, s[6:7]
	v_lshl_add_u64 v[158:159], v[138:139], 0, v[146:147]
	v_mul_f32_e32 v145, 0x42000000, v25
	v_mul_f32_e32 v146, 0x42000000, v1
	v_med3_f32 v145, v145, s34, v144
	v_med3_f32 v148, v146, s34, v144
	v_mov_b32_e32 v146, v137
	v_cvt_pk_fp8_f32 v146, v145, v148
	v_mul_f32_e32 v147, 0x42000000, v5
	v_mul_f32_e32 v145, 0x42000000, v9
	v_med3_f32 v147, v147, s34, v144
	v_med3_f32 v145, v145, s34, v144
	v_cvt_pk_fp8_f32 v146, v147, v145 op_sel:[0,0,1]
	v_mul_f32_e32 v145, 0x42000000, v13
	v_mul_f32_e32 v147, 0x42000000, v17
	v_med3_f32 v145, v145, s34, v144
	v_med3_f32 v149, v147, s34, v144
	v_mov_b32_e32 v147, v137
	v_cvt_pk_fp8_f32 v147, v145, v149
	v_mul_f32_e32 v148, 0x42000000, v21
	v_mul_f32_e32 v145, 0x42000000, v29
	v_med3_f32 v148, v148, s34, v144
	v_med3_f32 v145, v145, s34, v144
	v_cvt_pk_fp8_f32 v147, v148, v145 op_sel:[0,0,1]
	v_mul_f32_e32 v145, 0x42000000, v33
	v_mul_f32_e32 v148, 0x42000000, v37
	v_med3_f32 v145, v145, s34, v144
	v_med3_f32 v150, v148, s34, v144
	v_mov_b32_e32 v148, v137
	v_cvt_pk_fp8_f32 v148, v145, v150
	v_mul_f32_e32 v149, 0x42000000, v41
	v_mul_f32_e32 v145, 0x42000000, v45
	v_med3_f32 v149, v149, s34, v144
	v_med3_f32 v145, v145, s34, v144
	v_cvt_pk_fp8_f32 v148, v149, v145 op_sel:[0,0,1]
	v_mul_f32_e32 v145, 0x42000000, v49
	v_mul_f32_e32 v149, 0x42000000, v53
	v_med3_f32 v145, v145, s34, v144
	v_med3_f32 v151, v149, s34, v144
	v_mov_b32_e32 v149, v137
	v_cvt_pk_fp8_f32 v149, v145, v151
	v_mul_f32_e32 v150, 0x42000000, v57
	v_mul_f32_e32 v145, 0x42000000, v61
	v_med3_f32 v150, v150, s34, v144
	v_med3_f32 v145, v145, s34, v144
	v_cvt_pk_fp8_f32 v149, v150, v145 op_sel:[0,0,1]
	v_mul_f32_e32 v145, 0x42000000, v26
	v_mul_f32_e32 v150, 0x42000000, v2
	v_med3_f32 v145, v145, s34, v144
	v_med3_f32 v152, v150, s34, v144
	v_mov_b32_e32 v150, v137
	v_cvt_pk_fp8_f32 v150, v145, v152
	v_mul_f32_e32 v151, 0x42000000, v6
	v_mul_f32_e32 v145, 0x42000000, v10
	v_med3_f32 v151, v151, s34, v144
	v_med3_f32 v145, v145, s34, v144
	v_cvt_pk_fp8_f32 v150, v151, v145 op_sel:[0,0,1]
	v_mul_f32_e32 v145, 0x42000000, v14
	v_mul_f32_e32 v151, 0x42000000, v18
	v_med3_f32 v145, v145, s34, v144
	v_med3_f32 v153, v151, s34, v144
	v_mov_b32_e32 v151, v137
	v_cvt_pk_fp8_f32 v151, v145, v153
	v_mul_f32_e32 v152, 0x42000000, v22
	v_mul_f32_e32 v145, 0x42000000, v30
	v_med3_f32 v152, v152, s34, v144
	v_med3_f32 v145, v145, s34, v144
	v_cvt_pk_fp8_f32 v151, v152, v145 op_sel:[0,0,1]
	v_mul_f32_e32 v145, 0x42000000, v34
	v_mul_f32_e32 v152, 0x42000000, v38
	v_med3_f32 v145, v145, s34, v144
	v_med3_f32 v154, v152, s34, v144
	v_mov_b32_e32 v152, v137
	v_cvt_pk_fp8_f32 v152, v145, v154
	v_mul_f32_e32 v153, 0x42000000, v42
	v_mul_f32_e32 v145, 0x42000000, v46
	v_med3_f32 v153, v153, s34, v144
	v_med3_f32 v145, v145, s34, v144
	v_cvt_pk_fp8_f32 v152, v153, v145 op_sel:[0,0,1]
	v_mul_f32_e32 v145, 0x42000000, v50
	v_mul_f32_e32 v153, 0x42000000, v54
	v_med3_f32 v145, v145, s34, v144
	v_med3_f32 v155, v153, s34, v144
	v_mov_b32_e32 v153, v137
	v_cvt_pk_fp8_f32 v153, v145, v155
	v_mul_f32_e32 v154, 0x42000000, v58
	v_mul_f32_e32 v145, 0x42000000, v62
	v_med3_f32 v154, v154, s34, v144
	v_med3_f32 v145, v145, s34, v144
	v_cvt_pk_fp8_f32 v153, v154, v145 op_sel:[0,0,1]
	v_mul_f32_e32 v145, 0x42000000, v27
	v_mul_f32_e32 v154, 0x42000000, v3
	v_med3_f32 v145, v145, s34, v144
	v_med3_f32 v156, v154, s34, v144
	v_mov_b32_e32 v154, v137
	v_cvt_pk_fp8_f32 v154, v145, v156
	v_mul_f32_e32 v155, 0x42000000, v7
	v_mul_f32_e32 v145, 0x42000000, v11
	v_med3_f32 v155, v155, s34, v144
	v_med3_f32 v145, v145, s34, v144
	v_cvt_pk_fp8_f32 v154, v155, v145 op_sel:[0,0,1]
	v_mul_f32_e32 v145, 0x42000000, v15
	v_mul_f32_e32 v155, 0x42000000, v19
	v_med3_f32 v145, v145, s34, v144
	v_med3_f32 v157, v155, s34, v144
	v_mov_b32_e32 v155, v137
	v_cvt_pk_fp8_f32 v155, v145, v157
	v_mul_f32_e32 v156, 0x42000000, v23
	v_mul_f32_e32 v145, 0x42000000, v31
	v_med3_f32 v156, v156, s34, v144
	v_med3_f32 v145, v145, s34, v144
	v_cvt_pk_fp8_f32 v155, v156, v145 op_sel:[0,0,1]
	v_mul_f32_e32 v145, 0x42000000, v35
	v_mul_f32_e32 v156, 0x42000000, v39
	v_med3_f32 v145, v145, s34, v144
	v_med3_f32 v160, v156, s34, v144
	v_mov_b32_e32 v156, v137
	v_cvt_pk_fp8_f32 v156, v145, v160
	v_mul_f32_e32 v157, 0x42000000, v43
	v_mul_f32_e32 v145, 0x42000000, v47
	v_med3_f32 v157, v157, s34, v144
	v_med3_f32 v145, v145, s34, v144
	v_cvt_pk_fp8_f32 v156, v157, v145 op_sel:[0,0,1]
	v_mul_f32_e32 v145, 0x42000000, v51
	v_mul_f32_e32 v157, 0x42000000, v55
	v_med3_f32 v145, v145, s34, v144
	v_med3_f32 v161, v157, s34, v144
	v_mov_b32_e32 v157, v137
	v_cvt_pk_fp8_f32 v157, v145, v161
	v_mul_f32_e32 v160, 0x42000000, v59
	v_mul_f32_e32 v145, 0x42000000, v63
	v_med3_f32 v160, v160, s34, v144
	v_med3_f32 v145, v145, s34, v144
	v_cvt_pk_fp8_f32 v157, v160, v145 op_sel:[0,0,1]
	s_andn2_b64 vcc, exec, s[14:15]
	s_mov_b64 s[14:15], -1
	global_store_dwordx4 v[158:159], v[128:131], off offset:-3072 nt
	global_store_dwordx4 v[158:159], v[146:149], off offset:-2048 nt
	global_store_dwordx4 v[158:159], v[150:153], off offset:-1024 nt
	global_store_dwordx4 v[158:159], v[154:157], off nt
	s_cbranch_vccnz .LBB0_965
	s_cmpk_gt_i32 s36, 0x1dff
	s_cbranch_scc1 .LBB0_964
	s_lshr_b32 s13, s24, 8
	s_add_i32 s14, s13, 32
	s_mov_b32 s15, s7
	s_lshl_b64 s[14:15], s[14:15], 22
	v_add_u32_e32 v0, s6, v132
	s_add_u32 s14, s4, s14
	v_ashrrev_i32_e32 v1, 31, v0
	s_addc_u32 s15, s5, s15
	v_lshlrev_b64 v[0:1], 12, v[0:1]
	v_lshl_add_u64 v[0:1], s[14:15], 0, v[0:1]
	s_mov_b32 s13, s7
	v_lshl_add_u64 v[0:1], s[12:13], 2, v[0:1]
	v_lshlrev_b32_e32 v2, 2, v134
	v_mov_b32_e32 v3, v137
	v_lshl_add_u64 v[56:57], v[0:1], 0, v[2:3]
	v_add_co_u32_e32 v8, vcc, s25, v56
	s_nop 1
	v_addc_co_u32_e32 v9, vcc, 0, v57, vcc
	v_add_co_u32_e32 v16, vcc, s26, v56
	global_load_dwordx4 v[0:3], v[8:9], off offset:-4096 nt
	global_load_dwordx4 v[4:7], v[8:9], off nt
	v_addc_co_u32_e32 v17, vcc, 0, v57, vcc
	v_add_co_u32_e32 v24, vcc, s27, v56
	global_load_dwordx4 v[8:11], v[16:17], off offset:-4096 nt
	global_load_dwordx4 v[12:15], v[16:17], off nt
	v_addc_co_u32_e32 v25, vcc, 0, v57, vcc
	global_load_dwordx4 v[16:19], v[24:25], off offset:-4096 nt
	global_load_dwordx4 v[20:23], v[24:25], off nt
	v_add_co_u32_e32 v24, vcc, s28, v56
	s_nop 1
	v_addc_co_u32_e32 v25, vcc, 0, v57, vcc
	global_load_dwordx4 v[28:31], v[24:25], off offset:-4096 nt
	global_load_dwordx4 v[32:35], v[24:25], off nt
	v_add_co_u32_e32 v24, vcc, s29, v56
	s_nop 1
	v_addc_co_u32_e32 v25, vcc, 0, v57, vcc
	global_load_dwordx4 v[36:39], v[24:25], off offset:-4096 nt
	global_load_dwordx4 v[40:43], v[24:25], off nt
	v_add_co_u32_e32 v24, vcc, s31, v56
	s_nop 1
	v_addc_co_u32_e32 v25, vcc, 0, v57, vcc
	v_add_co_u32_e32 v52, vcc, 0xd000, v56
	global_load_dwordx4 v[44:47], v[24:25], off offset:-4096 nt
	global_load_dwordx4 v[48:51], v[24:25], off nt
	v_addc_co_u32_e32 v53, vcc, 0, v57, vcc
	v_add_co_u32_e32 v58, vcc, 0xe000, v56
	global_load_dwordx4 v[24:27], v[56:57], off nt
	s_nop 0
	global_load_dwordx4 v[52:55], v[52:53], off nt
	v_addc_co_u32_e32 v59, vcc, 0, v57, vcc
	v_add_co_u32_e32 v60, vcc, 0xf000, v56
	s_nop 1
	v_addc_co_u32_e32 v61, vcc, 0, v57, vcc
	global_load_dwordx4 v[56:59], v[58:59], off nt
	s_nop 0
	global_load_dwordx4 v[60:63], v[60:61], off nt
	s_branch .LBB0_964

.LBB0_975:
	v_ashrrev_i32_e32 v141, 31, v140
	v_lshlrev_b64 v[140:141], 10, v[140:141]
	v_lshl_add_u64 v[138:139], v[138:139], 0, v[140:141]
	global_store_dwordx4 v[138:139], v[128:131], off nt

.LBB0_979:
	s_ashr_i32 s8, s19, 31
	s_lshr_b32 s9, s8, 24
	s_add_i32 s9, s19, s9
	s_lshr_b32 s8, s8, 23
	s_ashr_i32 s25, s9, 8
	s_and_b32 s24, s9, 0xffffff00
	s_add_i32 s8, s19, s8
	s_lshr_b32 s9, s9, 31
	s_ashr_i32 s8, s8, 9
	s_add_i32 s9, s25, s9
	s_add_i32 s8, s8, 50
	s_and_b32 s9, s9, -2
	s_sub_i32 s24, s19, s24
	s_sub_i32 s27, s25, s9
	s_mul_hi_i32 s9, s8, 0x300000
	s_mul_i32 s8, s8, 0x300000
	s_add_u32 s25, s20, s8
	s_addc_u32 s26, s21, s9
	s_mov_b64 s[8:9], -1
	s_cmp_gt_i32 s27, 0
	s_waitcnt vmcnt(15)
	v_mul_f32_e32 v202, 0x42000000, v0
	s_waitcnt vmcnt(14)
	v_mul_f32_e32 v203, 0x42000000, v4
	s_waitcnt vmcnt(13)
	v_mul_f32_e32 v204, 0x42000000, v8
	s_waitcnt vmcnt(12)
	v_mul_f32_e32 v205, 0x42000000, v12
	s_waitcnt vmcnt(11)
	v_mul_f32_e32 v200, 0x42000000, v16
	s_waitcnt vmcnt(10)
	v_mul_f32_e32 v201, 0x42000000, v20
	s_waitcnt vmcnt(9)
	v_mul_f32_e32 v198, 0x42000000, v24
	s_waitcnt vmcnt(8)
	v_mul_f32_e32 v199, 0x42000000, v28
	s_waitcnt vmcnt(7)
	v_mul_f32_e32 v194, 0x42000000, v32
	s_waitcnt vmcnt(6)
	v_mul_f32_e32 v195, 0x42000000, v36
	s_waitcnt vmcnt(5)
	v_mul_f32_e32 v196, 0x42000000, v40
	s_waitcnt vmcnt(4)
	v_mul_f32_e32 v197, 0x42000000, v44
	s_waitcnt vmcnt(3)
	v_mul_f32_e32 v192, 0x42000000, v48
	s_waitcnt vmcnt(2)
	v_mul_f32_e32 v193, 0x42000000, v60
	s_waitcnt vmcnt(1)
	v_mul_f32_e32 v190, 0x42000000, v88
	s_waitcnt vmcnt(0)
	v_mul_f32_e32 v191, 0x42000000, v100
	v_mul_f32_e32 v186, 0x42000000, v1
	v_mul_f32_e32 v187, 0x42000000, v5
	v_mul_f32_e32 v188, 0x42000000, v9
	v_mul_f32_e32 v189, 0x42000000, v13
	v_mul_f32_e32 v184, 0x42000000, v17
	v_mul_f32_e32 v185, 0x42000000, v21
	v_mul_f32_e32 v182, 0x42000000, v25
	v_mul_f32_e32 v183, 0x42000000, v29
	v_mul_f32_e32 v178, 0x42000000, v33
	v_mul_f32_e32 v179, 0x42000000, v37
	v_mul_f32_e32 v180, 0x42000000, v41
	v_mul_f32_e32 v181, 0x42000000, v45
	v_mul_f32_e32 v176, 0x42000000, v49
	v_mul_f32_e32 v177, 0x42000000, v61
	v_mul_f32_e32 v174, 0x42000000, v89
	v_mul_f32_e32 v175, 0x42000000, v101
	v_mul_f32_e32 v170, 0x42000000, v2
	v_mul_f32_e32 v171, 0x42000000, v6
	v_mul_f32_e32 v172, 0x42000000, v10
	v_mul_f32_e32 v173, 0x42000000, v14
	v_mul_f32_e32 v168, 0x42000000, v18
	v_mul_f32_e32 v169, 0x42000000, v22
	v_mul_f32_e32 v166, 0x42000000, v26
	v_mul_f32_e32 v167, 0x42000000, v30
	v_mul_f32_e32 v162, 0x42000000, v34
	v_mul_f32_e32 v163, 0x42000000, v38
	v_mul_f32_e32 v164, 0x42000000, v42
	v_mul_f32_e32 v165, 0x42000000, v46
	v_mul_f32_e32 v160, 0x42000000, v50
	v_mul_f32_e32 v161, 0x42000000, v62
	v_mul_f32_e32 v158, 0x42000000, v90
	v_mul_f32_e32 v159, 0x42000000, v102
	v_mul_f32_e32 v154, 0x42000000, v3
	v_mul_f32_e32 v155, 0x42000000, v7
	v_mul_f32_e32 v156, 0x42000000, v11
	v_mul_f32_e32 v157, 0x42000000, v15
	v_mul_f32_e32 v152, 0x42000000, v19
	v_mul_f32_e32 v153, 0x42000000, v23
	v_mul_f32_e32 v150, 0x42000000, v27
	v_mul_f32_e32 v151, 0x42000000, v31
	v_mul_f32_e32 v146, 0x42000000, v35
	v_mul_f32_e32 v147, 0x42000000, v39
	v_mul_f32_e32 v148, 0x42000000, v43
	v_mul_f32_e32 v149, 0x42000000, v47
	v_mul_f32_e32 v144, 0x42000000, v51
	v_mul_f32_e32 v145, 0x42000000, v63
	v_mul_f32_e32 v136, 0x42000000, v91
	v_mul_f32_e32 v141, 0x42000000, v103
	s_cbranch_scc0 .LBB0_981
	v_med3_f32 v129, v202, s22, v142
	v_med3_f32 v130, v203, s22, v142
	v_mov_b32_e32 v128, v137
	v_cvt_pk_fp8_f32 v128, v129, v130
	v_med3_f32 v130, v200, s22, v142
	v_med3_f32 v207, v201, s22, v142
	v_mov_b32_e32 v129, v137
	v_cvt_pk_fp8_f32 v129, v130, v207
	s_bfe_u32 s8, s24, 0x5001a
	s_add_i32 s8, s24, s8
	v_med3_f32 v131, v204, s22, v142
	v_med3_f32 v206, v205, s22, v142
	s_sext_i32_i16 s9, s8
	s_and_b32 s8, s8, 0xffe0
	v_cvt_pk_fp8_f32 v128, v131, v206 op_sel:[0,0,1]
	v_med3_f32 v130, v198, s22, v142
	v_med3_f32 v131, v199, s22, v142
	s_sub_i32 s8, s24, s8
	v_cvt_pk_fp8_f32 v129, v130, v131 op_sel:[0,0,1]
	v_med3_f32 v131, v194, s22, v142
	v_med3_f32 v206, v195, s22, v142
	v_mov_b32_e32 v130, v137
	s_sext_i32_i16 s8, s8
	v_cvt_pk_fp8_f32 v130, v131, v206
	v_med3_f32 v206, v192, s22, v142
	v_med3_f32 v209, v193, s22, v142
	v_mov_b32_e32 v131, v137
	s_lshl_b32 s28, s8, 5
	s_lshl_b32 s8, s8, 6
	v_cvt_pk_fp8_f32 v131, v206, v209
	s_lshl_b32 s9, s9, 2
	s_and_b32 s8, s8, 0xffffff00
	s_and_b32 s28, s28, 0x60
	s_and_b32 s9, s9, 0xffffff80
	s_or_b32 s8, s28, s8
	v_med3_f32 v207, v196, s22, v142
	v_med3_f32 v208, v197, s22, v142
	v_or_b32_e32 v140, s8, v134
	s_ashr_i32 s28, s9, 31
	v_cvt_pk_fp8_f32 v130, v207, v208 op_sel:[0,0,1]
	v_med3_f32 v206, v190, s22, v142
	v_med3_f32 v207, v191, s22, v142
	s_add_u32 s8, s25, s9
	v_cvt_pk_fp8_f32 v131, v206, v207 op_sel:[0,0,1]
	v_or_b32_e32 v206, 0x80, v140
	s_addc_u32 s9, s26, s28
	v_ashrrev_i32_e32 v207, 31, v206
	v_lshl_add_u64 v[138:139], s[8:9], 0, v[132:133]
	v_lshlrev_b64 v[206:207], 10, v[206:207]
	v_lshl_add_u64 v[206:207], v[138:139], 0, v[206:207]
	global_store_dwordx4 v[206:207], v[128:131], off nt
	v_med3_f32 v207, v185, s22, v142
	v_med3_f32 v206, v189, s22, v142
	v_med3_f32 v129, v186, s22, v142
	v_med3_f32 v130, v187, s22, v142
	v_mov_b32_e32 v128, v137
	v_cvt_pk_fp8_f32 v128, v129, v130
	v_med3_f32 v130, v184, s22, v142
	v_mov_b32_e32 v129, v137
	v_cvt_pk_fp8_f32 v129, v130, v207
	v_med3_f32 v131, v188, s22, v142
	v_cvt_pk_fp8_f32 v128, v131, v206 op_sel:[0,0,1]
	v_med3_f32 v130, v182, s22, v142
	v_med3_f32 v131, v183, s22, v142
	v_cvt_pk_fp8_f32 v129, v130, v131 op_sel:[0,0,1]
	v_med3_f32 v131, v178, s22, v142
	v_med3_f32 v206, v179, s22, v142
	v_mov_b32_e32 v130, v137
	v_cvt_pk_fp8_f32 v130, v131, v206
	v_med3_f32 v206, v176, s22, v142
	v_med3_f32 v209, v177, s22, v142
	v_mov_b32_e32 v131, v137
	v_cvt_pk_fp8_f32 v131, v206, v209
	v_med3_f32 v207, v180, s22, v142
	v_med3_f32 v208, v181, s22, v142
	v_cvt_pk_fp8_f32 v130, v207, v208 op_sel:[0,0,1]
	v_med3_f32 v206, v174, s22, v142
	v_med3_f32 v207, v175, s22, v142
	v_cvt_pk_fp8_f32 v131, v206, v207 op_sel:[0,0,1]
	v_or_b32_e32 v206, 0x81, v140
	v_ashrrev_i32_e32 v207, 31, v206
	v_lshlrev_b64 v[206:207], 10, v[206:207]
	v_lshl_add_u64 v[206:207], v[138:139], 0, v[206:207]
	global_store_dwordx4 v[206:207], v[128:131], off nt
	v_mov_b32_e32 v206, v137
	v_mov_b32_e32 v207, v137
	v_med3_f32 v128, v170, s22, v142
	v_med3_f32 v129, v171, s22, v142
	v_cvt_pk_fp8_f32 v206, v128, v129
	v_med3_f32 v128, v168, s22, v142
	v_med3_f32 v129, v169, s22, v142
	v_cvt_pk_fp8_f32 v207, v128, v129
	v_med3_f32 v128, v166, s22, v142
	v_med3_f32 v129, v167, s22, v142
	v_mov_b32_e32 v208, v137
	v_cvt_pk_fp8_f32 v207, v128, v129 op_sel:[0,0,1]
	v_med3_f32 v128, v162, s22, v142
	v_med3_f32 v129, v163, s22, v142
	v_cvt_pk_fp8_f32 v208, v128, v129
	v_med3_f32 v128, v160, s22, v142
	v_med3_f32 v129, v161, s22, v142
	v_mov_b32_e32 v209, v137
	v_cvt_pk_fp8_f32 v209, v128, v129
	v_med3_f32 v128, v158, s22, v142
	v_med3_f32 v129, v159, s22, v142
	v_med3_f32 v130, v172, s22, v142
	v_cvt_pk_fp8_f32 v209, v128, v129 op_sel:[0,0,1]
	v_or_b32_e32 v128, 0x82, v140
	v_med3_f32 v131, v173, s22, v142
	v_ashrrev_i32_e32 v129, 31, v128
	v_cvt_pk_fp8_f32 v206, v130, v131 op_sel:[0,0,1]
	v_med3_f32 v130, v164, s22, v142
	v_med3_f32 v131, v165, s22, v142
	v_lshlrev_b64 v[128:129], 10, v[128:129]
	v_cvt_pk_fp8_f32 v208, v130, v131 op_sel:[0,0,1]
	v_lshl_add_u64 v[210:211], v[138:139], 0, v[128:129]
	v_med3_f32 v129, v154, s22, v142
	v_med3_f32 v130, v155, s22, v142
	v_mov_b32_e32 v128, v137
	v_cvt_pk_fp8_f32 v128, v129, v130
	v_med3_f32 v130, v152, s22, v142
	v_med3_f32 v213, v153, s22, v142
	v_mov_b32_e32 v129, v137
	v_cvt_pk_fp8_f32 v129, v130, v213
	v_med3_f32 v131, v156, s22, v142
	v_med3_f32 v212, v157, s22, v142
	v_cvt_pk_fp8_f32 v128, v131, v212 op_sel:[0,0,1]
	v_med3_f32 v130, v150, s22, v142
	v_med3_f32 v131, v151, s22, v142
	v_cvt_pk_fp8_f32 v129, v130, v131 op_sel:[0,0,1]
	v_med3_f32 v131, v146, s22, v142
	v_med3_f32 v212, v147, s22, v142
	v_mov_b32_e32 v130, v137
	v_cvt_pk_fp8_f32 v130, v131, v212
	v_med3_f32 v212, v144, s22, v142
	v_med3_f32 v215, v145, s22, v142
	v_mov_b32_e32 v131, v137
	v_cvt_pk_fp8_f32 v131, v212, v215
	v_med3_f32 v213, v148, s22, v142
	v_med3_f32 v214, v149, s22, v142
	v_cvt_pk_fp8_f32 v130, v213, v214 op_sel:[0,0,1]
	v_med3_f32 v212, v136, s22, v142
	v_med3_f32 v213, v141, s22, v142
	v_cvt_pk_fp8_f32 v131, v212, v213 op_sel:[0,0,1]
	global_store_dwordx4 v[210:211], v[206:209], off nt
	v_or_b32_e32 v140, 0x83, v140
	s_mov_b64 s[8:9], 0
.LBB0_981:
	s_andn2_b64 vcc, exec, s[8:9]
	s_cbranch_vccnz .LBB0_985
	s_cmp_lg_u32 s27, 0
	s_cbranch_scc0 .LBB0_993
	s_bfe_u32 s8, s24, 0x5001a
	s_add_i32 s8, s24, s8
	s_sext_i32_i16 s9, s8
	s_and_b32 s8, s8, 0xffe0
	s_sub_i32 s8, s24, s8
	s_sext_i32_i16 s8, s8
	s_lshl_b32 s9, s9, 2
	s_and_b32 s9, s9, 0xffffff80
	s_lshl_b32 s8, s8, 5
	v_or_b32_e32 v128, s8, v134
	s_ashr_i32 s27, s9, 31
	v_lshlrev_b32_e32 v129, 4, v134
	v_lshrrev_b32_e32 v128, 1, v128
	v_bitop3_b32 v130, s8, v143, v134 bitop3:0xc8
	s_add_u32 s8, s25, s9
	v_and_b32_e32 v129, 0x80, v129
	v_and_b32_e32 v128, 0x78, v128
	s_addc_u32 s9, s26, s27
	v_or3_b32 v210, v129, v130, v128
	v_lshl_add_u64 v[128:129], s[8:9], 0, v[132:133]
	v_lshl_add_u64 v[138:139], v[128:129], 0, s[4:5]
	v_med3_f32 v129, v202, s22, v142
	v_med3_f32 v130, v203, s22, v142
	v_mov_b32_e32 v128, v137
	v_cvt_pk_fp8_f32 v128, v129, v130
	v_med3_f32 v130, v200, s22, v142
	v_med3_f32 v206, v201, s22, v142
	v_mov_b32_e32 v129, v137
	v_cvt_pk_fp8_f32 v129, v130, v206
	v_med3_f32 v131, v204, s22, v142
	v_med3_f32 v140, v205, s22, v142
	v_cvt_pk_fp8_f32 v128, v131, v140 op_sel:[0,0,1]
	v_med3_f32 v130, v198, s22, v142
	v_med3_f32 v131, v199, s22, v142
	v_cvt_pk_fp8_f32 v129, v130, v131 op_sel:[0,0,1]
	v_med3_f32 v131, v194, s22, v142
	v_med3_f32 v140, v195, s22, v142
	v_mov_b32_e32 v130, v137
	v_cvt_pk_fp8_f32 v130, v131, v140
	v_med3_f32 v140, v192, s22, v142
	v_med3_f32 v208, v193, s22, v142
	v_mov_b32_e32 v131, v137
	v_cvt_pk_fp8_f32 v131, v140, v208
	v_med3_f32 v206, v196, s22, v142
	v_med3_f32 v207, v197, s22, v142
	v_cvt_pk_fp8_f32 v130, v206, v207 op_sel:[0,0,1]
	v_med3_f32 v140, v190, s22, v142
	v_med3_f32 v206, v191, s22, v142
	v_cvt_pk_fp8_f32 v131, v140, v206 op_sel:[0,0,1]
	v_ashrrev_i32_e32 v211, 31, v210
	v_lshlrev_b64 v[206:207], 10, v[210:211]
	v_lshl_add_u64 v[206:207], v[138:139], 0, v[206:207]
	global_store_dwordx4 v[206:207], v[128:131], off nt
	v_med3_f32 v206, v185, s22, v142
	v_med3_f32 v140, v189, s22, v142
	v_med3_f32 v129, v186, s22, v142
	v_med3_f32 v130, v187, s22, v142
	v_mov_b32_e32 v128, v137
	v_cvt_pk_fp8_f32 v128, v129, v130
	v_med3_f32 v130, v184, s22, v142
	v_mov_b32_e32 v129, v137
	v_cvt_pk_fp8_f32 v129, v130, v206
	v_med3_f32 v131, v188, s22, v142
	v_cvt_pk_fp8_f32 v128, v131, v140 op_sel:[0,0,1]
	v_med3_f32 v130, v182, s22, v142
	v_med3_f32 v131, v183, s22, v142
	v_cvt_pk_fp8_f32 v129, v130, v131 op_sel:[0,0,1]
	v_med3_f32 v131, v178, s22, v142
	v_med3_f32 v140, v179, s22, v142
	v_mov_b32_e32 v130, v137
	v_cvt_pk_fp8_f32 v130, v131, v140
	v_med3_f32 v140, v176, s22, v142
	v_med3_f32 v208, v177, s22, v142
	v_mov_b32_e32 v131, v137
	v_cvt_pk_fp8_f32 v131, v140, v208
	v_med3_f32 v206, v180, s22, v142
	v_med3_f32 v207, v181, s22, v142
	v_cvt_pk_fp8_f32 v130, v206, v207 op_sel:[0,0,1]
	v_med3_f32 v140, v174, s22, v142
	v_med3_f32 v206, v175, s22, v142
	v_cvt_pk_fp8_f32 v131, v140, v206 op_sel:[0,0,1]
	v_or_b32_e32 v206, 1, v210
	v_ashrrev_i32_e32 v207, 31, v206
	v_lshlrev_b64 v[206:207], 10, v[206:207]
	v_lshl_add_u64 v[206:207], v[138:139], 0, v[206:207]
	global_store_dwordx4 v[206:207], v[128:131], off nt
	v_mov_b32_e32 v206, v137
	v_mov_b32_e32 v207, v137
	v_med3_f32 v128, v170, s22, v142
	v_med3_f32 v129, v171, s22, v142
	v_cvt_pk_fp8_f32 v206, v128, v129
	v_med3_f32 v128, v168, s22, v142
	v_med3_f32 v129, v169, s22, v142
	v_cvt_pk_fp8_f32 v207, v128, v129
	v_med3_f32 v128, v166, s22, v142
	v_med3_f32 v129, v167, s22, v142
	v_mov_b32_e32 v208, v137
	v_cvt_pk_fp8_f32 v207, v128, v129 op_sel:[0,0,1]
	v_med3_f32 v128, v162, s22, v142
	v_med3_f32 v129, v163, s22, v142
	v_cvt_pk_fp8_f32 v208, v128, v129
	v_med3_f32 v128, v160, s22, v142
	v_med3_f32 v129, v161, s22, v142
	v_mov_b32_e32 v209, v137
	v_cvt_pk_fp8_f32 v209, v128, v129
	v_med3_f32 v128, v158, s22, v142
	v_med3_f32 v129, v159, s22, v142
	v_med3_f32 v130, v172, s22, v142
	v_cvt_pk_fp8_f32 v209, v128, v129 op_sel:[0,0,1]
	v_or_b32_e32 v128, 2, v210
	v_med3_f32 v131, v173, s22, v142
	v_ashrrev_i32_e32 v129, 31, v128
	v_cvt_pk_fp8_f32 v206, v130, v131 op_sel:[0,0,1]
	v_med3_f32 v130, v164, s22, v142
	v_med3_f32 v131, v165, s22, v142
	v_lshlrev_b64 v[128:129], 10, v[128:129]
	v_cvt_pk_fp8_f32 v208, v130, v131 op_sel:[0,0,1]
	v_lshl_add_u64 v[212:213], v[138:139], 0, v[128:129]
	v_med3_f32 v129, v154, s22, v142
	v_med3_f32 v130, v155, s22, v142
	v_mov_b32_e32 v128, v137
	v_cvt_pk_fp8_f32 v128, v129, v130
	v_med3_f32 v130, v152, s22, v142
	v_med3_f32 v211, v153, s22, v142
	v_mov_b32_e32 v129, v137
	v_cvt_pk_fp8_f32 v129, v130, v211
	v_med3_f32 v131, v156, s22, v142
	v_med3_f32 v140, v157, s22, v142
	v_cvt_pk_fp8_f32 v128, v131, v140 op_sel:[0,0,1]
	v_med3_f32 v130, v150, s22, v142
	v_med3_f32 v131, v151, s22, v142
	v_cvt_pk_fp8_f32 v129, v130, v131 op_sel:[0,0,1]
	v_med3_f32 v131, v146, s22, v142
	v_med3_f32 v140, v147, s22, v142
	v_mov_b32_e32 v130, v137
	v_cvt_pk_fp8_f32 v130, v131, v140
	v_med3_f32 v140, v144, s22, v142
	v_med3_f32 v215, v145, s22, v142
	v_mov_b32_e32 v131, v137
	v_cvt_pk_fp8_f32 v131, v140, v215
	v_med3_f32 v211, v148, s22, v142
	v_med3_f32 v214, v149, s22, v142
	v_cvt_pk_fp8_f32 v130, v211, v214 op_sel:[0,0,1]
	v_med3_f32 v140, v136, s22, v142
	v_med3_f32 v211, v141, s22, v142
	v_cvt_pk_fp8_f32 v131, v140, v211 op_sel:[0,0,1]
	global_store_dwordx4 v[212:213], v[206:209], off nt
	v_or_b32_e32 v140, 3, v210
	s_cbranch_execnz .LBB0_985
.LBB0_984:
	v_med3_f32 v129, v202, s22, v142
	v_med3_f32 v130, v203, s22, v142
	v_mov_b32_e32 v128, v137
	v_cvt_pk_fp8_f32 v128, v129, v130
	v_med3_f32 v130, v200, s22, v142
	v_med3_f32 v200, v201, s22, v142
	v_mov_b32_e32 v129, v137
	v_cvt_pk_fp8_f32 v129, v130, v200
	s_bfe_u32 s8, s24, 0x5001a
	v_med3_f32 v131, v204, s22, v142
	v_med3_f32 v140, v205, s22, v142
	s_add_i32 s8, s24, s8
	v_cvt_pk_fp8_f32 v128, v131, v140 op_sel:[0,0,1]
	v_med3_f32 v130, v198, s22, v142
	v_med3_f32 v131, v199, s22, v142
	s_sext_i32_i16 s9, s8
	s_and_b32 s8, s8, 0xffe0
	v_cvt_pk_fp8_f32 v129, v130, v131 op_sel:[0,0,1]
	v_med3_f32 v131, v194, s22, v142
	v_med3_f32 v140, v195, s22, v142
	v_mov_b32_e32 v130, v137
	s_sub_i32 s8, s24, s8
	v_cvt_pk_fp8_f32 v130, v131, v140
	v_med3_f32 v140, v192, s22, v142
	v_med3_f32 v192, v193, s22, v142
	v_mov_b32_e32 v131, v137
	s_sext_i32_i16 s8, s8
	v_cvt_pk_fp8_f32 v131, v140, v192
	s_lshl_b32 s9, s9, 2
	s_lshl_b32 s24, s8, 5
	s_lshl_b32 s8, s8, 6
	s_and_b32 s9, s9, 0xffffff80
	s_and_b32 s8, s8, 0xffffff00
	s_and_b32 s24, s24, 0x60
	s_or_b32 s8, s24, s8
	s_ashr_i32 s24, s9, 31
	v_med3_f32 v194, v196, s22, v142
	v_med3_f32 v195, v197, s22, v142
	v_med3_f32 v140, v190, s22, v142
	v_med3_f32 v190, v191, s22, v142
	v_or_b32_e32 v206, s8, v134
	s_add_u32 s8, s25, s9
	v_cvt_pk_fp8_f32 v130, v194, v195 op_sel:[0,0,1]
	v_cvt_pk_fp8_f32 v131, v140, v190 op_sel:[0,0,1]
	s_addc_u32 s9, s26, s24
	v_ashrrev_i32_e32 v207, 31, v206
	v_lshl_add_u64 v[138:139], s[8:9], 0, v[132:133]
	v_lshlrev_b64 v[190:191], 10, v[206:207]
	v_lshl_add_u64 v[190:191], v[138:139], 0, v[190:191]
	global_store_dwordx4 v[190:191], v[128:131], off nt
	v_med3_f32 v140, v189, s22, v142
	v_med3_f32 v136, v136, s22, v142
	v_med3_f32 v129, v186, s22, v142
	v_med3_f32 v130, v187, s22, v142
	v_mov_b32_e32 v128, v137
	v_cvt_pk_fp8_f32 v128, v129, v130
	v_med3_f32 v130, v184, s22, v142
	v_med3_f32 v184, v185, s22, v142
	v_mov_b32_e32 v129, v137
	v_cvt_pk_fp8_f32 v129, v130, v184
	v_med3_f32 v131, v188, s22, v142
	v_cvt_pk_fp8_f32 v128, v131, v140 op_sel:[0,0,1]
	v_med3_f32 v130, v182, s22, v142
	v_med3_f32 v131, v183, s22, v142
	v_cvt_pk_fp8_f32 v129, v130, v131 op_sel:[0,0,1]
	v_med3_f32 v131, v178, s22, v142
	v_med3_f32 v140, v179, s22, v142
	v_mov_b32_e32 v130, v137
	v_cvt_pk_fp8_f32 v130, v131, v140
	v_med3_f32 v140, v176, s22, v142
	v_med3_f32 v176, v177, s22, v142
	v_mov_b32_e32 v131, v137
	v_cvt_pk_fp8_f32 v131, v140, v176
	v_med3_f32 v178, v180, s22, v142
	v_med3_f32 v179, v181, s22, v142
	v_med3_f32 v140, v174, s22, v142
	v_med3_f32 v174, v175, s22, v142
	v_cvt_pk_fp8_f32 v130, v178, v179 op_sel:[0,0,1]
	v_cvt_pk_fp8_f32 v131, v140, v174 op_sel:[0,0,1]
	v_or_b32_e32 v174, 1, v206
	v_ashrrev_i32_e32 v175, 31, v174
	v_lshlrev_b64 v[174:175], 10, v[174:175]
	v_lshl_add_u64 v[174:175], v[138:139], 0, v[174:175]
	global_store_dwordx4 v[174:175], v[128:131], off nt
	v_med3_f32 v140, v157, s22, v142
	s_nop 0
	v_med3_f32 v128, v170, s22, v142
	v_med3_f32 v129, v171, s22, v142
	v_mov_b32_e32 v170, v137
	v_cvt_pk_fp8_f32 v170, v128, v129
	v_med3_f32 v128, v168, s22, v142
	v_med3_f32 v129, v169, s22, v142
	v_mov_b32_e32 v171, v137
	v_cvt_pk_fp8_f32 v171, v128, v129
	v_med3_f32 v128, v166, s22, v142
	v_med3_f32 v129, v167, s22, v142
	v_med3_f32 v130, v172, s22, v142
	v_cvt_pk_fp8_f32 v171, v128, v129 op_sel:[0,0,1]
	v_med3_f32 v128, v162, s22, v142
	v_med3_f32 v129, v163, s22, v142
	v_mov_b32_e32 v172, v137
	v_med3_f32 v131, v173, s22, v142
	v_cvt_pk_fp8_f32 v172, v128, v129
	v_med3_f32 v128, v160, s22, v142
	v_med3_f32 v129, v161, s22, v142
	v_mov_b32_e32 v173, v137
	v_cvt_pk_fp8_f32 v173, v128, v129
	v_med3_f32 v128, v158, s22, v142
	v_med3_f32 v129, v159, s22, v142
	v_cvt_pk_fp8_f32 v170, v130, v131 op_sel:[0,0,1]
	v_cvt_pk_fp8_f32 v173, v128, v129 op_sel:[0,0,1]
	v_or_b32_e32 v128, 2, v206
	v_med3_f32 v130, v164, s22, v142
	v_med3_f32 v131, v165, s22, v142
	v_ashrrev_i32_e32 v129, 31, v128
	v_cvt_pk_fp8_f32 v172, v130, v131 op_sel:[0,0,1]
	v_lshlrev_b64 v[158:159], 10, v[128:129]
	v_med3_f32 v129, v154, s22, v142
	v_med3_f32 v130, v155, s22, v142
	v_mov_b32_e32 v128, v137
	v_cvt_pk_fp8_f32 v128, v129, v130
	v_med3_f32 v130, v152, s22, v142
	v_med3_f32 v152, v153, s22, v142
	v_mov_b32_e32 v129, v137
	v_cvt_pk_fp8_f32 v129, v130, v152
	v_med3_f32 v131, v156, s22, v142
	v_cvt_pk_fp8_f32 v128, v131, v140 op_sel:[0,0,1]
	v_med3_f32 v130, v150, s22, v142
	v_med3_f32 v131, v151, s22, v142
	v_cvt_pk_fp8_f32 v129, v130, v131 op_sel:[0,0,1]
	v_med3_f32 v131, v146, s22, v142
	v_med3_f32 v140, v147, s22, v142
	v_mov_b32_e32 v130, v137
	v_cvt_pk_fp8_f32 v130, v131, v140
	v_med3_f32 v140, v144, s22, v142
	v_med3_f32 v144, v145, s22, v142
	v_mov_b32_e32 v131, v137
	v_cvt_pk_fp8_f32 v131, v140, v144
	v_med3_f32 v146, v148, s22, v142
	v_med3_f32 v147, v149, s22, v142
	v_med3_f32 v140, v141, s22, v142
	v_cvt_pk_fp8_f32 v130, v146, v147 op_sel:[0,0,1]
	v_cvt_pk_fp8_f32 v131, v136, v140 op_sel:[0,0,1]
	v_lshl_add_u64 v[140:141], v[138:139], 0, v[158:159]
	global_store_dwordx4 v[140:141], v[170:173], off nt
	v_or_b32_e32 v140, 3, v206
.LBB0_985:
	v_ashrrev_i32_e32 v141, 31, v140
	v_lshlrev_b64 v[140:141], 10, v[140:141]
	v_lshl_add_u64 v[138:139], v[138:139], 0, v[140:141]
	s_andn2_b64 vcc, exec, s[6:7]
	s_mov_b64 s[6:7], -1
	global_store_dwordx4 v[138:139], v[128:131], off nt
	s_cbranch_vccnz .LBB0_976
	s_add_i32 s24, s19, 0x200
	s_cmpk_gt_i32 s19, 0x5ff
	s_cselect_b64 s[6:7], -1, 0
	s_and_b64 vcc, exec, s[6:7]
	s_cbranch_vccnz .LBB0_988
	s_ashr_i32 s25, s24, 31
	s_lshr_b32 s8, s25, 24
	s_add_i32 s28, s24, s8
	s_ashr_i32 s8, s28, 8
	s_lshr_b32 s9, s28, 31
	s_add_i32 s9, s8, s9
	s_and_b32 s9, s9, -2
	s_sub_i32 s8, s8, s9
	s_cmp_eq_u32 s8, 1
	s_cselect_b32 s9, s10, 0x118
	s_cmp_lg_u32 s8, 0
	s_cselect_b32 s8, s9, 0xf8
	s_add_u32 s8, s2, s8
	s_addc_u32 s9, s3, 0
	s_load_dwordx2 s[8:9], s[8:9], 0x0
	s_lshr_b32 s25, s25, 23
	s_add_i32 s25, s24, s25
	s_ashr_i32 s26, s25, 9
	s_ashr_i32 s27, s26, 31
	s_lshl_b64 s[26:27], s[26:27], 22
	s_waitcnt lgkmcnt(0)
	s_add_u32 s8, s8, s26
	s_addc_u32 s9, s9, s27
	s_and_b32 s25, s28, 0xff00
	s_sub_i32 s19, s19, s25
	s_addk_i32 s19, 0x200
	s_sext_i32_i16 s25, s19
	s_bfe_u32 s25, s25, 0x5001a
	s_add_i32 s25, s19, s25
	s_sext_i32_i16 s26, s25
	s_and_b32 s25, s25, 0xffe0
	s_sub_i32 s19, s19, s25
	s_lshl_b32 s25, s26, 2
	s_and_b32 s25, s25, 0xffffff80
	v_add_u32_e32 v0, s25, v132
	s_sext_i32_i16 s19, s19
	v_ashrrev_i32_e32 v1, 31, v0
	s_lshl_b32 s26, s19, 5
	v_lshlrev_b64 v[0:1], 12, v[0:1]
	v_lshl_add_u64 v[0:1], s[8:9], 0, v[0:1]
	s_ashr_i32 s27, s26, 31
	v_lshl_add_u64 v[0:1], s[26:27], 2, v[0:1]
	v_lshlrev_b32_e32 v136, 2, v134
	v_lshl_add_u64 v[88:89], v[0:1], 0, v[136:137]
	v_add_co_u32_e32 v8, vcc, s11, v88
	s_nop 1
	v_addc_co_u32_e32 v9, vcc, 0, v89, vcc
	v_add_co_u32_e32 v16, vcc, s12, v88
	global_load_dwordx4 v[0:3], v[8:9], off offset:-4096 nt
	global_load_dwordx4 v[4:7], v[8:9], off nt
	v_addc_co_u32_e32 v17, vcc, 0, v89, vcc
	v_add_co_u32_e32 v24, vcc, s13, v88
	global_load_dwordx4 v[8:11], v[16:17], off offset:-4096 nt
	global_load_dwordx4 v[12:15], v[16:17], off nt
	v_addc_co_u32_e32 v25, vcc, 0, v89, vcc
	v_add_co_u32_e32 v32, vcc, s14, v88
	global_load_dwordx4 v[16:19], v[24:25], off offset:-4096 nt
	global_load_dwordx4 v[20:23], v[24:25], off nt
	v_addc_co_u32_e32 v33, vcc, 0, v89, vcc
	v_add_co_u32_e32 v40, vcc, s15, v88
	global_load_dwordx4 v[24:27], v[32:33], off offset:-4096 nt
	global_load_dwordx4 v[28:31], v[32:33], off nt
	v_addc_co_u32_e32 v41, vcc, 0, v89, vcc
	v_add_co_u32_e32 v48, vcc, s16, v88
	global_load_dwordx4 v[32:35], v[40:41], off offset:-4096 nt
	global_load_dwordx4 v[36:39], v[40:41], off nt
	v_addc_co_u32_e32 v49, vcc, 0, v89, vcc
	global_load_dwordx4 v[40:43], v[48:49], off offset:-4096 nt
	global_load_dwordx4 v[44:47], v[48:49], off nt
	v_add_co_u32_e32 v48, vcc, s17, v88
	s_nop 1
	v_addc_co_u32_e32 v49, vcc, 0, v89, vcc
	v_add_co_u32_e32 v60, vcc, 0xc80d000, v88
	s_nop 1
	v_addc_co_u32_e32 v61, vcc, 0, v89, vcc
	v_add_co_u32_e32 v90, vcc, 0xc80e000, v88
	global_load_dwordx4 v[48:51], v[48:49], off nt
	s_nop 0
	global_load_dwordx4 v[60:63], v[60:61], off nt
	v_addc_co_u32_e32 v91, vcc, 0, v89, vcc
	v_add_co_u32_e32 v100, vcc, 0xc80f000, v88
	s_nop 1
	v_addc_co_u32_e32 v101, vcc, 0, v89, vcc
	global_load_dwordx4 v[88:91], v[90:91], off nt
	s_nop 0
	global_load_dwordx4 v[100:103], v[100:101], off nt
.LBB0_988:
	s_ashr_i32 s8, s23, 31
	s_lshr_b32 s9, s8, 24
	s_add_i32 s9, s23, s9
	s_and_b32 s19, s9, 0xffffff00
	s_lshr_b32 s8, s8, 23
	s_ashr_i32 s25, s9, 8
	s_sub_i32 s19, s23, s19
	s_add_i32 s23, s23, s8
	s_lshr_b32 s9, s9, 31
	s_ashr_i32 s8, s23, 9
	s_add_i32 s9, s25, s9
	s_add_i32 s8, s8, 50
	s_and_b32 s9, s9, -2
	s_sub_i32 s26, s25, s9
	s_mul_hi_i32 s9, s8, 0x300000
	s_mul_i32 s8, s8, 0x300000
	s_add_u32 s23, s20, s8
	s_addc_u32 s25, s21, s9
	s_mov_b64 s[8:9], -1
	s_cmp_gt_i32 s26, 0
	v_mul_f32_e32 v202, 0x42000000, v56
	v_mul_f32_e32 v203, 0x42000000, v52
	v_mul_f32_e32 v204, 0x42000000, v68
	v_mul_f32_e32 v205, 0x42000000, v64
	v_mul_f32_e32 v200, 0x42000000, v76
	v_mul_f32_e32 v201, 0x42000000, v72
	v_mul_f32_e32 v198, 0x42000000, v84
	v_mul_f32_e32 v199, 0x42000000, v80
	v_mul_f32_e32 v194, 0x42000000, v96
	v_mul_f32_e32 v195, 0x42000000, v92
	v_mul_f32_e32 v196, 0x42000000, v108
	v_mul_f32_e32 v197, 0x42000000, v104
	v_mul_f32_e32 v192, 0x42000000, v112
	v_mul_f32_e32 v193, 0x42000000, v116
	v_mul_f32_e32 v190, 0x42000000, v120
	v_mul_f32_e32 v191, 0x42000000, v124
	v_mul_f32_e32 v186, 0x42000000, v57
	v_mul_f32_e32 v187, 0x42000000, v53
	v_mul_f32_e32 v188, 0x42000000, v69
	v_mul_f32_e32 v189, 0x42000000, v65
	v_mul_f32_e32 v184, 0x42000000, v77
	v_mul_f32_e32 v185, 0x42000000, v73
	v_mul_f32_e32 v182, 0x42000000, v85
	v_mul_f32_e32 v183, 0x42000000, v81
	v_mul_f32_e32 v178, 0x42000000, v97
	v_mul_f32_e32 v179, 0x42000000, v93
	v_mul_f32_e32 v180, 0x42000000, v109
	v_mul_f32_e32 v181, 0x42000000, v105
	v_mul_f32_e32 v176, 0x42000000, v113
	v_mul_f32_e32 v177, 0x42000000, v117
	v_mul_f32_e32 v174, 0x42000000, v121
	v_mul_f32_e32 v175, 0x42000000, v125
	v_mul_f32_e32 v170, 0x42000000, v58
	v_mul_f32_e32 v171, 0x42000000, v54
	v_mul_f32_e32 v172, 0x42000000, v70
	v_mul_f32_e32 v173, 0x42000000, v66
	v_mul_f32_e32 v168, 0x42000000, v78
	v_mul_f32_e32 v169, 0x42000000, v74
	v_mul_f32_e32 v166, 0x42000000, v86
	v_mul_f32_e32 v167, 0x42000000, v82
	v_mul_f32_e32 v162, 0x42000000, v98
	v_mul_f32_e32 v163, 0x42000000, v94
	v_mul_f32_e32 v164, 0x42000000, v110
	v_mul_f32_e32 v165, 0x42000000, v106
	v_mul_f32_e32 v160, 0x42000000, v114
	v_mul_f32_e32 v161, 0x42000000, v118
	v_mul_f32_e32 v158, 0x42000000, v122
	v_mul_f32_e32 v159, 0x42000000, v126
	v_mul_f32_e32 v154, 0x42000000, v59
	v_mul_f32_e32 v155, 0x42000000, v55
	v_mul_f32_e32 v156, 0x42000000, v71
	v_mul_f32_e32 v157, 0x42000000, v67
	v_mul_f32_e32 v152, 0x42000000, v79
	v_mul_f32_e32 v153, 0x42000000, v75
	v_mul_f32_e32 v150, 0x42000000, v87
	v_mul_f32_e32 v151, 0x42000000, v83
	v_mul_f32_e32 v146, 0x42000000, v99
	v_mul_f32_e32 v147, 0x42000000, v95
	v_mul_f32_e32 v148, 0x42000000, v111
	v_mul_f32_e32 v149, 0x42000000, v107
	v_mul_f32_e32 v144, 0x42000000, v115
	v_mul_f32_e32 v145, 0x42000000, v119
	v_mul_f32_e32 v136, 0x42000000, v123
	v_mul_f32_e32 v141, 0x42000000, v127
	s_cbranch_scc0 .LBB0_990
	v_med3_f32 v129, v202, s22, v142
	v_med3_f32 v130, v203, s22, v142
	v_mov_b32_e32 v128, v137
	v_cvt_pk_fp8_f32 v128, v129, v130
	v_med3_f32 v130, v200, s22, v142
	v_med3_f32 v207, v201, s22, v142
	v_mov_b32_e32 v129, v137
	v_cvt_pk_fp8_f32 v129, v130, v207
	s_bfe_u32 s8, s19, 0x5001a
	s_add_i32 s8, s19, s8
	v_med3_f32 v131, v204, s22, v142
	v_med3_f32 v206, v205, s22, v142
	s_sext_i32_i16 s9, s8
	s_and_b32 s8, s8, 0xffe0
	v_cvt_pk_fp8_f32 v128, v131, v206 op_sel:[0,0,1]
	v_med3_f32 v130, v198, s22, v142
	v_med3_f32 v131, v199, s22, v142
	s_sub_i32 s8, s19, s8
	v_cvt_pk_fp8_f32 v129, v130, v131 op_sel:[0,0,1]
	v_med3_f32 v131, v194, s22, v142
	v_med3_f32 v206, v195, s22, v142
	v_mov_b32_e32 v130, v137
	s_sext_i32_i16 s8, s8
	v_cvt_pk_fp8_f32 v130, v131, v206
	v_med3_f32 v206, v192, s22, v142
	v_med3_f32 v209, v193, s22, v142
	v_mov_b32_e32 v131, v137
	s_lshl_b32 s27, s8, 5
	s_lshl_b32 s8, s8, 6
	v_cvt_pk_fp8_f32 v131, v206, v209
	s_lshl_b32 s9, s9, 2
	s_and_b32 s8, s8, 0xffffff00
	s_and_b32 s27, s27, 0x60
	s_and_b32 s9, s9, 0xffffff80
	s_or_b32 s8, s27, s8
	v_med3_f32 v207, v196, s22, v142
	v_med3_f32 v208, v197, s22, v142
	v_or_b32_e32 v140, s8, v134
	s_ashr_i32 s27, s9, 31
	v_cvt_pk_fp8_f32 v130, v207, v208 op_sel:[0,0,1]
	v_med3_f32 v206, v190, s22, v142
	v_med3_f32 v207, v191, s22, v142
	s_add_u32 s8, s23, s9
	v_cvt_pk_fp8_f32 v131, v206, v207 op_sel:[0,0,1]
	v_or_b32_e32 v206, 0x80, v140
	s_addc_u32 s9, s25, s27
	v_ashrrev_i32_e32 v207, 31, v206
	v_lshl_add_u64 v[138:139], s[8:9], 0, v[132:133]
	v_lshlrev_b64 v[206:207], 10, v[206:207]
	v_lshl_add_u64 v[206:207], v[138:139], 0, v[206:207]
	global_store_dwordx4 v[206:207], v[128:131], off nt
	v_med3_f32 v207, v185, s22, v142
	v_med3_f32 v206, v189, s22, v142
	v_med3_f32 v129, v186, s22, v142
	v_med3_f32 v130, v187, s22, v142
	v_mov_b32_e32 v128, v137
	v_cvt_pk_fp8_f32 v128, v129, v130
	v_med3_f32 v130, v184, s22, v142
	v_mov_b32_e32 v129, v137
	v_cvt_pk_fp8_f32 v129, v130, v207
	v_med3_f32 v131, v188, s22, v142
	v_cvt_pk_fp8_f32 v128, v131, v206 op_sel:[0,0,1]
	v_med3_f32 v130, v182, s22, v142
	v_med3_f32 v131, v183, s22, v142
	v_cvt_pk_fp8_f32 v129, v130, v131 op_sel:[0,0,1]
	v_med3_f32 v131, v178, s22, v142
	v_med3_f32 v206, v179, s22, v142
	v_mov_b32_e32 v130, v137
	v_cvt_pk_fp8_f32 v130, v131, v206
	v_med3_f32 v206, v176, s22, v142
	v_med3_f32 v209, v177, s22, v142
	v_mov_b32_e32 v131, v137
	v_cvt_pk_fp8_f32 v131, v206, v209
	v_med3_f32 v207, v180, s22, v142
	v_med3_f32 v208, v181, s22, v142
	v_cvt_pk_fp8_f32 v130, v207, v208 op_sel:[0,0,1]
	v_med3_f32 v206, v174, s22, v142
	v_med3_f32 v207, v175, s22, v142
	v_cvt_pk_fp8_f32 v131, v206, v207 op_sel:[0,0,1]
	v_or_b32_e32 v206, 0x81, v140
	v_ashrrev_i32_e32 v207, 31, v206
	v_lshlrev_b64 v[206:207], 10, v[206:207]
	v_lshl_add_u64 v[206:207], v[138:139], 0, v[206:207]
	global_store_dwordx4 v[206:207], v[128:131], off nt
	v_mov_b32_e32 v206, v137
	v_mov_b32_e32 v207, v137
	v_med3_f32 v128, v170, s22, v142
	v_med3_f32 v129, v171, s22, v142
	v_cvt_pk_fp8_f32 v206, v128, v129
	v_med3_f32 v128, v168, s22, v142
	v_med3_f32 v129, v169, s22, v142
	v_cvt_pk_fp8_f32 v207, v128, v129
	v_med3_f32 v128, v166, s22, v142
	v_med3_f32 v129, v167, s22, v142
	v_mov_b32_e32 v208, v137
	v_cvt_pk_fp8_f32 v207, v128, v129 op_sel:[0,0,1]
	v_med3_f32 v128, v162, s22, v142
	v_med3_f32 v129, v163, s22, v142
	v_cvt_pk_fp8_f32 v208, v128, v129
	v_med3_f32 v128, v160, s22, v142
	v_med3_f32 v129, v161, s22, v142
	v_mov_b32_e32 v209, v137
	v_cvt_pk_fp8_f32 v209, v128, v129
	v_med3_f32 v128, v158, s22, v142
	v_med3_f32 v129, v159, s22, v142
	v_med3_f32 v130, v172, s22, v142
	v_cvt_pk_fp8_f32 v209, v128, v129 op_sel:[0,0,1]
	v_or_b32_e32 v128, 0x82, v140
	v_med3_f32 v131, v173, s22, v142
	v_ashrrev_i32_e32 v129, 31, v128
	v_cvt_pk_fp8_f32 v206, v130, v131 op_sel:[0,0,1]
	v_med3_f32 v130, v164, s22, v142
	v_med3_f32 v131, v165, s22, v142
	v_lshlrev_b64 v[128:129], 10, v[128:129]
	v_cvt_pk_fp8_f32 v208, v130, v131 op_sel:[0,0,1]
	v_lshl_add_u64 v[210:211], v[138:139], 0, v[128:129]
	v_med3_f32 v129, v154, s22, v142
	v_med3_f32 v130, v155, s22, v142
	v_mov_b32_e32 v128, v137
	v_cvt_pk_fp8_f32 v128, v129, v130
	v_med3_f32 v130, v152, s22, v142
	v_med3_f32 v213, v153, s22, v142
	v_mov_b32_e32 v129, v137
	v_cvt_pk_fp8_f32 v129, v130, v213
	v_med3_f32 v131, v156, s22, v142
	v_med3_f32 v212, v157, s22, v142
	v_cvt_pk_fp8_f32 v128, v131, v212 op_sel:[0,0,1]
	v_med3_f32 v130, v150, s22, v142
	v_med3_f32 v131, v151, s22, v142
	v_cvt_pk_fp8_f32 v129, v130, v131 op_sel:[0,0,1]
	v_med3_f32 v131, v146, s22, v142
	v_med3_f32 v212, v147, s22, v142
	v_mov_b32_e32 v130, v137
	v_cvt_pk_fp8_f32 v130, v131, v212
	v_med3_f32 v212, v144, s22, v142
	v_med3_f32 v215, v145, s22, v142
	v_mov_b32_e32 v131, v137
	v_cvt_pk_fp8_f32 v131, v212, v215
	v_med3_f32 v213, v148, s22, v142
	v_med3_f32 v214, v149, s22, v142
	v_cvt_pk_fp8_f32 v130, v213, v214 op_sel:[0,0,1]
	v_med3_f32 v212, v136, s22, v142
	v_med3_f32 v213, v141, s22, v142
	v_cvt_pk_fp8_f32 v131, v212, v213 op_sel:[0,0,1]
	global_store_dwordx4 v[210:211], v[206:209], off nt
	v_or_b32_e32 v140, 0x83, v140
	s_mov_b64 s[8:9], 0
.LBB0_990:
	s_andn2_b64 vcc, exec, s[8:9]
	s_cbranch_vccnz .LBB0_975
	s_cmp_lg_u32 s26, 0
	s_cbranch_scc0 .LBB0_994
	s_bfe_u32 s8, s19, 0x5001a
	s_add_i32 s8, s19, s8
	s_sext_i32_i16 s9, s8
	s_and_b32 s8, s8, 0xffe0
	s_sub_i32 s8, s19, s8
	s_sext_i32_i16 s8, s8
	s_lshl_b32 s9, s9, 2
	s_and_b32 s9, s9, 0xffffff80
	s_lshl_b32 s8, s8, 5
	v_or_b32_e32 v128, s8, v134
	s_ashr_i32 s26, s9, 31
	v_lshlrev_b32_e32 v129, 4, v134
	v_lshrrev_b32_e32 v128, 1, v128
	v_bitop3_b32 v130, s8, v143, v134 bitop3:0xc8
	s_add_u32 s8, s23, s9
	v_and_b32_e32 v129, 0x80, v129
	v_and_b32_e32 v128, 0x78, v128
	s_addc_u32 s9, s25, s26
	v_or3_b32 v210, v129, v130, v128
	v_lshl_add_u64 v[128:129], s[8:9], 0, v[132:133]
	v_lshl_add_u64 v[138:139], v[128:129], 0, s[4:5]
	v_med3_f32 v129, v202, s22, v142
	v_med3_f32 v130, v203, s22, v142
	v_mov_b32_e32 v128, v137
	v_cvt_pk_fp8_f32 v128, v129, v130
	v_med3_f32 v130, v200, s22, v142
	v_med3_f32 v206, v201, s22, v142
	v_mov_b32_e32 v129, v137
	v_cvt_pk_fp8_f32 v129, v130, v206
	v_med3_f32 v131, v204, s22, v142
	v_med3_f32 v140, v205, s22, v142
	v_cvt_pk_fp8_f32 v128, v131, v140 op_sel:[0,0,1]
	v_med3_f32 v130, v198, s22, v142
	v_med3_f32 v131, v199, s22, v142
	v_cvt_pk_fp8_f32 v129, v130, v131 op_sel:[0,0,1]
	v_med3_f32 v131, v194, s22, v142
	v_med3_f32 v140, v195, s22, v142
	v_mov_b32_e32 v130, v137
	v_cvt_pk_fp8_f32 v130, v131, v140
	v_med3_f32 v140, v192, s22, v142
	v_med3_f32 v208, v193, s22, v142
	v_mov_b32_e32 v131, v137
	v_cvt_pk_fp8_f32 v131, v140, v208
	v_med3_f32 v206, v196, s22, v142
	v_med3_f32 v207, v197, s22, v142
	v_cvt_pk_fp8_f32 v130, v206, v207 op_sel:[0,0,1]
	v_med3_f32 v140, v190, s22, v142
	v_med3_f32 v206, v191, s22, v142
	v_cvt_pk_fp8_f32 v131, v140, v206 op_sel:[0,0,1]
	v_ashrrev_i32_e32 v211, 31, v210
	v_lshlrev_b64 v[206:207], 10, v[210:211]
	v_lshl_add_u64 v[206:207], v[138:139], 0, v[206:207]
	global_store_dwordx4 v[206:207], v[128:131], off nt
	v_med3_f32 v206, v185, s22, v142
	v_med3_f32 v140, v189, s22, v142
	v_med3_f32 v129, v186, s22, v142
	v_med3_f32 v130, v187, s22, v142
	v_mov_b32_e32 v128, v137
	v_cvt_pk_fp8_f32 v128, v129, v130
	v_med3_f32 v130, v184, s22, v142
	v_mov_b32_e32 v129, v137
	v_cvt_pk_fp8_f32 v129, v130, v206
	v_med3_f32 v131, v188, s22, v142
	v_cvt_pk_fp8_f32 v128, v131, v140 op_sel:[0,0,1]
	v_med3_f32 v130, v182, s22, v142
	v_med3_f32 v131, v183, s22, v142
	v_cvt_pk_fp8_f32 v129, v130, v131 op_sel:[0,0,1]
	v_med3_f32 v131, v178, s22, v142
	v_med3_f32 v140, v179, s22, v142
	v_mov_b32_e32 v130, v137
	v_cvt_pk_fp8_f32 v130, v131, v140
	v_med3_f32 v140, v176, s22, v142
	v_med3_f32 v208, v177, s22, v142
	v_mov_b32_e32 v131, v137
	v_cvt_pk_fp8_f32 v131, v140, v208
	v_med3_f32 v206, v180, s22, v142
	v_med3_f32 v207, v181, s22, v142
	v_cvt_pk_fp8_f32 v130, v206, v207 op_sel:[0,0,1]
	v_med3_f32 v140, v174, s22, v142
	v_med3_f32 v206, v175, s22, v142
	v_cvt_pk_fp8_f32 v131, v140, v206 op_sel:[0,0,1]
	v_or_b32_e32 v206, 1, v210
	v_ashrrev_i32_e32 v207, 31, v206
	v_lshlrev_b64 v[206:207], 10, v[206:207]
	v_lshl_add_u64 v[206:207], v[138:139], 0, v[206:207]
	global_store_dwordx4 v[206:207], v[128:131], off nt
	v_mov_b32_e32 v206, v137
	v_mov_b32_e32 v207, v137
	v_med3_f32 v128, v170, s22, v142
	v_med3_f32 v129, v171, s22, v142
	v_cvt_pk_fp8_f32 v206, v128, v129
	v_med3_f32 v128, v168, s22, v142
	v_med3_f32 v129, v169, s22, v142
	v_cvt_pk_fp8_f32 v207, v128, v129
	v_med3_f32 v128, v166, s22, v142
	v_med3_f32 v129, v167, s22, v142
	v_mov_b32_e32 v208, v137
	v_cvt_pk_fp8_f32 v207, v128, v129 op_sel:[0,0,1]
	v_med3_f32 v128, v162, s22, v142
	v_med3_f32 v129, v163, s22, v142
	v_cvt_pk_fp8_f32 v208, v128, v129
	v_med3_f32 v128, v160, s22, v142
	v_med3_f32 v129, v161, s22, v142
	v_mov_b32_e32 v209, v137
	v_cvt_pk_fp8_f32 v209, v128, v129
	v_med3_f32 v128, v158, s22, v142
	v_med3_f32 v129, v159, s22, v142
	v_med3_f32 v130, v172, s22, v142
	v_cvt_pk_fp8_f32 v209, v128, v129 op_sel:[0,0,1]
	v_or_b32_e32 v128, 2, v210
	v_med3_f32 v131, v173, s22, v142
	v_ashrrev_i32_e32 v129, 31, v128
	v_cvt_pk_fp8_f32 v206, v130, v131 op_sel:[0,0,1]
	v_med3_f32 v130, v164, s22, v142
	v_med3_f32 v131, v165, s22, v142
	v_lshlrev_b64 v[128:129], 10, v[128:129]
	v_cvt_pk_fp8_f32 v208, v130, v131 op_sel:[0,0,1]
	v_lshl_add_u64 v[212:213], v[138:139], 0, v[128:129]
	v_med3_f32 v129, v154, s22, v142
	v_med3_f32 v130, v155, s22, v142
	v_mov_b32_e32 v128, v137
	v_cvt_pk_fp8_f32 v128, v129, v130
	v_med3_f32 v130, v152, s22, v142
	v_med3_f32 v211, v153, s22, v142
	v_mov_b32_e32 v129, v137
	v_cvt_pk_fp8_f32 v129, v130, v211
	v_med3_f32 v131, v156, s22, v142
	v_med3_f32 v140, v157, s22, v142
	v_cvt_pk_fp8_f32 v128, v131, v140 op_sel:[0,0,1]
	v_med3_f32 v130, v150, s22, v142
	v_med3_f32 v131, v151, s22, v142
	v_cvt_pk_fp8_f32 v129, v130, v131 op_sel:[0,0,1]
	v_med3_f32 v131, v146, s22, v142
	v_med3_f32 v140, v147, s22, v142
	v_mov_b32_e32 v130, v137
	v_cvt_pk_fp8_f32 v130, v131, v140
	v_med3_f32 v140, v144, s22, v142
	v_med3_f32 v215, v145, s22, v142
	v_mov_b32_e32 v131, v137
	v_cvt_pk_fp8_f32 v131, v140, v215
	v_med3_f32 v211, v148, s22, v142
	v_med3_f32 v214, v149, s22, v142
	v_cvt_pk_fp8_f32 v130, v211, v214 op_sel:[0,0,1]
	v_med3_f32 v140, v136, s22, v142
	v_med3_f32 v211, v141, s22, v142
	v_cvt_pk_fp8_f32 v131, v140, v211 op_sel:[0,0,1]
	global_store_dwordx4 v[212:213], v[206:209], off nt
	v_or_b32_e32 v140, 3, v210
	s_cbranch_execnz .LBB0_975
	s_branch .LBB0_995

.LBB0_994:
.LBB0_995:
	v_med3_f32 v129, v202, s22, v142
	v_med3_f32 v130, v203, s22, v142
	v_mov_b32_e32 v128, v137
	v_cvt_pk_fp8_f32 v128, v129, v130
	v_med3_f32 v130, v200, s22, v142
	v_med3_f32 v200, v201, s22, v142
	v_mov_b32_e32 v129, v137
	v_cvt_pk_fp8_f32 v129, v130, v200
	s_bfe_u32 s8, s19, 0x5001a
	v_med3_f32 v131, v204, s22, v142
	v_med3_f32 v140, v205, s22, v142
	s_add_i32 s8, s19, s8
	v_cvt_pk_fp8_f32 v128, v131, v140 op_sel:[0,0,1]
	v_med3_f32 v130, v198, s22, v142
	v_med3_f32 v131, v199, s22, v142
	s_sext_i32_i16 s9, s8
	s_and_b32 s8, s8, 0xffe0
	v_cvt_pk_fp8_f32 v129, v130, v131 op_sel:[0,0,1]
	v_med3_f32 v131, v194, s22, v142
	v_med3_f32 v140, v195, s22, v142
	v_mov_b32_e32 v130, v137
	s_sub_i32 s8, s19, s8
	v_cvt_pk_fp8_f32 v130, v131, v140
	v_med3_f32 v140, v192, s22, v142
	v_med3_f32 v192, v193, s22, v142
	v_mov_b32_e32 v131, v137
	s_sext_i32_i16 s8, s8
	v_cvt_pk_fp8_f32 v131, v140, v192
	s_lshl_b32 s9, s9, 2
	s_lshl_b32 s19, s8, 5
	s_lshl_b32 s8, s8, 6
	s_and_b32 s9, s9, 0xffffff80
	s_and_b32 s8, s8, 0xffffff00
	s_and_b32 s19, s19, 0x60
	s_or_b32 s8, s19, s8
	s_ashr_i32 s19, s9, 31
	v_med3_f32 v194, v196, s22, v142
	v_med3_f32 v195, v197, s22, v142
	v_med3_f32 v140, v190, s22, v142
	v_med3_f32 v190, v191, s22, v142
	v_or_b32_e32 v206, s8, v134
	s_add_u32 s8, s23, s9
	v_cvt_pk_fp8_f32 v130, v194, v195 op_sel:[0,0,1]
	v_cvt_pk_fp8_f32 v131, v140, v190 op_sel:[0,0,1]
	s_addc_u32 s9, s25, s19
	v_ashrrev_i32_e32 v207, 31, v206
	v_lshl_add_u64 v[138:139], s[8:9], 0, v[132:133]
	v_lshlrev_b64 v[190:191], 10, v[206:207]
	v_lshl_add_u64 v[190:191], v[138:139], 0, v[190:191]
	global_store_dwordx4 v[190:191], v[128:131], off nt
	v_med3_f32 v140, v189, s22, v142
	v_med3_f32 v136, v136, s22, v142
	v_med3_f32 v129, v186, s22, v142
	v_med3_f32 v130, v187, s22, v142
	v_mov_b32_e32 v128, v137
	v_cvt_pk_fp8_f32 v128, v129, v130
	v_med3_f32 v130, v184, s22, v142
	v_med3_f32 v184, v185, s22, v142
	v_mov_b32_e32 v129, v137
	v_cvt_pk_fp8_f32 v129, v130, v184
	v_med3_f32 v131, v188, s22, v142
	v_cvt_pk_fp8_f32 v128, v131, v140 op_sel:[0,0,1]
	v_med3_f32 v130, v182, s22, v142
	v_med3_f32 v131, v183, s22, v142
	v_cvt_pk_fp8_f32 v129, v130, v131 op_sel:[0,0,1]
	v_med3_f32 v131, v178, s22, v142
	v_med3_f32 v140, v179, s22, v142
	v_mov_b32_e32 v130, v137
	v_cvt_pk_fp8_f32 v130, v131, v140
	v_med3_f32 v140, v176, s22, v142
	v_med3_f32 v176, v177, s22, v142
	v_mov_b32_e32 v131, v137
	v_cvt_pk_fp8_f32 v131, v140, v176
	v_med3_f32 v178, v180, s22, v142
	v_med3_f32 v179, v181, s22, v142
	v_med3_f32 v140, v174, s22, v142
	v_med3_f32 v174, v175, s22, v142
	v_cvt_pk_fp8_f32 v130, v178, v179 op_sel:[0,0,1]
	v_cvt_pk_fp8_f32 v131, v140, v174 op_sel:[0,0,1]
	v_or_b32_e32 v174, 1, v206
	v_ashrrev_i32_e32 v175, 31, v174
	v_lshlrev_b64 v[174:175], 10, v[174:175]
	v_lshl_add_u64 v[174:175], v[138:139], 0, v[174:175]
	global_store_dwordx4 v[174:175], v[128:131], off nt
	v_med3_f32 v140, v157, s22, v142
	s_nop 0
	v_med3_f32 v128, v170, s22, v142
	v_med3_f32 v129, v171, s22, v142
	v_mov_b32_e32 v170, v137
	v_cvt_pk_fp8_f32 v170, v128, v129
	v_med3_f32 v128, v168, s22, v142
	v_med3_f32 v129, v169, s22, v142
	v_mov_b32_e32 v171, v137
	v_cvt_pk_fp8_f32 v171, v128, v129
	v_med3_f32 v128, v166, s22, v142
	v_med3_f32 v129, v167, s22, v142
	v_med3_f32 v130, v172, s22, v142
	v_cvt_pk_fp8_f32 v171, v128, v129 op_sel:[0,0,1]
	v_med3_f32 v128, v162, s22, v142
	v_med3_f32 v129, v163, s22, v142
	v_mov_b32_e32 v172, v137
	v_med3_f32 v131, v173, s22, v142
	v_cvt_pk_fp8_f32 v172, v128, v129
	v_med3_f32 v128, v160, s22, v142
	v_med3_f32 v129, v161, s22, v142
	v_mov_b32_e32 v173, v137
	v_cvt_pk_fp8_f32 v173, v128, v129
	v_med3_f32 v128, v158, s22, v142
	v_med3_f32 v129, v159, s22, v142
	v_cvt_pk_fp8_f32 v170, v130, v131 op_sel:[0,0,1]
	v_cvt_pk_fp8_f32 v173, v128, v129 op_sel:[0,0,1]
	v_or_b32_e32 v128, 2, v206
	v_med3_f32 v130, v164, s22, v142
	v_med3_f32 v131, v165, s22, v142
	v_ashrrev_i32_e32 v129, 31, v128
	v_cvt_pk_fp8_f32 v172, v130, v131 op_sel:[0,0,1]
	v_lshlrev_b64 v[158:159], 10, v[128:129]
	v_med3_f32 v129, v154, s22, v142
	v_med3_f32 v130, v155, s22, v142
	v_mov_b32_e32 v128, v137
	v_cvt_pk_fp8_f32 v128, v129, v130
	v_med3_f32 v130, v152, s22, v142
	v_med3_f32 v152, v153, s22, v142
	v_mov_b32_e32 v129, v137
	v_cvt_pk_fp8_f32 v129, v130, v152
	v_med3_f32 v131, v156, s22, v142
	v_cvt_pk_fp8_f32 v128, v131, v140 op_sel:[0,0,1]
	v_med3_f32 v130, v150, s22, v142
	v_med3_f32 v131, v151, s22, v142
	v_cvt_pk_fp8_f32 v129, v130, v131 op_sel:[0,0,1]
	v_med3_f32 v131, v146, s22, v142
	v_med3_f32 v140, v147, s22, v142
	v_mov_b32_e32 v130, v137
	v_cvt_pk_fp8_f32 v130, v131, v140
	v_med3_f32 v140, v144, s22, v142
	v_med3_f32 v144, v145, s22, v142
	v_mov_b32_e32 v131, v137
	v_cvt_pk_fp8_f32 v131, v140, v144
	v_med3_f32 v146, v148, s22, v142
	v_med3_f32 v147, v149, s22, v142
	v_med3_f32 v140, v141, s22, v142
	v_cvt_pk_fp8_f32 v130, v146, v147 op_sel:[0,0,1]
	v_cvt_pk_fp8_f32 v131, v136, v140 op_sel:[0,0,1]
	v_lshl_add_u64 v[140:141], v[138:139], 0, v[158:159]
	global_store_dwordx4 v[140:141], v[170:173], off nt
	v_or_b32_e32 v140, 3, v206
	s_branch .LBB0_975

.LBB0_1097:
	s_lshl_b32 s22, s58, 8
	s_or_b32 s22, s22, s50
	v_or_b32_e32 v0, s22, v0
	v_lshl_add_u32 v2, v0, 2, 0
	v_add_u32_e32 v10, 0x21000, v2
	ds_read_b128 v[2:5], v10
	ds_read_b128 v[6:9], v10 offset:16
	ds_read_b128 v[20:23], v10 offset:32
	ds_read_b128 v[24:27], v10 offset:48
	v_or_b32_e32 v18, s46, v1
	v_ashrrev_i32_e32 v1, 31, v0
	s_waitcnt lgkmcnt(0)
	v_pk_mul_f32 v[12:13], v[6:7], s[10:11] op_sel_hi:[1,0]
	v_pk_mul_f32 v[16:17], v[2:3], s[10:11] op_sel_hi:[1,0]
	v_pk_mul_f32 v[14:15], v[4:5], s[10:11] op_sel_hi:[1,0]
	v_pk_mul_f32 v[10:11], v[8:9], s[10:11] op_sel_hi:[1,0]
	v_pk_mul_f32 v[8:9], v[20:21], s[10:11] op_sel_hi:[1,0]
	v_pk_mul_f32 v[6:7], v[22:23], s[10:11] op_sel_hi:[1,0]
	v_pk_mul_f32 v[4:5], v[24:25], s[10:11] op_sel_hi:[1,0]
	v_pk_mul_f32 v[2:3], v[26:27], s[10:11] op_sel_hi:[1,0]
	v_cmp_gt_i32_e32 vcc, s56, v18
	s_and_saveexec_b64 s[22:23], vcc
	s_cbranch_execz .LBB0_1099
	v_pk_fma_f32 v[20:21], v[148:149], s[12:13], v[16:17] op_sel_hi:[1,0,1]
	v_pk_fma_f32 v[22:23], v[150:151], s[12:13], v[14:15] op_sel_hi:[1,0,1]
	v_med3_f32 v19, v20, s54, v170
	v_med3_f32 v21, v21, s54, v170
	v_mov_b32_e32 v20, 0
	v_cvt_pk_fp8_f32 v20, v19, v21
	v_med3_f32 v19, v22, s54, v170
	v_med3_f32 v21, v23, s54, v170
	v_pk_fma_f32 v[22:23], v[144:145], s[12:13], v[12:13] op_sel_hi:[1,0,1]
	v_cvt_pk_fp8_f32 v20, v19, v21 op_sel:[0,0,1]
	v_med3_f32 v19, v22, s54, v170
	v_med3_f32 v22, v23, s54, v170
	v_mov_b32_e32 v21, 0
	v_cvt_pk_fp8_f32 v21, v19, v22
	v_pk_fma_f32 v[22:23], v[146:147], s[12:13], v[10:11] op_sel_hi:[1,0,1]
	v_pk_fma_f32 v[24:25], v[158:159], s[12:13], v[6:7] op_sel_hi:[1,0,1]
	v_med3_f32 v19, v22, s54, v170
	v_med3_f32 v22, v23, s54, v170
	v_cvt_pk_fp8_f32 v21, v19, v22 op_sel:[0,0,1]
	v_pk_fma_f32 v[22:23], v[156:157], s[12:13], v[8:9] op_sel_hi:[1,0,1]
	s_nop 0
	v_med3_f32 v19, v22, s54, v170
	v_med3_f32 v23, v23, s54, v170
	v_mov_b32_e32 v22, 0
	v_cvt_pk_fp8_f32 v22, v19, v23
	v_med3_f32 v19, v24, s54, v170
	v_med3_f32 v23, v25, s54, v170
	v_pk_fma_f32 v[24:25], v[152:153], s[12:13], v[4:5] op_sel_hi:[1,0,1]
	v_cvt_pk_fp8_f32 v22, v19, v23 op_sel:[0,0,1]
	v_med3_f32 v19, v24, s54, v170
	v_med3_f32 v24, v25, s54, v170
	v_mov_b32_e32 v23, 0
	v_cvt_pk_fp8_f32 v23, v19, v24
	v_pk_fma_f32 v[24:25], v[154:155], s[12:13], v[2:3] op_sel_hi:[1,0,1]
	s_nop 0
	v_med3_f32 v19, v24, s54, v170
	v_med3_f32 v24, v25, s54, v170
	v_cvt_pk_fp8_f32 v23, v19, v24 op_sel:[0,0,1]
	v_add_u32_e32 v24, s55, v18
	v_ashrrev_i32_e32 v25, 31, v24
	v_lshlrev_b64 v[24:25], 10, v[24:25]
	v_lshl_add_u64 v[24:25], s[6:7], 0, v[24:25]
	v_lshl_add_u64 v[24:25], v[24:25], 0, v[0:1]
	global_store_dwordx4 v[24:25], v[20:23], off nt
.LBB0_1099:
	s_or_b64 exec, exec, s[22:23]
	v_or_b32_e32 v19, 16, v18
	v_cmp_gt_i32_e32 vcc, s56, v19
	s_and_saveexec_b64 s[22:23], vcc
	s_cbranch_execz .LBB0_1101
	v_pk_fma_f32 v[20:21], v[136:137], s[12:13], v[16:17] op_sel_hi:[1,0,1]
	s_nop 0
	v_med3_f32 v22, v20, s54, v170
	v_med3_f32 v21, v21, s54, v170
	v_mov_b32_e32 v20, 0
	v_cvt_pk_fp8_f32 v20, v22, v21
	v_pk_fma_f32 v[22:23], v[138:139], s[12:13], v[14:15] op_sel_hi:[1,0,1]
	s_nop 0
	v_med3_f32 v21, v22, s54, v170
	v_med3_f32 v22, v23, s54, v170
	v_cvt_pk_fp8_f32 v20, v21, v22 op_sel:[0,0,1]
	v_pk_fma_f32 v[22:23], v[128:129], s[12:13], v[12:13] op_sel_hi:[1,0,1]
	v_mov_b32_e32 v21, 0
	v_med3_f32 v22, v22, s54, v170
	v_med3_f32 v23, v23, s54, v170
	v_cvt_pk_fp8_f32 v21, v22, v23
	v_pk_fma_f32 v[22:23], v[130:131], s[12:13], v[10:11] op_sel_hi:[1,0,1]
	s_nop 0
	v_med3_f32 v22, v22, s54, v170
	v_med3_f32 v23, v23, s54, v170
	v_cvt_pk_fp8_f32 v21, v22, v23 op_sel:[0,0,1]
	v_pk_fma_f32 v[22:23], v[140:141], s[12:13], v[8:9] op_sel_hi:[1,0,1]
	s_nop 0
	v_med3_f32 v24, v22, s54, v170
	v_med3_f32 v23, v23, s54, v170
	v_mov_b32_e32 v22, 0
	v_cvt_pk_fp8_f32 v22, v24, v23
	v_pk_fma_f32 v[24:25], v[142:143], s[12:13], v[6:7] op_sel_hi:[1,0,1]
	s_nop 0
	v_med3_f32 v23, v24, s54, v170
	v_med3_f32 v24, v25, s54, v170
	v_cvt_pk_fp8_f32 v22, v23, v24 op_sel:[0,0,1]
	v_pk_fma_f32 v[24:25], v[132:133], s[12:13], v[4:5] op_sel_hi:[1,0,1]
	v_mov_b32_e32 v23, 0
	v_med3_f32 v24, v24, s54, v170
	v_med3_f32 v25, v25, s54, v170
	v_cvt_pk_fp8_f32 v23, v24, v25
	v_pk_fma_f32 v[24:25], v[134:135], s[12:13], v[2:3] op_sel_hi:[1,0,1]
	s_nop 0
	v_med3_f32 v24, v24, s54, v170
	v_med3_f32 v25, v25, s54, v170
	v_cvt_pk_fp8_f32 v23, v24, v25 op_sel:[0,0,1]
	v_add_u32_e32 v24, s55, v19
	v_ashrrev_i32_e32 v25, 31, v24
	v_lshlrev_b64 v[24:25], 10, v[24:25]
	v_lshl_add_u64 v[24:25], s[6:7], 0, v[24:25]
	v_lshl_add_u64 v[24:25], v[24:25], 0, v[0:1]
	global_store_dwordx4 v[24:25], v[20:23], off nt
.LBB0_1101:
	s_or_b64 exec, exec, s[22:23]
	v_or_b32_e32 v19, 32, v18
	v_cmp_gt_i32_e32 vcc, s56, v19
	s_and_saveexec_b64 s[22:23], vcc
	s_cbranch_execz .LBB0_1103
	v_pk_fma_f32 v[20:21], v[120:121], s[12:13], v[16:17] op_sel_hi:[1,0,1]
	s_nop 0
	v_med3_f32 v22, v20, s54, v170
	v_med3_f32 v21, v21, s54, v170
	v_mov_b32_e32 v20, 0
	v_cvt_pk_fp8_f32 v20, v22, v21
	v_pk_fma_f32 v[22:23], v[122:123], s[12:13], v[14:15] op_sel_hi:[1,0,1]
	s_nop 0
	v_med3_f32 v21, v22, s54, v170
	v_med3_f32 v22, v23, s54, v170
	v_cvt_pk_fp8_f32 v20, v21, v22 op_sel:[0,0,1]
	v_pk_fma_f32 v[22:23], v[112:113], s[12:13], v[12:13] op_sel_hi:[1,0,1]
	v_mov_b32_e32 v21, 0
	v_med3_f32 v22, v22, s54, v170
	v_med3_f32 v23, v23, s54, v170
	v_cvt_pk_fp8_f32 v21, v22, v23
	v_pk_fma_f32 v[22:23], v[114:115], s[12:13], v[10:11] op_sel_hi:[1,0,1]
	s_nop 0
	v_med3_f32 v22, v22, s54, v170
	v_med3_f32 v23, v23, s54, v170
	v_cvt_pk_fp8_f32 v21, v22, v23 op_sel:[0,0,1]
	v_pk_fma_f32 v[22:23], v[124:125], s[12:13], v[8:9] op_sel_hi:[1,0,1]
	s_nop 0
	v_med3_f32 v24, v22, s54, v170
	v_med3_f32 v23, v23, s54, v170
	v_mov_b32_e32 v22, 0
	v_cvt_pk_fp8_f32 v22, v24, v23
	v_pk_fma_f32 v[24:25], v[126:127], s[12:13], v[6:7] op_sel_hi:[1,0,1]
	s_nop 0
	v_med3_f32 v23, v24, s54, v170
	v_med3_f32 v24, v25, s54, v170
	v_cvt_pk_fp8_f32 v22, v23, v24 op_sel:[0,0,1]
	v_pk_fma_f32 v[24:25], v[116:117], s[12:13], v[4:5] op_sel_hi:[1,0,1]
	v_mov_b32_e32 v23, 0
	v_med3_f32 v24, v24, s54, v170
	v_med3_f32 v25, v25, s54, v170
	v_cvt_pk_fp8_f32 v23, v24, v25
	v_pk_fma_f32 v[24:25], v[118:119], s[12:13], v[2:3] op_sel_hi:[1,0,1]
	s_nop 0
	v_med3_f32 v24, v24, s54, v170
	v_med3_f32 v25, v25, s54, v170
	v_cvt_pk_fp8_f32 v23, v24, v25 op_sel:[0,0,1]
	v_add_u32_e32 v24, s55, v19
	v_ashrrev_i32_e32 v25, 31, v24
	v_lshlrev_b64 v[24:25], 10, v[24:25]
	v_lshl_add_u64 v[24:25], s[6:7], 0, v[24:25]
	v_lshl_add_u64 v[24:25], v[24:25], 0, v[0:1]
	global_store_dwordx4 v[24:25], v[20:23], off nt
.LBB0_1103:
	s_or_b64 exec, exec, s[22:23]
	v_or_b32_e32 v19, 48, v18
	v_cmp_gt_i32_e32 vcc, s56, v19
	s_and_saveexec_b64 s[22:23], vcc
	s_cbranch_execz .LBB0_1105
	v_pk_fma_f32 v[20:21], v[108:109], s[12:13], v[16:17] op_sel_hi:[1,0,1]
	s_nop 0
	v_med3_f32 v22, v20, s54, v170
	v_med3_f32 v21, v21, s54, v170
	v_mov_b32_e32 v20, 0
	v_cvt_pk_fp8_f32 v20, v22, v21
	v_pk_fma_f32 v[22:23], v[110:111], s[12:13], v[14:15] op_sel_hi:[1,0,1]
	s_nop 0
	v_med3_f32 v21, v22, s54, v170
	v_med3_f32 v22, v23, s54, v170
	v_cvt_pk_fp8_f32 v20, v21, v22 op_sel:[0,0,1]
	v_pk_fma_f32 v[22:23], v[92:93], s[12:13], v[12:13] op_sel_hi:[1,0,1]
	v_mov_b32_e32 v21, 0
	v_med3_f32 v22, v22, s54, v170
	v_med3_f32 v23, v23, s54, v170
	v_cvt_pk_fp8_f32 v21, v22, v23
	v_pk_fma_f32 v[22:23], v[94:95], s[12:13], v[10:11] op_sel_hi:[1,0,1]
	s_nop 0
	v_med3_f32 v22, v22, s54, v170
	v_med3_f32 v23, v23, s54, v170
	v_cvt_pk_fp8_f32 v21, v22, v23 op_sel:[0,0,1]
	v_pk_fma_f32 v[22:23], v[96:97], s[12:13], v[8:9] op_sel_hi:[1,0,1]
	s_nop 0
	v_med3_f32 v24, v22, s54, v170
	v_med3_f32 v23, v23, s54, v170
	v_mov_b32_e32 v22, 0
	v_cvt_pk_fp8_f32 v22, v24, v23
	v_pk_fma_f32 v[24:25], v[98:99], s[12:13], v[6:7] op_sel_hi:[1,0,1]
	s_nop 0
	v_med3_f32 v23, v24, s54, v170
	v_med3_f32 v24, v25, s54, v170
	v_cvt_pk_fp8_f32 v22, v23, v24 op_sel:[0,0,1]
	v_pk_fma_f32 v[24:25], v[80:81], s[12:13], v[4:5] op_sel_hi:[1,0,1]
	v_mov_b32_e32 v23, 0
	v_med3_f32 v24, v24, s54, v170
	v_med3_f32 v25, v25, s54, v170
	v_cvt_pk_fp8_f32 v23, v24, v25
	v_pk_fma_f32 v[24:25], v[82:83], s[12:13], v[2:3] op_sel_hi:[1,0,1]
	s_nop 0
	v_med3_f32 v24, v24, s54, v170
	v_med3_f32 v25, v25, s54, v170
	v_cvt_pk_fp8_f32 v23, v24, v25 op_sel:[0,0,1]
	v_add_u32_e32 v24, s55, v19
	v_ashrrev_i32_e32 v25, 31, v24
	v_lshlrev_b64 v[24:25], 10, v[24:25]
	v_lshl_add_u64 v[24:25], s[6:7], 0, v[24:25]
	v_lshl_add_u64 v[24:25], v[24:25], 0, v[0:1]
	global_store_dwordx4 v[24:25], v[20:23], off nt
.LBB0_1105:
	s_or_b64 exec, exec, s[22:23]
	v_add_u32_e32 v19, 0x80, v18
	v_cmp_gt_i32_e32 vcc, s56, v19
	s_and_saveexec_b64 s[22:23], vcc
	s_cbranch_execz .LBB0_1107
	v_pk_fma_f32 v[20:21], v[100:101], s[12:13], v[16:17] op_sel_hi:[1,0,1]
	s_nop 0
	v_med3_f32 v22, v20, s54, v170
	v_med3_f32 v21, v21, s54, v170
	v_mov_b32_e32 v20, 0
	v_cvt_pk_fp8_f32 v20, v22, v21
	v_pk_fma_f32 v[22:23], v[102:103], s[12:13], v[14:15] op_sel_hi:[1,0,1]
	s_nop 0
	v_med3_f32 v21, v22, s54, v170
	v_med3_f32 v22, v23, s54, v170
	v_cvt_pk_fp8_f32 v20, v21, v22 op_sel:[0,0,1]
	v_pk_fma_f32 v[22:23], v[84:85], s[12:13], v[12:13] op_sel_hi:[1,0,1]
	v_mov_b32_e32 v21, 0
	v_med3_f32 v22, v22, s54, v170
	v_med3_f32 v23, v23, s54, v170
	v_cvt_pk_fp8_f32 v21, v22, v23
	v_pk_fma_f32 v[22:23], v[86:87], s[12:13], v[10:11] op_sel_hi:[1,0,1]
	s_nop 0
	v_med3_f32 v22, v22, s54, v170
	v_med3_f32 v23, v23, s54, v170
	v_cvt_pk_fp8_f32 v21, v22, v23 op_sel:[0,0,1]
	v_pk_fma_f32 v[22:23], v[104:105], s[12:13], v[8:9] op_sel_hi:[1,0,1]
	s_nop 0
	v_med3_f32 v24, v22, s54, v170
	v_med3_f32 v23, v23, s54, v170
	v_mov_b32_e32 v22, 0
	v_cvt_pk_fp8_f32 v22, v24, v23
	v_pk_fma_f32 v[24:25], v[106:107], s[12:13], v[6:7] op_sel_hi:[1,0,1]
	s_nop 0
	v_med3_f32 v23, v24, s54, v170
	v_med3_f32 v24, v25, s54, v170
	v_cvt_pk_fp8_f32 v22, v23, v24 op_sel:[0,0,1]
	v_pk_fma_f32 v[24:25], v[88:89], s[12:13], v[4:5] op_sel_hi:[1,0,1]
	v_mov_b32_e32 v23, 0
	v_med3_f32 v24, v24, s54, v170
	v_med3_f32 v25, v25, s54, v170
	v_cvt_pk_fp8_f32 v23, v24, v25
	v_pk_fma_f32 v[24:25], v[90:91], s[12:13], v[2:3] op_sel_hi:[1,0,1]
	s_nop 0
	v_med3_f32 v24, v24, s54, v170
	v_med3_f32 v25, v25, s54, v170
	v_cvt_pk_fp8_f32 v23, v24, v25 op_sel:[0,0,1]
	v_add_u32_e32 v24, s55, v19
	v_ashrrev_i32_e32 v25, 31, v24
	v_lshlrev_b64 v[24:25], 10, v[24:25]
	v_lshl_add_u64 v[24:25], s[6:7], 0, v[24:25]
	v_lshl_add_u64 v[24:25], v[24:25], 0, v[0:1]
	global_store_dwordx4 v[24:25], v[20:23], off nt
.LBB0_1107:
	s_or_b64 exec, exec, s[22:23]
	v_add_u32_e32 v19, 0x90, v18
	v_cmp_gt_i32_e32 vcc, s56, v19
	s_and_saveexec_b64 s[22:23], vcc
	s_cbranch_execz .LBB0_1109
	v_pk_fma_f32 v[20:21], v[76:77], s[12:13], v[16:17] op_sel_hi:[1,0,1]
	s_nop 0
	v_med3_f32 v22, v20, s54, v170
	v_med3_f32 v21, v21, s54, v170
	v_mov_b32_e32 v20, 0
	v_cvt_pk_fp8_f32 v20, v22, v21
	v_pk_fma_f32 v[22:23], v[78:79], s[12:13], v[14:15] op_sel_hi:[1,0,1]
	s_nop 0
	v_med3_f32 v21, v22, s54, v170
	v_med3_f32 v22, v23, s54, v170
	v_cvt_pk_fp8_f32 v20, v21, v22 op_sel:[0,0,1]
	v_pk_fma_f32 v[22:23], v[68:69], s[12:13], v[12:13] op_sel_hi:[1,0,1]
	v_mov_b32_e32 v21, 0
	v_med3_f32 v22, v22, s54, v170
	v_med3_f32 v23, v23, s54, v170
	v_cvt_pk_fp8_f32 v21, v22, v23
	v_pk_fma_f32 v[22:23], v[70:71], s[12:13], v[10:11] op_sel_hi:[1,0,1]
	s_nop 0
	v_med3_f32 v22, v22, s54, v170
	v_med3_f32 v23, v23, s54, v170
	v_cvt_pk_fp8_f32 v21, v22, v23 op_sel:[0,0,1]
	v_pk_fma_f32 v[22:23], v[72:73], s[12:13], v[8:9] op_sel_hi:[1,0,1]
	s_nop 0
	v_med3_f32 v24, v22, s54, v170
	v_med3_f32 v23, v23, s54, v170
	v_mov_b32_e32 v22, 0
	v_cvt_pk_fp8_f32 v22, v24, v23
	v_pk_fma_f32 v[24:25], v[74:75], s[12:13], v[6:7] op_sel_hi:[1,0,1]
	s_nop 0
	v_med3_f32 v23, v24, s54, v170
	v_med3_f32 v24, v25, s54, v170
	v_cvt_pk_fp8_f32 v22, v23, v24 op_sel:[0,0,1]
	v_pk_fma_f32 v[24:25], v[64:65], s[12:13], v[4:5] op_sel_hi:[1,0,1]
	v_mov_b32_e32 v23, 0
	v_med3_f32 v24, v24, s54, v170
	v_med3_f32 v25, v25, s54, v170
	v_cvt_pk_fp8_f32 v23, v24, v25
	v_pk_fma_f32 v[24:25], v[66:67], s[12:13], v[2:3] op_sel_hi:[1,0,1]
	s_nop 0
	v_med3_f32 v24, v24, s54, v170
	v_med3_f32 v25, v25, s54, v170
	v_cvt_pk_fp8_f32 v23, v24, v25 op_sel:[0,0,1]
	v_add_u32_e32 v24, s55, v19
	v_ashrrev_i32_e32 v25, 31, v24
	v_lshlrev_b64 v[24:25], 10, v[24:25]
	v_lshl_add_u64 v[24:25], s[6:7], 0, v[24:25]
	v_lshl_add_u64 v[24:25], v[24:25], 0, v[0:1]
	global_store_dwordx4 v[24:25], v[20:23], off nt
.LBB0_1109:
	s_or_b64 exec, exec, s[22:23]
	v_add_u32_e32 v19, 0xa0, v18
	v_cmp_gt_i32_e32 vcc, s56, v19
	s_and_saveexec_b64 s[22:23], vcc
	s_cbranch_execz .LBB0_1111
	v_pk_fma_f32 v[20:21], v[60:61], s[12:13], v[16:17] op_sel_hi:[1,0,1]
	s_nop 0
	v_med3_f32 v22, v20, s54, v170
	v_med3_f32 v21, v21, s54, v170
	v_mov_b32_e32 v20, 0
	v_cvt_pk_fp8_f32 v20, v22, v21
	v_pk_fma_f32 v[22:23], v[62:63], s[12:13], v[14:15] op_sel_hi:[1,0,1]
	s_nop 0
	v_med3_f32 v21, v22, s54, v170
	v_med3_f32 v22, v23, s54, v170
	v_cvt_pk_fp8_f32 v20, v21, v22 op_sel:[0,0,1]
	v_pk_fma_f32 v[22:23], v[52:53], s[12:13], v[12:13] op_sel_hi:[1,0,1]
	v_mov_b32_e32 v21, 0
	v_med3_f32 v22, v22, s54, v170
	v_med3_f32 v23, v23, s54, v170
	v_cvt_pk_fp8_f32 v21, v22, v23
	v_pk_fma_f32 v[22:23], v[54:55], s[12:13], v[10:11] op_sel_hi:[1,0,1]
	s_nop 0
	v_med3_f32 v22, v22, s54, v170
	v_med3_f32 v23, v23, s54, v170
	v_cvt_pk_fp8_f32 v21, v22, v23 op_sel:[0,0,1]
	v_pk_fma_f32 v[22:23], v[56:57], s[12:13], v[8:9] op_sel_hi:[1,0,1]
	s_nop 0
	v_med3_f32 v24, v22, s54, v170
	v_med3_f32 v23, v23, s54, v170
	v_mov_b32_e32 v22, 0
	v_cvt_pk_fp8_f32 v22, v24, v23
	v_pk_fma_f32 v[24:25], v[58:59], s[12:13], v[6:7] op_sel_hi:[1,0,1]
	s_nop 0
	v_med3_f32 v23, v24, s54, v170
	v_med3_f32 v24, v25, s54, v170
	v_cvt_pk_fp8_f32 v22, v23, v24 op_sel:[0,0,1]
	v_pk_fma_f32 v[24:25], v[48:49], s[12:13], v[4:5] op_sel_hi:[1,0,1]
	v_mov_b32_e32 v23, 0
	v_med3_f32 v24, v24, s54, v170
	v_med3_f32 v25, v25, s54, v170
	v_cvt_pk_fp8_f32 v23, v24, v25
	v_pk_fma_f32 v[24:25], v[50:51], s[12:13], v[2:3] op_sel_hi:[1,0,1]
	s_nop 0
	v_med3_f32 v24, v24, s54, v170
	v_med3_f32 v25, v25, s54, v170
	v_cvt_pk_fp8_f32 v23, v24, v25 op_sel:[0,0,1]
	v_add_u32_e32 v24, s55, v19
	v_ashrrev_i32_e32 v25, 31, v24
	v_lshlrev_b64 v[24:25], 10, v[24:25]
	v_lshl_add_u64 v[24:25], s[6:7], 0, v[24:25]
	v_lshl_add_u64 v[24:25], v[24:25], 0, v[0:1]
	global_store_dwordx4 v[24:25], v[20:23], off nt
.LBB0_1111:
	s_or_b64 exec, exec, s[22:23]
	v_add_u32_e32 v18, 0xb0, v18
	v_cmp_gt_i32_e32 vcc, s56, v18
	s_and_saveexec_b64 s[22:23], vcc
	s_cbranch_execz .LBB0_1113
	v_pk_fma_f32 v[4:5], v[32:33], s[12:13], v[4:5] op_sel_hi:[1,0,1]
	v_pk_fma_f32 v[16:17], v[44:45], s[12:13], v[16:17] op_sel_hi:[1,0,1]
	v_pk_fma_f32 v[12:13], v[40:41], s[12:13], v[12:13] op_sel_hi:[1,0,1]
	v_pk_fma_f32 v[8:9], v[36:37], s[12:13], v[8:9] op_sel_hi:[1,0,1]
	v_med3_f32 v4, v4, s54, v170
	v_med3_f32 v5, v5, s54, v170
	v_mov_b32_e32 v23, 0
	v_med3_f32 v16, v16, s54, v170
	v_med3_f32 v17, v17, s54, v170
	v_mov_b32_e32 v20, 0
	v_med3_f32 v12, v12, s54, v170
	v_med3_f32 v13, v13, s54, v170
	v_mov_b32_e32 v21, 0
	v_med3_f32 v8, v8, s54, v170
	v_med3_f32 v9, v9, s54, v170
	v_mov_b32_e32 v22, 0
	v_cvt_pk_fp8_f32 v23, v4, v5
	v_cvt_pk_fp8_f32 v20, v16, v17
	v_cvt_pk_fp8_f32 v21, v12, v13
	v_cvt_pk_fp8_f32 v22, v8, v9
	v_pk_fma_f32 v[2:3], v[34:35], s[12:13], v[2:3] op_sel_hi:[1,0,1]
	v_pk_fma_f32 v[14:15], v[46:47], s[12:13], v[14:15] op_sel_hi:[1,0,1]
	v_pk_fma_f32 v[10:11], v[42:43], s[12:13], v[10:11] op_sel_hi:[1,0,1]
	v_pk_fma_f32 v[6:7], v[38:39], s[12:13], v[6:7] op_sel_hi:[1,0,1]
	v_med3_f32 v2, v2, s54, v170
	v_med3_f32 v3, v3, s54, v170
	v_med3_f32 v14, v14, s54, v170
	v_med3_f32 v15, v15, s54, v170
	v_med3_f32 v10, v10, s54, v170
	v_med3_f32 v11, v11, s54, v170
	v_med3_f32 v6, v6, s54, v170
	v_med3_f32 v7, v7, s54, v170
	v_cvt_pk_fp8_f32 v23, v2, v3 op_sel:[0,0,1]
	v_add_u32_e32 v2, s55, v18
	v_cvt_pk_fp8_f32 v20, v14, v15 op_sel:[0,0,1]
	v_cvt_pk_fp8_f32 v21, v10, v11 op_sel:[0,0,1]
	v_cvt_pk_fp8_f32 v22, v6, v7 op_sel:[0,0,1]
	v_ashrrev_i32_e32 v3, 31, v2
	v_lshlrev_b64 v[2:3], 10, v[2:3]
	v_lshl_add_u64 v[2:3], s[6:7], 0, v[2:3]
	v_lshl_add_u64 v[0:1], v[2:3], 0, v[0:1]
	global_store_dwordx4 v[0:1], v[20:23], off nt

.LBB0_1826:
	s_waitcnt vmcnt(23)
	v_mul_f32_e32 v76, 0x42000000, v76
	s_waitcnt vmcnt(22)
	v_mul_f32_e32 v72, 0x42000000, v72
	v_med3_f32 v76, v76, s4, v163
	v_med3_f32 v72, v72, s4, v163
	v_mov_b32_e32 v167, 0
	v_cvt_pk_fp8_f32 v167, v76, v72
	s_waitcnt vmcnt(21)
	v_mul_f32_e32 v68, 0x42000000, v68
	s_waitcnt vmcnt(20)
	v_mul_f32_e32 v64, 0x42000000, v64
	v_med3_f32 v68, v68, s4, v163
	v_med3_f32 v64, v64, s4, v163
	v_cvt_pk_fp8_f32 v167, v68, v64 op_sel:[0,0,1]
	v_mul_f32_e32 v64, 0x42000000, v125
	v_mul_f32_e32 v68, 0x42000000, v121
	v_med3_f32 v64, v64, s4, v163
	v_med3_f32 v68, v68, s4, v163
	v_mov_b32_e32 v168, 0
	v_cvt_pk_fp8_f32 v168, v64, v68
	v_mul_f32_e32 v72, 0x42000000, v117
	v_mul_f32_e32 v64, 0x42000000, v113
	v_med3_f32 v68, v72, s4, v163
	v_med3_f32 v64, v64, s4, v163
	v_cvt_pk_fp8_f32 v168, v68, v64 op_sel:[0,0,1]
	v_mul_f32_e32 v64, 0x42000000, v109
	v_mul_f32_e32 v68, 0x42000000, v105
	v_med3_f32 v64, v64, s4, v163
	v_med3_f32 v68, v68, s4, v163
	v_mov_b32_e32 v169, 0
	v_cvt_pk_fp8_f32 v169, v64, v68
	v_mul_f32_e32 v72, 0x42000000, v101
	v_mul_f32_e32 v64, 0x42000000, v97
	v_med3_f32 v68, v72, s4, v163
	v_med3_f32 v64, v64, s4, v163
	v_cvt_pk_fp8_f32 v169, v68, v64 op_sel:[0,0,1]
	v_mul_f32_e32 v64, 0x42000000, v93
	v_mul_f32_e32 v68, 0x42000000, v89
	v_med3_f32 v64, v64, s4, v163
	v_med3_f32 v68, v68, s4, v163
	v_mov_b32_e32 v170, 0
	v_cvt_pk_fp8_f32 v170, v64, v68
	v_mul_f32_e32 v72, 0x42000000, v85
	v_mul_f32_e32 v64, 0x42000000, v81
	v_med3_f32 v68, v72, s4, v163
	v_med3_f32 v64, v64, s4, v163
	v_cvt_pk_fp8_f32 v170, v68, v64 op_sel:[0,0,1]
	v_mul_f32_e32 v64, 0x42000000, v77
	v_mul_f32_e32 v68, 0x42000000, v73
	v_med3_f32 v64, v64, s4, v163
	v_med3_f32 v68, v68, s4, v163
	v_mov_b32_e32 v171, 0
	v_cvt_pk_fp8_f32 v171, v64, v68
	v_mul_f32_e32 v69, 0x42000000, v69
	v_mul_f32_e32 v64, 0x42000000, v65
	v_med3_f32 v65, v69, s4, v163
	v_med3_f32 v64, v64, s4, v163
	v_cvt_pk_fp8_f32 v171, v65, v64 op_sel:[0,0,1]
	v_mul_f32_e32 v64, 0x42000000, v126
	v_mul_f32_e32 v65, 0x42000000, v122
	v_med3_f32 v64, v64, s4, v163
	v_med3_f32 v65, v65, s4, v163
	v_mov_b32_e32 v172, 0
	v_cvt_pk_fp8_f32 v172, v64, v65
	v_mul_f32_e32 v68, 0x42000000, v118
	v_mul_f32_e32 v64, 0x42000000, v114
	v_med3_f32 v65, v68, s4, v163
	v_med3_f32 v64, v64, s4, v163
	v_cvt_pk_fp8_f32 v172, v65, v64 op_sel:[0,0,1]
	v_mul_f32_e32 v64, 0x42000000, v110
	v_mul_f32_e32 v65, 0x42000000, v106
	v_med3_f32 v64, v64, s4, v163
	v_med3_f32 v65, v65, s4, v163
	v_mov_b32_e32 v173, 0
	v_cvt_pk_fp8_f32 v173, v64, v65
	v_mul_f32_e32 v68, 0x42000000, v102
	v_mul_f32_e32 v64, 0x42000000, v98
	v_med3_f32 v65, v68, s4, v163
	v_med3_f32 v64, v64, s4, v163
	v_cvt_pk_fp8_f32 v173, v65, v64 op_sel:[0,0,1]
	v_mul_f32_e32 v64, 0x42000000, v94
	v_mul_f32_e32 v65, 0x42000000, v90
	v_med3_f32 v64, v64, s4, v163
	v_med3_f32 v65, v65, s4, v163
	v_mov_b32_e32 v174, 0
	v_cvt_pk_fp8_f32 v174, v64, v65
	v_mul_f32_e32 v68, 0x42000000, v86
	v_mul_f32_e32 v64, 0x42000000, v82
	v_med3_f32 v65, v68, s4, v163
	v_med3_f32 v64, v64, s4, v163
	v_cvt_pk_fp8_f32 v174, v65, v64 op_sel:[0,0,1]
	v_mul_f32_e32 v64, 0x42000000, v78
	v_mul_f32_e32 v65, 0x42000000, v74
	v_med3_f32 v64, v64, s4, v163
	v_med3_f32 v65, v65, s4, v163
	v_mov_b32_e32 v175, 0
	v_cvt_pk_fp8_f32 v175, v64, v65
	v_mul_f32_e32 v68, 0x42000000, v70
	v_mul_f32_e32 v64, 0x42000000, v66
	v_med3_f32 v65, v68, s4, v163
	v_med3_f32 v64, v64, s4, v163
	v_cvt_pk_fp8_f32 v175, v65, v64 op_sel:[0,0,1]
	v_mul_f32_e32 v64, 0x42000000, v127
	v_mul_f32_e32 v65, 0x42000000, v123
	v_med3_f32 v64, v64, s4, v163
	v_med3_f32 v65, v65, s4, v163
	v_mov_b32_e32 v68, 0
	v_cvt_pk_fp8_f32 v68, v64, v65
	v_mul_f32_e32 v66, 0x42000000, v119
	v_mul_f32_e32 v64, 0x42000000, v115
	v_med3_f32 v65, v66, s4, v163
	v_med3_f32 v64, v64, s4, v163
	v_cvt_pk_fp8_f32 v68, v65, v64 op_sel:[0,0,1]
	v_mul_f32_e32 v64, 0x42000000, v111
	v_mul_f32_e32 v65, 0x42000000, v107
	v_med3_f32 v64, v64, s4, v163
	v_med3_f32 v65, v65, s4, v163
	v_mov_b32_e32 v69, 0
	v_cvt_pk_fp8_f32 v69, v64, v65
	v_mul_f32_e32 v66, 0x42000000, v103
	v_mul_f32_e32 v64, 0x42000000, v99
	v_med3_f32 v65, v66, s4, v163
	v_med3_f32 v64, v64, s4, v163
	v_cvt_pk_fp8_f32 v69, v65, v64 op_sel:[0,0,1]
	v_mul_f32_e32 v64, 0x42000000, v95
	v_mul_f32_e32 v65, 0x42000000, v91
	v_med3_f32 v64, v64, s4, v163
	v_med3_f32 v65, v65, s4, v163
	v_mov_b32_e32 v70, 0
	v_cvt_pk_fp8_f32 v70, v64, v65
	v_mul_f32_e32 v124, 0x42000000, v124
	v_mul_f32_e32 v120, 0x42000000, v120
	v_mul_f32_e32 v108, 0x42000000, v108
	v_mul_f32_e32 v104, 0x42000000, v104
	v_mul_f32_e32 v92, 0x42000000, v92
	v_mul_f32_e32 v88, 0x42000000, v88
	v_med3_f32 v124, v124, s4, v163
	v_med3_f32 v120, v120, s4, v163
	v_mov_b32_e32 v164, 0
	v_med3_f32 v108, v108, s4, v163
	v_med3_f32 v104, v104, s4, v163
	v_mov_b32_e32 v165, 0
	v_med3_f32 v92, v92, s4, v163
	v_med3_f32 v88, v88, s4, v163
	v_mov_b32_e32 v166, 0
	v_mul_f32_e32 v66, 0x42000000, v87
	v_mul_f32_e32 v64, 0x42000000, v83
	v_cvt_pk_fp8_f32 v164, v124, v120
	v_cvt_pk_fp8_f32 v165, v108, v104
	v_cvt_pk_fp8_f32 v166, v92, v88
	v_med3_f32 v65, v66, s4, v163
	v_med3_f32 v64, v64, s4, v163
	v_cvt_pk_fp8_f32 v70, v65, v64 op_sel:[0,0,1]
	v_mul_f32_e32 v64, 0x42000000, v79
	v_mul_f32_e32 v65, 0x42000000, v75
	v_mul_f32_e32 v116, 0x42000000, v116
	v_mul_f32_e32 v112, 0x42000000, v112
	v_mul_f32_e32 v100, 0x42000000, v100
	v_mul_f32_e32 v96, 0x42000000, v96
	v_mul_f32_e32 v84, 0x42000000, v84
	v_mul_f32_e32 v80, 0x42000000, v80
	v_mul_f32_e32 v66, 0x42000000, v71
	v_med3_f32 v64, v64, s4, v163
	v_med3_f32 v65, v65, s4, v163
	v_mov_b32_e32 v71, 0
	v_med3_f32 v116, v116, s4, v163
	v_med3_f32 v112, v112, s4, v163
	v_med3_f32 v100, v100, s4, v163
	v_med3_f32 v96, v96, s4, v163
	v_med3_f32 v84, v84, s4, v163
	v_med3_f32 v80, v80, s4, v163
	v_cvt_pk_fp8_f32 v71, v64, v65
	v_cvt_pk_fp8_f32 v164, v116, v112 op_sel:[0,0,1]
	v_cvt_pk_fp8_f32 v165, v100, v96 op_sel:[0,0,1]
	v_cvt_pk_fp8_f32 v166, v84, v80 op_sel:[0,0,1]
	v_mul_f32_e32 v64, 0x42000000, v67
	v_med3_f32 v65, v66, s4, v163
	v_med3_f32 v64, v64, s4, v163
	v_cvt_pk_fp8_f32 v71, v65, v64 op_sel:[0,0,1]
	s_waitcnt vmcnt(15)
	v_mul_f32_e32 v0, 0x42000000, v0
	s_waitcnt vmcnt(14)
	v_mul_f32_e32 v48, 0x42000000, v48
	global_store_dwordx4 v[160:161], v[164:167], off nt
	global_store_dwordx4 v[160:161], v[168:171], off offset:1024 nt
	global_store_dwordx4 v[160:161], v[172:175], off offset:2048 nt
	global_store_dwordx4 v[160:161], v[68:71], off offset:3072 nt
	v_med3_f32 v0, v0, s4, v163
	v_med3_f32 v48, v48, s4, v163
	v_mov_b32_e32 v164, 0
	v_cvt_pk_fp8_f32 v164, v0, v48
	s_waitcnt vmcnt(17)
	v_mul_f32_e32 v60, 0x42000000, v60
	s_waitcnt vmcnt(16)
	v_mul_f32_e32 v0, 0x42000000, v56
	v_med3_f32 v48, v60, s4, v163
	v_med3_f32 v0, v0, s4, v163
	v_cvt_pk_fp8_f32 v164, v48, v0 op_sel:[0,0,1]
	s_waitcnt vmcnt(15)
	v_mul_f32_e32 v0, 0x42000000, v44
	s_waitcnt vmcnt(14)
	v_mul_f32_e32 v44, 0x42000000, v52
	v_med3_f32 v0, v0, s4, v163
	v_med3_f32 v44, v44, s4, v163
	v_mov_b32_e32 v165, 0
	v_cvt_pk_fp8_f32 v165, v0, v44
	s_waitcnt vmcnt(13)
	v_mul_f32_e32 v40, 0x42000000, v40
	s_waitcnt vmcnt(12)
	v_mul_f32_e32 v0, 0x42000000, v36
	v_med3_f32 v36, v40, s4, v163
	v_med3_f32 v0, v0, s4, v163
	v_cvt_pk_fp8_f32 v165, v36, v0 op_sel:[0,0,1]
	s_waitcnt vmcnt(11)
	v_mul_f32_e32 v0, 0x42000000, v28
	s_waitcnt vmcnt(10)
	v_mul_f32_e32 v28, 0x42000000, v32
	v_med3_f32 v0, v0, s4, v163
	v_med3_f32 v28, v28, s4, v163
	v_mov_b32_e32 v166, 0
	v_cvt_pk_fp8_f32 v166, v0, v28
	s_waitcnt vmcnt(9)
	v_mul_f32_e32 v24, 0x42000000, v24
	s_waitcnt vmcnt(8)
	v_mul_f32_e32 v0, 0x42000000, v20
	v_med3_f32 v20, v24, s4, v163
	v_med3_f32 v0, v0, s4, v163
	v_cvt_pk_fp8_f32 v166, v20, v0 op_sel:[0,0,1]
	s_waitcnt vmcnt(7)
	v_mul_f32_e32 v0, 0x42000000, v4
	s_waitcnt vmcnt(6)
	v_mul_f32_e32 v4, 0x42000000, v8
	v_med3_f32 v0, v0, s4, v163
	v_med3_f32 v4, v4, s4, v163
	v_mov_b32_e32 v167, 0
	v_cvt_pk_fp8_f32 v167, v0, v4
	s_waitcnt vmcnt(5)
	v_mul_f32_e32 v8, 0x42000000, v16
	s_waitcnt vmcnt(4)
	v_mul_f32_e32 v0, 0x42000000, v12
	v_med3_f32 v4, v8, s4, v163
	v_med3_f32 v0, v0, s4, v163
	v_cvt_pk_fp8_f32 v167, v4, v0 op_sel:[0,0,1]
	v_mul_f32_e32 v0, 0x42000000, v1
	v_mul_f32_e32 v1, 0x42000000, v49
	v_med3_f32 v0, v0, s4, v163
	v_med3_f32 v1, v1, s4, v163
	v_mov_b32_e32 v168, 0
	v_cvt_pk_fp8_f32 v168, v0, v1
	v_mul_f32_e32 v4, 0x42000000, v61
	v_mul_f32_e32 v0, 0x42000000, v57
	v_med3_f32 v1, v4, s4, v163
	v_med3_f32 v0, v0, s4, v163
	v_cvt_pk_fp8_f32 v168, v1, v0 op_sel:[0,0,1]
	v_mul_f32_e32 v0, 0x42000000, v45
	v_mul_f32_e32 v1, 0x42000000, v53
	v_med3_f32 v0, v0, s4, v163
	v_med3_f32 v1, v1, s4, v163
	v_mov_b32_e32 v169, 0
	v_cvt_pk_fp8_f32 v169, v0, v1
	v_mul_f32_e32 v4, 0x42000000, v41
	v_mul_f32_e32 v0, 0x42000000, v37
	v_med3_f32 v1, v4, s4, v163
	v_med3_f32 v0, v0, s4, v163
	v_cvt_pk_fp8_f32 v169, v1, v0 op_sel:[0,0,1]
	v_mul_f32_e32 v0, 0x42000000, v29
	v_mul_f32_e32 v1, 0x42000000, v33
	v_med3_f32 v0, v0, s4, v163
	v_med3_f32 v1, v1, s4, v163
	v_mov_b32_e32 v170, 0
	v_cvt_pk_fp8_f32 v170, v0, v1
	v_mul_f32_e32 v4, 0x42000000, v25
	v_mul_f32_e32 v0, 0x42000000, v21
	v_med3_f32 v1, v4, s4, v163
	v_med3_f32 v0, v0, s4, v163
	v_cvt_pk_fp8_f32 v170, v1, v0 op_sel:[0,0,1]
	v_mul_f32_e32 v0, 0x42000000, v5
	v_mul_f32_e32 v1, 0x42000000, v9
	v_med3_f32 v0, v0, s4, v163
	v_med3_f32 v1, v1, s4, v163
	v_mov_b32_e32 v171, 0
	v_cvt_pk_fp8_f32 v171, v0, v1
	v_mul_f32_e32 v4, 0x42000000, v17
	v_mul_f32_e32 v0, 0x42000000, v13
	v_med3_f32 v1, v4, s4, v163
	v_med3_f32 v0, v0, s4, v163
	v_cvt_pk_fp8_f32 v171, v1, v0 op_sel:[0,0,1]
	v_mul_f32_e32 v0, 0x42000000, v2
	v_mul_f32_e32 v1, 0x42000000, v50
	v_med3_f32 v0, v0, s4, v163
	v_med3_f32 v1, v1, s4, v163
	v_mov_b32_e32 v172, 0
	v_cvt_pk_fp8_f32 v172, v0, v1
	v_mul_f32_e32 v2, 0x42000000, v62
	v_mul_f32_e32 v0, 0x42000000, v58
	v_med3_f32 v1, v2, s4, v163
	v_med3_f32 v0, v0, s4, v163
	v_cvt_pk_fp8_f32 v172, v1, v0 op_sel:[0,0,1]
	v_mul_f32_e32 v0, 0x42000000, v46
	v_mul_f32_e32 v1, 0x42000000, v54
	v_med3_f32 v0, v0, s4, v163
	v_med3_f32 v1, v1, s4, v163
	v_mov_b32_e32 v173, 0
	v_cvt_pk_fp8_f32 v173, v0, v1
	v_mul_f32_e32 v2, 0x42000000, v42
	v_mul_f32_e32 v0, 0x42000000, v38
	v_med3_f32 v1, v2, s4, v163
	v_med3_f32 v0, v0, s4, v163
	v_cvt_pk_fp8_f32 v173, v1, v0 op_sel:[0,0,1]
	v_mul_f32_e32 v0, 0x42000000, v30
	v_mul_f32_e32 v1, 0x42000000, v34
	v_med3_f32 v0, v0, s4, v163
	v_med3_f32 v1, v1, s4, v163
	v_mov_b32_e32 v174, 0
	v_cvt_pk_fp8_f32 v174, v0, v1
	v_mul_f32_e32 v2, 0x42000000, v26
	v_mul_f32_e32 v0, 0x42000000, v22
	v_med3_f32 v1, v2, s4, v163
	v_med3_f32 v0, v0, s4, v163
	v_cvt_pk_fp8_f32 v174, v1, v0 op_sel:[0,0,1]
	v_mul_f32_e32 v0, 0x42000000, v6
	v_mul_f32_e32 v1, 0x42000000, v10
	v_med3_f32 v0, v0, s4, v163
	v_med3_f32 v1, v1, s4, v163
	v_mov_b32_e32 v175, 0
	v_cvt_pk_fp8_f32 v175, v0, v1
	v_mul_f32_e32 v2, 0x42000000, v18
	v_mul_f32_e32 v0, 0x42000000, v14
	v_med3_f32 v1, v2, s4, v163
	v_med3_f32 v0, v0, s4, v163
	v_cvt_pk_fp8_f32 v175, v1, v0 op_sel:[0,0,1]
	v_mul_f32_e32 v0, 0x42000000, v3
	v_mul_f32_e32 v1, 0x42000000, v51
	v_med3_f32 v3, v0, s4, v163
	v_med3_f32 v1, v1, s4, v163
	v_mov_b32_e32 v0, 0
	v_cvt_pk_fp8_f32 v0, v3, v1
	v_mul_f32_e32 v2, 0x42000000, v63
	v_mul_f32_e32 v1, 0x42000000, v59
	v_med3_f32 v2, v2, s4, v163
	v_med3_f32 v1, v1, s4, v163
	v_cvt_pk_fp8_f32 v0, v2, v1 op_sel:[0,0,1]
	v_mul_f32_e32 v1, 0x42000000, v47
	v_mul_f32_e32 v2, 0x42000000, v55
	v_med3_f32 v4, v1, s4, v163
	v_med3_f32 v2, v2, s4, v163
	v_mov_b32_e32 v1, 0
	v_cvt_pk_fp8_f32 v1, v4, v2
	v_mul_f32_e32 v3, 0x42000000, v43
	v_mul_f32_e32 v2, 0x42000000, v39
	v_med3_f32 v3, v3, s4, v163
	v_med3_f32 v2, v2, s4, v163
	v_cvt_pk_fp8_f32 v1, v3, v2 op_sel:[0,0,1]
	v_mul_f32_e32 v2, 0x42000000, v31
	v_mul_f32_e32 v3, 0x42000000, v35
	v_med3_f32 v5, v2, s4, v163
	v_med3_f32 v3, v3, s4, v163
	v_mov_b32_e32 v2, 0
	v_cvt_pk_fp8_f32 v2, v5, v3
	v_mul_f32_e32 v4, 0x42000000, v27
	v_mul_f32_e32 v3, 0x42000000, v23
	v_med3_f32 v4, v4, s4, v163
	v_med3_f32 v3, v3, s4, v163
	v_cvt_pk_fp8_f32 v2, v4, v3 op_sel:[0,0,1]
	v_mul_f32_e32 v3, 0x42000000, v7
	v_mul_f32_e32 v4, 0x42000000, v11
	v_med3_f32 v6, v3, s4, v163
	v_med3_f32 v4, v4, s4, v163
	v_mov_b32_e32 v3, 0
	v_cvt_pk_fp8_f32 v3, v6, v4
	v_mul_f32_e32 v5, 0x42000000, v19
	v_mul_f32_e32 v4, 0x42000000, v15
	v_med3_f32 v5, v5, s4, v163
	v_med3_f32 v4, v4, s4, v163
	v_cvt_pk_fp8_f32 v3, v5, v4 op_sel:[0,0,1]
	global_load_dwordx4 v[124:127], v[128:129], off nt
	global_load_dwordx4 v[120:123], v[130:131], off nt
	global_load_dwordx4 v[116:119], v[132:133], off nt
	global_load_dwordx4 v[112:115], v[134:135], off nt
	global_load_dwordx4 v[108:111], v[136:137], off nt
	global_load_dwordx4 v[104:107], v[138:139], off nt
	global_load_dwordx4 v[100:103], v[140:141], off nt
	global_load_dwordx4 v[96:99], v[142:143], off nt
	global_load_dwordx4 v[92:95], v[144:145], off nt
	global_load_dwordx4 v[88:91], v[146:147], off nt
	global_load_dwordx4 v[84:87], v[148:149], off nt
	global_load_dwordx4 v[80:83], v[150:151], off nt
	global_load_dwordx4 v[76:79], v[152:153], off nt
	global_load_dwordx4 v[72:75], v[154:155], off nt
	global_load_dwordx4 v[68:71], v[156:157], off nt
	global_load_dwordx4 v[64:67], v[158:159], off nt
	s_nop 0
	global_store_dwordx4 v[160:161], v[164:167], off nt
	global_store_dwordx4 v[160:161], v[168:171], off offset:1024 nt
	global_store_dwordx4 v[160:161], v[172:175], off offset:2048 nt
	global_store_dwordx4 v[160:161], v[0:3], off offset:3072 nt
	global_load_dwordx4 v[0:3], v[128:129], off
	s_nop 0
	global_load_dwordx4 v[48:51], v[130:131], off
	global_load_dwordx4 v[60:63], v[132:133], off
	global_load_dwordx4 v[56:59], v[134:135], off
	global_load_dwordx4 v[44:47], v[136:137], off
	global_load_dwordx4 v[52:55], v[138:139], off
	global_load_dwordx4 v[40:43], v[140:141], off
	global_load_dwordx4 v[36:39], v[142:143], off
	global_load_dwordx4 v[28:31], v[144:145], off
	global_load_dwordx4 v[32:35], v[146:147], off
	global_load_dwordx4 v[24:27], v[148:149], off
	global_load_dwordx4 v[20:23], v[150:151], off
	global_load_dwordx4 v[4:7], v[152:153], off
	global_load_dwordx4 v[8:11], v[154:155], off
	global_load_dwordx4 v[16:19], v[156:157], off
	global_load_dwordx4 v[12:15], v[158:159], off
	s_mov_b64 vcc, vcc
	s_cbranch_vccz .LBB0_1826
	s_mov_b64 s[4:5], 0
	v_add_u32_e32 v162, s33, v162
	s_branch .LBB0_1960

.LBB0_2019:
	s_waitcnt vmcnt(23)
	v_mul_f32_e32 v76, 0x42000000, v76
	s_waitcnt vmcnt(22)
	v_mul_f32_e32 v72, 0x42000000, v72
	v_med3_f32 v76, v76, s4, v163
	v_med3_f32 v72, v72, s4, v163
	v_mov_b32_e32 v167, 0
	v_cvt_pk_fp8_f32 v167, v76, v72
	s_waitcnt vmcnt(21)
	v_mul_f32_e32 v68, 0x42000000, v68
	s_waitcnt vmcnt(20)
	v_mul_f32_e32 v64, 0x42000000, v64
	v_med3_f32 v68, v68, s4, v163
	v_med3_f32 v64, v64, s4, v163
	v_cvt_pk_fp8_f32 v167, v68, v64 op_sel:[0,0,1]
	v_mul_f32_e32 v64, 0x42000000, v125
	v_mul_f32_e32 v68, 0x42000000, v121
	v_med3_f32 v64, v64, s4, v163
	v_med3_f32 v68, v68, s4, v163
	v_mov_b32_e32 v168, 0
	v_cvt_pk_fp8_f32 v168, v64, v68
	v_mul_f32_e32 v72, 0x42000000, v117
	v_mul_f32_e32 v64, 0x42000000, v113
	v_med3_f32 v68, v72, s4, v163
	v_med3_f32 v64, v64, s4, v163
	v_cvt_pk_fp8_f32 v168, v68, v64 op_sel:[0,0,1]
	v_mul_f32_e32 v64, 0x42000000, v109
	v_mul_f32_e32 v68, 0x42000000, v105
	v_med3_f32 v64, v64, s4, v163
	v_med3_f32 v68, v68, s4, v163
	v_mov_b32_e32 v169, 0
	v_cvt_pk_fp8_f32 v169, v64, v68
	v_mul_f32_e32 v72, 0x42000000, v101
	v_mul_f32_e32 v64, 0x42000000, v97
	v_med3_f32 v68, v72, s4, v163
	v_med3_f32 v64, v64, s4, v163
	v_cvt_pk_fp8_f32 v169, v68, v64 op_sel:[0,0,1]
	v_mul_f32_e32 v64, 0x42000000, v93
	v_mul_f32_e32 v68, 0x42000000, v89
	v_med3_f32 v64, v64, s4, v163
	v_med3_f32 v68, v68, s4, v163
	v_mov_b32_e32 v170, 0
	v_cvt_pk_fp8_f32 v170, v64, v68
	v_mul_f32_e32 v72, 0x42000000, v85
	v_mul_f32_e32 v64, 0x42000000, v81
	v_med3_f32 v68, v72, s4, v163
	v_med3_f32 v64, v64, s4, v163
	v_cvt_pk_fp8_f32 v170, v68, v64 op_sel:[0,0,1]
	v_mul_f32_e32 v64, 0x42000000, v77
	v_mul_f32_e32 v68, 0x42000000, v73
	v_med3_f32 v64, v64, s4, v163
	v_med3_f32 v68, v68, s4, v163
	v_mov_b32_e32 v171, 0
	v_cvt_pk_fp8_f32 v171, v64, v68
	v_mul_f32_e32 v69, 0x42000000, v69
	v_mul_f32_e32 v64, 0x42000000, v65
	v_med3_f32 v65, v69, s4, v163
	v_med3_f32 v64, v64, s4, v163
	v_cvt_pk_fp8_f32 v171, v65, v64 op_sel:[0,0,1]
	v_mul_f32_e32 v64, 0x42000000, v126
	v_mul_f32_e32 v65, 0x42000000, v122
	v_med3_f32 v64, v64, s4, v163
	v_med3_f32 v65, v65, s4, v163
	v_mov_b32_e32 v172, 0
	v_cvt_pk_fp8_f32 v172, v64, v65
	v_mul_f32_e32 v68, 0x42000000, v118
	v_mul_f32_e32 v64, 0x42000000, v114
	v_med3_f32 v65, v68, s4, v163
	v_med3_f32 v64, v64, s4, v163
	v_cvt_pk_fp8_f32 v172, v65, v64 op_sel:[0,0,1]
	v_mul_f32_e32 v64, 0x42000000, v110
	v_mul_f32_e32 v65, 0x42000000, v106
	v_med3_f32 v64, v64, s4, v163
	v_med3_f32 v65, v65, s4, v163
	v_mov_b32_e32 v173, 0
	v_cvt_pk_fp8_f32 v173, v64, v65
	v_mul_f32_e32 v68, 0x42000000, v102
	v_mul_f32_e32 v64, 0x42000000, v98
	v_med3_f32 v65, v68, s4, v163
	v_med3_f32 v64, v64, s4, v163
	v_cvt_pk_fp8_f32 v173, v65, v64 op_sel:[0,0,1]
	v_mul_f32_e32 v64, 0x42000000, v94
	v_mul_f32_e32 v65, 0x42000000, v90
	v_med3_f32 v64, v64, s4, v163
	v_med3_f32 v65, v65, s4, v163
	v_mov_b32_e32 v174, 0
	v_cvt_pk_fp8_f32 v174, v64, v65
	v_mul_f32_e32 v68, 0x42000000, v86
	v_mul_f32_e32 v64, 0x42000000, v82
	v_med3_f32 v65, v68, s4, v163
	v_med3_f32 v64, v64, s4, v163
	v_cvt_pk_fp8_f32 v174, v65, v64 op_sel:[0,0,1]
	v_mul_f32_e32 v64, 0x42000000, v78
	v_mul_f32_e32 v65, 0x42000000, v74
	v_med3_f32 v64, v64, s4, v163
	v_med3_f32 v65, v65, s4, v163
	v_mov_b32_e32 v175, 0
	v_cvt_pk_fp8_f32 v175, v64, v65
	v_mul_f32_e32 v68, 0x42000000, v70
	v_mul_f32_e32 v64, 0x42000000, v66
	v_med3_f32 v65, v68, s4, v163
	v_med3_f32 v64, v64, s4, v163
	v_cvt_pk_fp8_f32 v175, v65, v64 op_sel:[0,0,1]
	v_mul_f32_e32 v64, 0x42000000, v127
	v_mul_f32_e32 v65, 0x42000000, v123
	v_med3_f32 v64, v64, s4, v163
	v_med3_f32 v65, v65, s4, v163
	v_mov_b32_e32 v68, 0
	v_cvt_pk_fp8_f32 v68, v64, v65
	v_mul_f32_e32 v66, 0x42000000, v119
	v_mul_f32_e32 v64, 0x42000000, v115
	v_med3_f32 v65, v66, s4, v163
	v_med3_f32 v64, v64, s4, v163
	v_cvt_pk_fp8_f32 v68, v65, v64 op_sel:[0,0,1]
	v_mul_f32_e32 v64, 0x42000000, v111
	v_mul_f32_e32 v65, 0x42000000, v107
	v_med3_f32 v64, v64, s4, v163
	v_med3_f32 v65, v65, s4, v163
	v_mov_b32_e32 v69, 0
	v_cvt_pk_fp8_f32 v69, v64, v65
	v_mul_f32_e32 v66, 0x42000000, v103
	v_mul_f32_e32 v64, 0x42000000, v99
	v_med3_f32 v65, v66, s4, v163
	v_med3_f32 v64, v64, s4, v163
	v_cvt_pk_fp8_f32 v69, v65, v64 op_sel:[0,0,1]
	v_mul_f32_e32 v64, 0x42000000, v95
	v_mul_f32_e32 v65, 0x42000000, v91
	v_med3_f32 v64, v64, s4, v163
	v_med3_f32 v65, v65, s4, v163
	v_mov_b32_e32 v70, 0
	v_cvt_pk_fp8_f32 v70, v64, v65
	v_mul_f32_e32 v124, 0x42000000, v124
	v_mul_f32_e32 v120, 0x42000000, v120
	v_mul_f32_e32 v108, 0x42000000, v108
	v_mul_f32_e32 v104, 0x42000000, v104
	v_mul_f32_e32 v92, 0x42000000, v92
	v_mul_f32_e32 v88, 0x42000000, v88
	v_med3_f32 v124, v124, s4, v163
	v_med3_f32 v120, v120, s4, v163
	v_mov_b32_e32 v164, 0
	v_med3_f32 v108, v108, s4, v163
	v_med3_f32 v104, v104, s4, v163
	v_mov_b32_e32 v165, 0
	v_med3_f32 v92, v92, s4, v163
	v_med3_f32 v88, v88, s4, v163
	v_mov_b32_e32 v166, 0
	v_mul_f32_e32 v66, 0x42000000, v87
	v_mul_f32_e32 v64, 0x42000000, v83
	v_cvt_pk_fp8_f32 v164, v124, v120
	v_cvt_pk_fp8_f32 v165, v108, v104
	v_cvt_pk_fp8_f32 v166, v92, v88
	v_med3_f32 v65, v66, s4, v163
	v_med3_f32 v64, v64, s4, v163
	v_cvt_pk_fp8_f32 v70, v65, v64 op_sel:[0,0,1]
	v_mul_f32_e32 v64, 0x42000000, v79
	v_mul_f32_e32 v65, 0x42000000, v75
	v_mul_f32_e32 v116, 0x42000000, v116
	v_mul_f32_e32 v112, 0x42000000, v112
	v_mul_f32_e32 v100, 0x42000000, v100
	v_mul_f32_e32 v96, 0x42000000, v96
	v_mul_f32_e32 v84, 0x42000000, v84
	v_mul_f32_e32 v80, 0x42000000, v80
	v_mul_f32_e32 v66, 0x42000000, v71
	v_med3_f32 v64, v64, s4, v163
	v_med3_f32 v65, v65, s4, v163
	v_mov_b32_e32 v71, 0
	v_med3_f32 v116, v116, s4, v163
	v_med3_f32 v112, v112, s4, v163
	v_med3_f32 v100, v100, s4, v163
	v_med3_f32 v96, v96, s4, v163
	v_med3_f32 v84, v84, s4, v163
	v_med3_f32 v80, v80, s4, v163
	v_cvt_pk_fp8_f32 v71, v64, v65
	v_cvt_pk_fp8_f32 v164, v116, v112 op_sel:[0,0,1]
	v_cvt_pk_fp8_f32 v165, v100, v96 op_sel:[0,0,1]
	v_cvt_pk_fp8_f32 v166, v84, v80 op_sel:[0,0,1]
	v_mul_f32_e32 v64, 0x42000000, v67
	v_med3_f32 v65, v66, s4, v163
	v_med3_f32 v64, v64, s4, v163
	v_cvt_pk_fp8_f32 v71, v65, v64 op_sel:[0,0,1]
	s_waitcnt vmcnt(15)
	v_mul_f32_e32 v0, 0x42000000, v0
	s_waitcnt vmcnt(14)
	v_mul_f32_e32 v48, 0x42000000, v48
	global_store_dwordx4 v[160:161], v[164:167], off nt
	global_store_dwordx4 v[160:161], v[168:171], off offset:1024 nt
	global_store_dwordx4 v[160:161], v[172:175], off offset:2048 nt
	global_store_dwordx4 v[160:161], v[68:71], off offset:3072 nt
	v_med3_f32 v0, v0, s4, v163
	v_med3_f32 v48, v48, s4, v163
	v_mov_b32_e32 v164, 0
	v_cvt_pk_fp8_f32 v164, v0, v48
	s_waitcnt vmcnt(17)
	v_mul_f32_e32 v60, 0x42000000, v60
	s_waitcnt vmcnt(16)
	v_mul_f32_e32 v0, 0x42000000, v56
	v_med3_f32 v48, v60, s4, v163
	v_med3_f32 v0, v0, s4, v163
	v_cvt_pk_fp8_f32 v164, v48, v0 op_sel:[0,0,1]
	s_waitcnt vmcnt(15)
	v_mul_f32_e32 v0, 0x42000000, v44
	s_waitcnt vmcnt(14)
	v_mul_f32_e32 v44, 0x42000000, v52
	v_med3_f32 v0, v0, s4, v163
	v_med3_f32 v44, v44, s4, v163
	v_mov_b32_e32 v165, 0
	v_cvt_pk_fp8_f32 v165, v0, v44
	s_waitcnt vmcnt(13)
	v_mul_f32_e32 v40, 0x42000000, v40
	s_waitcnt vmcnt(12)
	v_mul_f32_e32 v0, 0x42000000, v36
	v_med3_f32 v36, v40, s4, v163
	v_med3_f32 v0, v0, s4, v163
	v_cvt_pk_fp8_f32 v165, v36, v0 op_sel:[0,0,1]
	s_waitcnt vmcnt(11)
	v_mul_f32_e32 v0, 0x42000000, v28
	s_waitcnt vmcnt(10)
	v_mul_f32_e32 v28, 0x42000000, v32
	v_med3_f32 v0, v0, s4, v163
	v_med3_f32 v28, v28, s4, v163
	v_mov_b32_e32 v166, 0
	v_cvt_pk_fp8_f32 v166, v0, v28
	s_waitcnt vmcnt(9)
	v_mul_f32_e32 v24, 0x42000000, v24
	s_waitcnt vmcnt(8)
	v_mul_f32_e32 v0, 0x42000000, v20
	v_med3_f32 v20, v24, s4, v163
	v_med3_f32 v0, v0, s4, v163
	v_cvt_pk_fp8_f32 v166, v20, v0 op_sel:[0,0,1]
	s_waitcnt vmcnt(7)
	v_mul_f32_e32 v0, 0x42000000, v4
	s_waitcnt vmcnt(6)
	v_mul_f32_e32 v4, 0x42000000, v8
	v_med3_f32 v0, v0, s4, v163
	v_med3_f32 v4, v4, s4, v163
	v_mov_b32_e32 v167, 0
	v_cvt_pk_fp8_f32 v167, v0, v4
	s_waitcnt vmcnt(5)
	v_mul_f32_e32 v8, 0x42000000, v16
	s_waitcnt vmcnt(4)
	v_mul_f32_e32 v0, 0x42000000, v12
	v_med3_f32 v4, v8, s4, v163
	v_med3_f32 v0, v0, s4, v163
	v_cvt_pk_fp8_f32 v167, v4, v0 op_sel:[0,0,1]
	v_mul_f32_e32 v0, 0x42000000, v1
	v_mul_f32_e32 v1, 0x42000000, v49
	v_med3_f32 v0, v0, s4, v163
	v_med3_f32 v1, v1, s4, v163
	v_mov_b32_e32 v168, 0
	v_cvt_pk_fp8_f32 v168, v0, v1
	v_mul_f32_e32 v4, 0x42000000, v61
	v_mul_f32_e32 v0, 0x42000000, v57
	v_med3_f32 v1, v4, s4, v163
	v_med3_f32 v0, v0, s4, v163
	v_cvt_pk_fp8_f32 v168, v1, v0 op_sel:[0,0,1]
	v_mul_f32_e32 v0, 0x42000000, v45
	v_mul_f32_e32 v1, 0x42000000, v53
	v_med3_f32 v0, v0, s4, v163
	v_med3_f32 v1, v1, s4, v163
	v_mov_b32_e32 v169, 0
	v_cvt_pk_fp8_f32 v169, v0, v1
	v_mul_f32_e32 v4, 0x42000000, v41
	v_mul_f32_e32 v0, 0x42000000, v37
	v_med3_f32 v1, v4, s4, v163
	v_med3_f32 v0, v0, s4, v163
	v_cvt_pk_fp8_f32 v169, v1, v0 op_sel:[0,0,1]
	v_mul_f32_e32 v0, 0x42000000, v29
	v_mul_f32_e32 v1, 0x42000000, v33
	v_med3_f32 v0, v0, s4, v163
	v_med3_f32 v1, v1, s4, v163
	v_mov_b32_e32 v170, 0
	v_cvt_pk_fp8_f32 v170, v0, v1
	v_mul_f32_e32 v4, 0x42000000, v25
	v_mul_f32_e32 v0, 0x42000000, v21
	v_med3_f32 v1, v4, s4, v163
	v_med3_f32 v0, v0, s4, v163
	v_cvt_pk_fp8_f32 v170, v1, v0 op_sel:[0,0,1]
	v_mul_f32_e32 v0, 0x42000000, v5
	v_mul_f32_e32 v1, 0x42000000, v9
	v_med3_f32 v0, v0, s4, v163
	v_med3_f32 v1, v1, s4, v163
	v_mov_b32_e32 v171, 0
	v_cvt_pk_fp8_f32 v171, v0, v1
	v_mul_f32_e32 v4, 0x42000000, v17
	v_mul_f32_e32 v0, 0x42000000, v13
	v_med3_f32 v1, v4, s4, v163
	v_med3_f32 v0, v0, s4, v163
	v_cvt_pk_fp8_f32 v171, v1, v0 op_sel:[0,0,1]
	v_mul_f32_e32 v0, 0x42000000, v2
	v_mul_f32_e32 v1, 0x42000000, v50
	v_med3_f32 v0, v0, s4, v163
	v_med3_f32 v1, v1, s4, v163
	v_mov_b32_e32 v172, 0
	v_cvt_pk_fp8_f32 v172, v0, v1
	v_mul_f32_e32 v2, 0x42000000, v62
	v_mul_f32_e32 v0, 0x42000000, v58
	v_med3_f32 v1, v2, s4, v163
	v_med3_f32 v0, v0, s4, v163
	v_cvt_pk_fp8_f32 v172, v1, v0 op_sel:[0,0,1]
	v_mul_f32_e32 v0, 0x42000000, v46
	v_mul_f32_e32 v1, 0x42000000, v54
	v_med3_f32 v0, v0, s4, v163
	v_med3_f32 v1, v1, s4, v163
	v_mov_b32_e32 v173, 0
	v_cvt_pk_fp8_f32 v173, v0, v1
	v_mul_f32_e32 v2, 0x42000000, v42
	v_mul_f32_e32 v0, 0x42000000, v38
	v_med3_f32 v1, v2, s4, v163
	v_med3_f32 v0, v0, s4, v163
	v_cvt_pk_fp8_f32 v173, v1, v0 op_sel:[0,0,1]
	v_mul_f32_e32 v0, 0x42000000, v30
	v_mul_f32_e32 v1, 0x42000000, v34
	v_med3_f32 v0, v0, s4, v163
	v_med3_f32 v1, v1, s4, v163
	v_mov_b32_e32 v174, 0
	v_cvt_pk_fp8_f32 v174, v0, v1
	v_mul_f32_e32 v2, 0x42000000, v26
	v_mul_f32_e32 v0, 0x42000000, v22
	v_med3_f32 v1, v2, s4, v163
	v_med3_f32 v0, v0, s4, v163
	v_cvt_pk_fp8_f32 v174, v1, v0 op_sel:[0,0,1]
	v_mul_f32_e32 v0, 0x42000000, v6
	v_mul_f32_e32 v1, 0x42000000, v10
	v_med3_f32 v0, v0, s4, v163
	v_med3_f32 v1, v1, s4, v163
	v_mov_b32_e32 v175, 0
	v_cvt_pk_fp8_f32 v175, v0, v1
	v_mul_f32_e32 v2, 0x42000000, v18
	v_mul_f32_e32 v0, 0x42000000, v14
	v_med3_f32 v1, v2, s4, v163
	v_med3_f32 v0, v0, s4, v163
	v_cvt_pk_fp8_f32 v175, v1, v0 op_sel:[0,0,1]
	v_mul_f32_e32 v0, 0x42000000, v3
	v_mul_f32_e32 v1, 0x42000000, v51
	v_med3_f32 v3, v0, s4, v163
	v_med3_f32 v1, v1, s4, v163
	v_mov_b32_e32 v0, 0
	v_cvt_pk_fp8_f32 v0, v3, v1
	v_mul_f32_e32 v2, 0x42000000, v63
	v_mul_f32_e32 v1, 0x42000000, v59
	v_med3_f32 v2, v2, s4, v163
	v_med3_f32 v1, v1, s4, v163
	v_cvt_pk_fp8_f32 v0, v2, v1 op_sel:[0,0,1]
	v_mul_f32_e32 v1, 0x42000000, v47
	v_mul_f32_e32 v2, 0x42000000, v55
	v_med3_f32 v4, v1, s4, v163
	v_med3_f32 v2, v2, s4, v163
	v_mov_b32_e32 v1, 0
	v_cvt_pk_fp8_f32 v1, v4, v2
	v_mul_f32_e32 v3, 0x42000000, v43
	v_mul_f32_e32 v2, 0x42000000, v39
	v_med3_f32 v3, v3, s4, v163
	v_med3_f32 v2, v2, s4, v163
	v_cvt_pk_fp8_f32 v1, v3, v2 op_sel:[0,0,1]
	v_mul_f32_e32 v2, 0x42000000, v31
	v_mul_f32_e32 v3, 0x42000000, v35
	v_med3_f32 v5, v2, s4, v163
	v_med3_f32 v3, v3, s4, v163
	v_mov_b32_e32 v2, 0
	v_cvt_pk_fp8_f32 v2, v5, v3
	v_mul_f32_e32 v4, 0x42000000, v27
	v_mul_f32_e32 v3, 0x42000000, v23
	v_med3_f32 v4, v4, s4, v163
	v_med3_f32 v3, v3, s4, v163
	v_cvt_pk_fp8_f32 v2, v4, v3 op_sel:[0,0,1]
	v_mul_f32_e32 v3, 0x42000000, v7
	v_mul_f32_e32 v4, 0x42000000, v11
	v_med3_f32 v6, v3, s4, v163
	v_med3_f32 v4, v4, s4, v163
	v_mov_b32_e32 v3, 0
	v_cvt_pk_fp8_f32 v3, v6, v4
	v_mul_f32_e32 v5, 0x42000000, v19
	v_mul_f32_e32 v4, 0x42000000, v15
	v_med3_f32 v5, v5, s4, v163
	v_med3_f32 v4, v4, s4, v163
	v_cvt_pk_fp8_f32 v3, v5, v4 op_sel:[0,0,1]
	global_load_dwordx4 v[124:127], v[128:129], off nt
	global_load_dwordx4 v[120:123], v[130:131], off nt
	global_load_dwordx4 v[116:119], v[132:133], off nt
	global_load_dwordx4 v[112:115], v[134:135], off nt
	global_load_dwordx4 v[108:111], v[136:137], off nt
	global_load_dwordx4 v[104:107], v[138:139], off nt
	global_load_dwordx4 v[100:103], v[140:141], off nt
	global_load_dwordx4 v[96:99], v[142:143], off nt
	global_load_dwordx4 v[92:95], v[144:145], off nt
	global_load_dwordx4 v[88:91], v[146:147], off nt
	global_load_dwordx4 v[84:87], v[148:149], off nt
	global_load_dwordx4 v[80:83], v[150:151], off nt
	global_load_dwordx4 v[76:79], v[152:153], off nt
	global_load_dwordx4 v[72:75], v[154:155], off nt
	global_load_dwordx4 v[68:71], v[156:157], off nt
	global_load_dwordx4 v[64:67], v[158:159], off nt
	s_nop 0
	global_store_dwordx4 v[160:161], v[164:167], off nt
	global_store_dwordx4 v[160:161], v[168:171], off offset:1024 nt
	global_store_dwordx4 v[160:161], v[172:175], off offset:2048 nt
	global_store_dwordx4 v[160:161], v[0:3], off offset:3072 nt
	global_load_dwordx4 v[0:3], v[128:129], off
	s_nop 0
	global_load_dwordx4 v[48:51], v[130:131], off
	global_load_dwordx4 v[60:63], v[132:133], off
	global_load_dwordx4 v[56:59], v[134:135], off
	global_load_dwordx4 v[44:47], v[136:137], off
	global_load_dwordx4 v[52:55], v[138:139], off
	global_load_dwordx4 v[40:43], v[140:141], off
	global_load_dwordx4 v[36:39], v[142:143], off
	global_load_dwordx4 v[28:31], v[144:145], off
	global_load_dwordx4 v[32:35], v[146:147], off
	global_load_dwordx4 v[24:27], v[148:149], off
	global_load_dwordx4 v[20:23], v[150:151], off
	global_load_dwordx4 v[4:7], v[152:153], off
	global_load_dwordx4 v[8:11], v[154:155], off
	global_load_dwordx4 v[16:19], v[156:157], off
	global_load_dwordx4 v[12:15], v[158:159], off
	s_mov_b64 vcc, vcc
	s_cbranch_vccz .LBB0_2019
	s_mov_b64 s[4:5], 0
	v_add_u32_e32 v160, s33, v162
	s_branch .LBB0_2142

.LBB0_2122:
	s_lshl_b32 s20, s58, 8
	s_or_b32 s20, s20, s50
	v_or_b32_e32 v0, s20, v0
	v_lshl_add_u32 v2, v0, 2, 0
	v_add_u32_e32 v10, 0x21000, v2
	ds_read_b128 v[2:5], v10
	ds_read_b128 v[6:9], v10 offset:16
	ds_read_b128 v[20:23], v10 offset:32
	ds_read_b128 v[24:27], v10 offset:48
	v_or_b32_e32 v18, s46, v1
	v_ashrrev_i32_e32 v1, 31, v0
	s_waitcnt lgkmcnt(0)
	v_pk_mul_f32 v[12:13], v[6:7], s[8:9] op_sel_hi:[1,0]
	v_pk_mul_f32 v[16:17], v[2:3], s[8:9] op_sel_hi:[1,0]
	v_pk_mul_f32 v[14:15], v[4:5], s[8:9] op_sel_hi:[1,0]
	v_pk_mul_f32 v[10:11], v[8:9], s[8:9] op_sel_hi:[1,0]
	v_pk_mul_f32 v[8:9], v[20:21], s[8:9] op_sel_hi:[1,0]
	v_pk_mul_f32 v[6:7], v[22:23], s[8:9] op_sel_hi:[1,0]
	v_pk_mul_f32 v[4:5], v[24:25], s[8:9] op_sel_hi:[1,0]
	v_pk_mul_f32 v[2:3], v[26:27], s[8:9] op_sel_hi:[1,0]
	v_cmp_gt_i32_e32 vcc, s56, v18
	s_and_saveexec_b64 s[20:21], vcc
	s_cbranch_execz .LBB0_2124
	v_pk_fma_f32 v[20:21], v[148:149], s[10:11], v[16:17] op_sel_hi:[1,0,1]
	v_pk_fma_f32 v[22:23], v[150:151], s[10:11], v[14:15] op_sel_hi:[1,0,1]
	v_med3_f32 v19, v20, s54, v170
	v_med3_f32 v21, v21, s54, v170
	v_mov_b32_e32 v20, 0
	v_cvt_pk_fp8_f32 v20, v19, v21
	v_med3_f32 v19, v22, s54, v170
	v_med3_f32 v21, v23, s54, v170
	v_pk_fma_f32 v[22:23], v[144:145], s[10:11], v[12:13] op_sel_hi:[1,0,1]
	v_cvt_pk_fp8_f32 v20, v19, v21 op_sel:[0,0,1]
	v_med3_f32 v19, v22, s54, v170
	v_med3_f32 v22, v23, s54, v170
	v_mov_b32_e32 v21, 0
	v_cvt_pk_fp8_f32 v21, v19, v22
	v_pk_fma_f32 v[22:23], v[146:147], s[10:11], v[10:11] op_sel_hi:[1,0,1]
	v_pk_fma_f32 v[24:25], v[158:159], s[10:11], v[6:7] op_sel_hi:[1,0,1]
	v_med3_f32 v19, v22, s54, v170
	v_med3_f32 v22, v23, s54, v170
	v_cvt_pk_fp8_f32 v21, v19, v22 op_sel:[0,0,1]
	v_pk_fma_f32 v[22:23], v[156:157], s[10:11], v[8:9] op_sel_hi:[1,0,1]
	s_nop 0
	v_med3_f32 v19, v22, s54, v170
	v_med3_f32 v23, v23, s54, v170
	v_mov_b32_e32 v22, 0
	v_cvt_pk_fp8_f32 v22, v19, v23
	v_med3_f32 v19, v24, s54, v170
	v_med3_f32 v23, v25, s54, v170
	v_pk_fma_f32 v[24:25], v[152:153], s[10:11], v[4:5] op_sel_hi:[1,0,1]
	v_cvt_pk_fp8_f32 v22, v19, v23 op_sel:[0,0,1]
	v_med3_f32 v19, v24, s54, v170
	v_med3_f32 v24, v25, s54, v170
	v_mov_b32_e32 v23, 0
	v_cvt_pk_fp8_f32 v23, v19, v24
	v_pk_fma_f32 v[24:25], v[154:155], s[10:11], v[2:3] op_sel_hi:[1,0,1]
	s_nop 0
	v_med3_f32 v19, v24, s54, v170
	v_med3_f32 v24, v25, s54, v170
	v_cvt_pk_fp8_f32 v23, v19, v24 op_sel:[0,0,1]
	v_add_u32_e32 v24, s55, v18
	v_ashrrev_i32_e32 v25, 31, v24
	v_lshlrev_b64 v[24:25], 10, v[24:25]
	v_lshl_add_u64 v[24:25], s[4:5], 0, v[24:25]
	v_lshl_add_u64 v[24:25], v[24:25], 0, v[0:1]
	global_store_dwordx4 v[24:25], v[20:23], off nt
.LBB0_2124:
	s_or_b64 exec, exec, s[20:21]
	v_or_b32_e32 v19, 16, v18
	v_cmp_gt_i32_e32 vcc, s56, v19
	s_and_saveexec_b64 s[20:21], vcc
	s_cbranch_execz .LBB0_2126
	v_pk_fma_f32 v[20:21], v[136:137], s[10:11], v[16:17] op_sel_hi:[1,0,1]
	s_nop 0
	v_med3_f32 v22, v20, s54, v170
	v_med3_f32 v21, v21, s54, v170
	v_mov_b32_e32 v20, 0
	v_cvt_pk_fp8_f32 v20, v22, v21
	v_pk_fma_f32 v[22:23], v[138:139], s[10:11], v[14:15] op_sel_hi:[1,0,1]
	s_nop 0
	v_med3_f32 v21, v22, s54, v170
	v_med3_f32 v22, v23, s54, v170
	v_cvt_pk_fp8_f32 v20, v21, v22 op_sel:[0,0,1]
	v_pk_fma_f32 v[22:23], v[128:129], s[10:11], v[12:13] op_sel_hi:[1,0,1]
	v_mov_b32_e32 v21, 0
	v_med3_f32 v22, v22, s54, v170
	v_med3_f32 v23, v23, s54, v170
	v_cvt_pk_fp8_f32 v21, v22, v23
	v_pk_fma_f32 v[22:23], v[130:131], s[10:11], v[10:11] op_sel_hi:[1,0,1]
	s_nop 0
	v_med3_f32 v22, v22, s54, v170
	v_med3_f32 v23, v23, s54, v170
	v_cvt_pk_fp8_f32 v21, v22, v23 op_sel:[0,0,1]
	v_pk_fma_f32 v[22:23], v[140:141], s[10:11], v[8:9] op_sel_hi:[1,0,1]
	s_nop 0
	v_med3_f32 v24, v22, s54, v170
	v_med3_f32 v23, v23, s54, v170
	v_mov_b32_e32 v22, 0
	v_cvt_pk_fp8_f32 v22, v24, v23
	v_pk_fma_f32 v[24:25], v[142:143], s[10:11], v[6:7] op_sel_hi:[1,0,1]
	s_nop 0
	v_med3_f32 v23, v24, s54, v170
	v_med3_f32 v24, v25, s54, v170
	v_cvt_pk_fp8_f32 v22, v23, v24 op_sel:[0,0,1]
	v_pk_fma_f32 v[24:25], v[132:133], s[10:11], v[4:5] op_sel_hi:[1,0,1]
	v_mov_b32_e32 v23, 0
	v_med3_f32 v24, v24, s54, v170
	v_med3_f32 v25, v25, s54, v170
	v_cvt_pk_fp8_f32 v23, v24, v25
	v_pk_fma_f32 v[24:25], v[134:135], s[10:11], v[2:3] op_sel_hi:[1,0,1]
	s_nop 0
	v_med3_f32 v24, v24, s54, v170
	v_med3_f32 v25, v25, s54, v170
	v_cvt_pk_fp8_f32 v23, v24, v25 op_sel:[0,0,1]
	v_add_u32_e32 v24, s55, v19
	v_ashrrev_i32_e32 v25, 31, v24
	v_lshlrev_b64 v[24:25], 10, v[24:25]
	v_lshl_add_u64 v[24:25], s[4:5], 0, v[24:25]
	v_lshl_add_u64 v[24:25], v[24:25], 0, v[0:1]
	global_store_dwordx4 v[24:25], v[20:23], off nt
.LBB0_2126:
	s_or_b64 exec, exec, s[20:21]
	v_or_b32_e32 v19, 32, v18
	v_cmp_gt_i32_e32 vcc, s56, v19
	s_and_saveexec_b64 s[20:21], vcc
	s_cbranch_execz .LBB0_2128
	v_pk_fma_f32 v[20:21], v[120:121], s[10:11], v[16:17] op_sel_hi:[1,0,1]
	s_nop 0
	v_med3_f32 v22, v20, s54, v170
	v_med3_f32 v21, v21, s54, v170
	v_mov_b32_e32 v20, 0
	v_cvt_pk_fp8_f32 v20, v22, v21
	v_pk_fma_f32 v[22:23], v[122:123], s[10:11], v[14:15] op_sel_hi:[1,0,1]
	s_nop 0
	v_med3_f32 v21, v22, s54, v170
	v_med3_f32 v22, v23, s54, v170
	v_cvt_pk_fp8_f32 v20, v21, v22 op_sel:[0,0,1]
	v_pk_fma_f32 v[22:23], v[112:113], s[10:11], v[12:13] op_sel_hi:[1,0,1]
	v_mov_b32_e32 v21, 0
	v_med3_f32 v22, v22, s54, v170
	v_med3_f32 v23, v23, s54, v170
	v_cvt_pk_fp8_f32 v21, v22, v23
	v_pk_fma_f32 v[22:23], v[114:115], s[10:11], v[10:11] op_sel_hi:[1,0,1]
	s_nop 0
	v_med3_f32 v22, v22, s54, v170
	v_med3_f32 v23, v23, s54, v170
	v_cvt_pk_fp8_f32 v21, v22, v23 op_sel:[0,0,1]
	v_pk_fma_f32 v[22:23], v[124:125], s[10:11], v[8:9] op_sel_hi:[1,0,1]
	s_nop 0
	v_med3_f32 v24, v22, s54, v170
	v_med3_f32 v23, v23, s54, v170
	v_mov_b32_e32 v22, 0
	v_cvt_pk_fp8_f32 v22, v24, v23
	v_pk_fma_f32 v[24:25], v[126:127], s[10:11], v[6:7] op_sel_hi:[1,0,1]
	s_nop 0
	v_med3_f32 v23, v24, s54, v170
	v_med3_f32 v24, v25, s54, v170
	v_cvt_pk_fp8_f32 v22, v23, v24 op_sel:[0,0,1]
	v_pk_fma_f32 v[24:25], v[116:117], s[10:11], v[4:5] op_sel_hi:[1,0,1]
	v_mov_b32_e32 v23, 0
	v_med3_f32 v24, v24, s54, v170
	v_med3_f32 v25, v25, s54, v170
	v_cvt_pk_fp8_f32 v23, v24, v25
	v_pk_fma_f32 v[24:25], v[118:119], s[10:11], v[2:3] op_sel_hi:[1,0,1]
	s_nop 0
	v_med3_f32 v24, v24, s54, v170
	v_med3_f32 v25, v25, s54, v170
	v_cvt_pk_fp8_f32 v23, v24, v25 op_sel:[0,0,1]
	v_add_u32_e32 v24, s55, v19
	v_ashrrev_i32_e32 v25, 31, v24
	v_lshlrev_b64 v[24:25], 10, v[24:25]
	v_lshl_add_u64 v[24:25], s[4:5], 0, v[24:25]
	v_lshl_add_u64 v[24:25], v[24:25], 0, v[0:1]
	global_store_dwordx4 v[24:25], v[20:23], off nt
.LBB0_2128:
	s_or_b64 exec, exec, s[20:21]
	v_or_b32_e32 v19, 48, v18
	v_cmp_gt_i32_e32 vcc, s56, v19
	s_and_saveexec_b64 s[20:21], vcc
	s_cbranch_execz .LBB0_2130
	v_pk_fma_f32 v[20:21], v[108:109], s[10:11], v[16:17] op_sel_hi:[1,0,1]
	s_nop 0
	v_med3_f32 v22, v20, s54, v170
	v_med3_f32 v21, v21, s54, v170
	v_mov_b32_e32 v20, 0
	v_cvt_pk_fp8_f32 v20, v22, v21
	v_pk_fma_f32 v[22:23], v[110:111], s[10:11], v[14:15] op_sel_hi:[1,0,1]
	s_nop 0
	v_med3_f32 v21, v22, s54, v170
	v_med3_f32 v22, v23, s54, v170
	v_cvt_pk_fp8_f32 v20, v21, v22 op_sel:[0,0,1]
	v_pk_fma_f32 v[22:23], v[92:93], s[10:11], v[12:13] op_sel_hi:[1,0,1]
	v_mov_b32_e32 v21, 0
	v_med3_f32 v22, v22, s54, v170
	v_med3_f32 v23, v23, s54, v170
	v_cvt_pk_fp8_f32 v21, v22, v23
	v_pk_fma_f32 v[22:23], v[94:95], s[10:11], v[10:11] op_sel_hi:[1,0,1]
	s_nop 0
	v_med3_f32 v22, v22, s54, v170
	v_med3_f32 v23, v23, s54, v170
	v_cvt_pk_fp8_f32 v21, v22, v23 op_sel:[0,0,1]
	v_pk_fma_f32 v[22:23], v[96:97], s[10:11], v[8:9] op_sel_hi:[1,0,1]
	s_nop 0
	v_med3_f32 v24, v22, s54, v170
	v_med3_f32 v23, v23, s54, v170
	v_mov_b32_e32 v22, 0
	v_cvt_pk_fp8_f32 v22, v24, v23
	v_pk_fma_f32 v[24:25], v[98:99], s[10:11], v[6:7] op_sel_hi:[1,0,1]
	s_nop 0
	v_med3_f32 v23, v24, s54, v170
	v_med3_f32 v24, v25, s54, v170
	v_cvt_pk_fp8_f32 v22, v23, v24 op_sel:[0,0,1]
	v_pk_fma_f32 v[24:25], v[80:81], s[10:11], v[4:5] op_sel_hi:[1,0,1]
	v_mov_b32_e32 v23, 0
	v_med3_f32 v24, v24, s54, v170
	v_med3_f32 v25, v25, s54, v170
	v_cvt_pk_fp8_f32 v23, v24, v25
	v_pk_fma_f32 v[24:25], v[82:83], s[10:11], v[2:3] op_sel_hi:[1,0,1]
	s_nop 0
	v_med3_f32 v24, v24, s54, v170
	v_med3_f32 v25, v25, s54, v170
	v_cvt_pk_fp8_f32 v23, v24, v25 op_sel:[0,0,1]
	v_add_u32_e32 v24, s55, v19
	v_ashrrev_i32_e32 v25, 31, v24
	v_lshlrev_b64 v[24:25], 10, v[24:25]
	v_lshl_add_u64 v[24:25], s[4:5], 0, v[24:25]
	v_lshl_add_u64 v[24:25], v[24:25], 0, v[0:1]
	global_store_dwordx4 v[24:25], v[20:23], off nt
.LBB0_2130:
	s_or_b64 exec, exec, s[20:21]
	v_add_u32_e32 v19, 0x80, v18
	v_cmp_gt_i32_e32 vcc, s56, v19
	s_and_saveexec_b64 s[20:21], vcc
	s_cbranch_execz .LBB0_2132
	v_pk_fma_f32 v[20:21], v[100:101], s[10:11], v[16:17] op_sel_hi:[1,0,1]
	s_nop 0
	v_med3_f32 v22, v20, s54, v170
	v_med3_f32 v21, v21, s54, v170
	v_mov_b32_e32 v20, 0
	v_cvt_pk_fp8_f32 v20, v22, v21
	v_pk_fma_f32 v[22:23], v[102:103], s[10:11], v[14:15] op_sel_hi:[1,0,1]
	s_nop 0
	v_med3_f32 v21, v22, s54, v170
	v_med3_f32 v22, v23, s54, v170
	v_cvt_pk_fp8_f32 v20, v21, v22 op_sel:[0,0,1]
	v_pk_fma_f32 v[22:23], v[84:85], s[10:11], v[12:13] op_sel_hi:[1,0,1]
	v_mov_b32_e32 v21, 0
	v_med3_f32 v22, v22, s54, v170
	v_med3_f32 v23, v23, s54, v170
	v_cvt_pk_fp8_f32 v21, v22, v23
	v_pk_fma_f32 v[22:23], v[86:87], s[10:11], v[10:11] op_sel_hi:[1,0,1]
	s_nop 0
	v_med3_f32 v22, v22, s54, v170
	v_med3_f32 v23, v23, s54, v170
	v_cvt_pk_fp8_f32 v21, v22, v23 op_sel:[0,0,1]
	v_pk_fma_f32 v[22:23], v[104:105], s[10:11], v[8:9] op_sel_hi:[1,0,1]
	s_nop 0
	v_med3_f32 v24, v22, s54, v170
	v_med3_f32 v23, v23, s54, v170
	v_mov_b32_e32 v22, 0
	v_cvt_pk_fp8_f32 v22, v24, v23
	v_pk_fma_f32 v[24:25], v[106:107], s[10:11], v[6:7] op_sel_hi:[1,0,1]
	s_nop 0
	v_med3_f32 v23, v24, s54, v170
	v_med3_f32 v24, v25, s54, v170
	v_cvt_pk_fp8_f32 v22, v23, v24 op_sel:[0,0,1]
	v_pk_fma_f32 v[24:25], v[88:89], s[10:11], v[4:5] op_sel_hi:[1,0,1]
	v_mov_b32_e32 v23, 0
	v_med3_f32 v24, v24, s54, v170
	v_med3_f32 v25, v25, s54, v170
	v_cvt_pk_fp8_f32 v23, v24, v25
	v_pk_fma_f32 v[24:25], v[90:91], s[10:11], v[2:3] op_sel_hi:[1,0,1]
	s_nop 0
	v_med3_f32 v24, v24, s54, v170
	v_med3_f32 v25, v25, s54, v170
	v_cvt_pk_fp8_f32 v23, v24, v25 op_sel:[0,0,1]
	v_add_u32_e32 v24, s55, v19
	v_ashrrev_i32_e32 v25, 31, v24
	v_lshlrev_b64 v[24:25], 10, v[24:25]
	v_lshl_add_u64 v[24:25], s[4:5], 0, v[24:25]
	v_lshl_add_u64 v[24:25], v[24:25], 0, v[0:1]
	global_store_dwordx4 v[24:25], v[20:23], off nt
.LBB0_2132:
	s_or_b64 exec, exec, s[20:21]
	v_add_u32_e32 v19, 0x90, v18
	v_cmp_gt_i32_e32 vcc, s56, v19
	s_and_saveexec_b64 s[20:21], vcc
	s_cbranch_execz .LBB0_2134
	v_pk_fma_f32 v[20:21], v[76:77], s[10:11], v[16:17] op_sel_hi:[1,0,1]
	s_nop 0
	v_med3_f32 v22, v20, s54, v170
	v_med3_f32 v21, v21, s54, v170
	v_mov_b32_e32 v20, 0
	v_cvt_pk_fp8_f32 v20, v22, v21
	v_pk_fma_f32 v[22:23], v[78:79], s[10:11], v[14:15] op_sel_hi:[1,0,1]
	s_nop 0
	v_med3_f32 v21, v22, s54, v170
	v_med3_f32 v22, v23, s54, v170
	v_cvt_pk_fp8_f32 v20, v21, v22 op_sel:[0,0,1]
	v_pk_fma_f32 v[22:23], v[68:69], s[10:11], v[12:13] op_sel_hi:[1,0,1]
	v_mov_b32_e32 v21, 0
	v_med3_f32 v22, v22, s54, v170
	v_med3_f32 v23, v23, s54, v170
	v_cvt_pk_fp8_f32 v21, v22, v23
	v_pk_fma_f32 v[22:23], v[70:71], s[10:11], v[10:11] op_sel_hi:[1,0,1]
	s_nop 0
	v_med3_f32 v22, v22, s54, v170
	v_med3_f32 v23, v23, s54, v170
	v_cvt_pk_fp8_f32 v21, v22, v23 op_sel:[0,0,1]
	v_pk_fma_f32 v[22:23], v[72:73], s[10:11], v[8:9] op_sel_hi:[1,0,1]
	s_nop 0
	v_med3_f32 v24, v22, s54, v170
	v_med3_f32 v23, v23, s54, v170
	v_mov_b32_e32 v22, 0
	v_cvt_pk_fp8_f32 v22, v24, v23
	v_pk_fma_f32 v[24:25], v[74:75], s[10:11], v[6:7] op_sel_hi:[1,0,1]
	s_nop 0
	v_med3_f32 v23, v24, s54, v170
	v_med3_f32 v24, v25, s54, v170
	v_cvt_pk_fp8_f32 v22, v23, v24 op_sel:[0,0,1]
	v_pk_fma_f32 v[24:25], v[64:65], s[10:11], v[4:5] op_sel_hi:[1,0,1]
	v_mov_b32_e32 v23, 0
	v_med3_f32 v24, v24, s54, v170
	v_med3_f32 v25, v25, s54, v170
	v_cvt_pk_fp8_f32 v23, v24, v25
	v_pk_fma_f32 v[24:25], v[66:67], s[10:11], v[2:3] op_sel_hi:[1,0,1]
	s_nop 0
	v_med3_f32 v24, v24, s54, v170
	v_med3_f32 v25, v25, s54, v170
	v_cvt_pk_fp8_f32 v23, v24, v25 op_sel:[0,0,1]
	v_add_u32_e32 v24, s55, v19
	v_ashrrev_i32_e32 v25, 31, v24
	v_lshlrev_b64 v[24:25], 10, v[24:25]
	v_lshl_add_u64 v[24:25], s[4:5], 0, v[24:25]
	v_lshl_add_u64 v[24:25], v[24:25], 0, v[0:1]
	global_store_dwordx4 v[24:25], v[20:23], off nt
.LBB0_2134:
	s_or_b64 exec, exec, s[20:21]
	v_add_u32_e32 v19, 0xa0, v18
	v_cmp_gt_i32_e32 vcc, s56, v19
	s_and_saveexec_b64 s[20:21], vcc
	s_cbranch_execz .LBB0_2136
	v_pk_fma_f32 v[20:21], v[60:61], s[10:11], v[16:17] op_sel_hi:[1,0,1]
	s_nop 0
	v_med3_f32 v22, v20, s54, v170
	v_med3_f32 v21, v21, s54, v170
	v_mov_b32_e32 v20, 0
	v_cvt_pk_fp8_f32 v20, v22, v21
	v_pk_fma_f32 v[22:23], v[62:63], s[10:11], v[14:15] op_sel_hi:[1,0,1]
	s_nop 0
	v_med3_f32 v21, v22, s54, v170
	v_med3_f32 v22, v23, s54, v170
	v_cvt_pk_fp8_f32 v20, v21, v22 op_sel:[0,0,1]
	v_pk_fma_f32 v[22:23], v[52:53], s[10:11], v[12:13] op_sel_hi:[1,0,1]
	v_mov_b32_e32 v21, 0
	v_med3_f32 v22, v22, s54, v170
	v_med3_f32 v23, v23, s54, v170
	v_cvt_pk_fp8_f32 v21, v22, v23
	v_pk_fma_f32 v[22:23], v[54:55], s[10:11], v[10:11] op_sel_hi:[1,0,1]
	s_nop 0
	v_med3_f32 v22, v22, s54, v170
	v_med3_f32 v23, v23, s54, v170
	v_cvt_pk_fp8_f32 v21, v22, v23 op_sel:[0,0,1]
	v_pk_fma_f32 v[22:23], v[56:57], s[10:11], v[8:9] op_sel_hi:[1,0,1]
	s_nop 0
	v_med3_f32 v24, v22, s54, v170
	v_med3_f32 v23, v23, s54, v170
	v_mov_b32_e32 v22, 0
	v_cvt_pk_fp8_f32 v22, v24, v23
	v_pk_fma_f32 v[24:25], v[58:59], s[10:11], v[6:7] op_sel_hi:[1,0,1]
	s_nop 0
	v_med3_f32 v23, v24, s54, v170
	v_med3_f32 v24, v25, s54, v170
	v_cvt_pk_fp8_f32 v22, v23, v24 op_sel:[0,0,1]
	v_pk_fma_f32 v[24:25], v[48:49], s[10:11], v[4:5] op_sel_hi:[1,0,1]
	v_mov_b32_e32 v23, 0
	v_med3_f32 v24, v24, s54, v170
	v_med3_f32 v25, v25, s54, v170
	v_cvt_pk_fp8_f32 v23, v24, v25
	v_pk_fma_f32 v[24:25], v[50:51], s[10:11], v[2:3] op_sel_hi:[1,0,1]
	s_nop 0
	v_med3_f32 v24, v24, s54, v170
	v_med3_f32 v25, v25, s54, v170
	v_cvt_pk_fp8_f32 v23, v24, v25 op_sel:[0,0,1]
	v_add_u32_e32 v24, s55, v19
	v_ashrrev_i32_e32 v25, 31, v24
	v_lshlrev_b64 v[24:25], 10, v[24:25]
	v_lshl_add_u64 v[24:25], s[4:5], 0, v[24:25]
	v_lshl_add_u64 v[24:25], v[24:25], 0, v[0:1]
	global_store_dwordx4 v[24:25], v[20:23], off nt
.LBB0_2136:
	s_or_b64 exec, exec, s[20:21]
	v_add_u32_e32 v18, 0xb0, v18
	v_cmp_gt_i32_e32 vcc, s56, v18
	s_and_saveexec_b64 s[20:21], vcc
	s_cbranch_execz .LBB0_2138
	v_pk_fma_f32 v[4:5], v[32:33], s[10:11], v[4:5] op_sel_hi:[1,0,1]
	v_pk_fma_f32 v[16:17], v[44:45], s[10:11], v[16:17] op_sel_hi:[1,0,1]
	v_pk_fma_f32 v[12:13], v[40:41], s[10:11], v[12:13] op_sel_hi:[1,0,1]
	v_pk_fma_f32 v[8:9], v[36:37], s[10:11], v[8:9] op_sel_hi:[1,0,1]
	v_med3_f32 v4, v4, s54, v170
	v_med3_f32 v5, v5, s54, v170
	v_mov_b32_e32 v23, 0
	v_med3_f32 v16, v16, s54, v170
	v_med3_f32 v17, v17, s54, v170
	v_mov_b32_e32 v20, 0
	v_med3_f32 v12, v12, s54, v170
	v_med3_f32 v13, v13, s54, v170
	v_mov_b32_e32 v21, 0
	v_med3_f32 v8, v8, s54, v170
	v_med3_f32 v9, v9, s54, v170
	v_mov_b32_e32 v22, 0
	v_cvt_pk_fp8_f32 v23, v4, v5
	v_cvt_pk_fp8_f32 v20, v16, v17
	v_cvt_pk_fp8_f32 v21, v12, v13
	v_cvt_pk_fp8_f32 v22, v8, v9
	v_pk_fma_f32 v[2:3], v[34:35], s[10:11], v[2:3] op_sel_hi:[1,0,1]
	v_pk_fma_f32 v[14:15], v[46:47], s[10:11], v[14:15] op_sel_hi:[1,0,1]
	v_pk_fma_f32 v[10:11], v[42:43], s[10:11], v[10:11] op_sel_hi:[1,0,1]
	v_pk_fma_f32 v[6:7], v[38:39], s[10:11], v[6:7] op_sel_hi:[1,0,1]
	v_med3_f32 v2, v2, s54, v170
	v_med3_f32 v3, v3, s54, v170
	v_med3_f32 v14, v14, s54, v170
	v_med3_f32 v15, v15, s54, v170
	v_med3_f32 v10, v10, s54, v170
	v_med3_f32 v11, v11, s54, v170
	v_med3_f32 v6, v6, s54, v170
	v_med3_f32 v7, v7, s54, v170
	v_cvt_pk_fp8_f32 v23, v2, v3 op_sel:[0,0,1]
	v_add_u32_e32 v2, s55, v18
	v_cvt_pk_fp8_f32 v20, v14, v15 op_sel:[0,0,1]
	v_cvt_pk_fp8_f32 v21, v10, v11 op_sel:[0,0,1]
	v_cvt_pk_fp8_f32 v22, v6, v7 op_sel:[0,0,1]
	v_ashrrev_i32_e32 v3, 31, v2
	v_lshlrev_b64 v[2:3], 10, v[2:3]
	v_lshl_add_u64 v[2:3], s[4:5], 0, v[2:3]
	v_lshl_add_u64 v[0:1], v[2:3], 0, v[0:1]
	global_store_dwordx4 v[0:1], v[20:23], off nt
